# speedup vs baseline: 1.0030x; 1.0030x over previous
.LE_cgot3:
	v_xor_b32_e32 v200, 32, v200
	v_xor_b32_e32 v201, 32, v201
	v_xor_b32_e32 v202, 32, v202
	v_xor_b32_e32 v203, 32, v203
	v_xor_b32_e32 v204, 32, v204
	v_xor_b32_e32 v205, 32, v205
	v_xor_b32_e32 v206, 32, v206
	v_xor_b32_e32 v207, 32, v207
	v_or_b32_e32 v200, v200, v201
	v_or_b32_e32 v202, v202, v203
	v_or_b32_e32 v204, v204, v205
	v_or_b32_e32 v206, v206, v207
	v_or_b32_e32 v200, v200, v202
	v_or_b32_e32 v204, v204, v206
	v_or_b32_e32 v200, v200, v204
	s_nop 1
	v_readfirstlane_b32 s67, v200
	v_readfirstlane_b32 s68, v250
	s_nop 1
	s_and_b32 s69, s2, 7
	s_lshr_b32 s70, s2, 3
	s_cmp_eq_u32 s67, 0
	s_cselect_b32 s31, 1, 0
	s_cselect_b32 s29, s64, s69
	s_cselect_b32 s30, s68, s70
	v_mov_b32_e32 v200, s31
	v_mov_b32_e32 v201, s29
	v_mov_b32_e32 v202, s30
	v_mov_b32_e32 v252, 0x20800
	ds_write_b32 v252, v200
	ds_write_b32 v252, v201 offset:4
	ds_write_b32 v252, v202 offset:8
	s_mov_b64 exec, -1
.LE_cdone1:
	s_waitcnt lgkmcnt(0)
	s_barrier
	v_mov_b32_e32 v252, 0x20800
	ds_read_b32 v200, v252
	ds_read_b32 v201, v252 offset:4
	ds_read_b32 v202, v252 offset:8
	s_waitcnt lgkmcnt(0)
	s_nop 1
	v_readfirstlane_b32 s31, v200
	v_readfirstlane_b32 s29, v201
	v_readfirstlane_b32 s30, v202
	s_nop 3
	s_barrier
	s_lshl_b32 s49, s29, 19
	s_lshl_b32 s64, s32, 13
	s_add_u32 s49, s49, s64
	s_mov_b32 s51, s64
	s_add_u32 s52, s51, 0x0
	s_add_u32 s53, s51, 0x1000
	s_add_u32 s54, s51, 0x8000
	s_add_u32 s55, s51, 0x9000
	s_add_u32 s56, s51, 0x10000
	s_add_u32 s57, s51, 0x11000
	s_add_u32 s58, s51, 0x18000
	s_add_u32 s59, s51, 0x19000
	s_lshl_b32 s64, s29, 8
	s_lshl_b32 s65, s30, 1
	s_add_u32 s64, s64, s65
	s_lshr_b32 s65, s32, 1
	s_add_u32 s64, s64, s65
	s_lshl_b32 s64, s64, 11
	s_and_b32 s65, s32, 1
	s_lshl_b32 s65, s65, 9
	s_add_u32 s50, s64, s65
	s_sub_u32 s60, s28, 1
	s_lshl_b32 s64, s30, 2
	s_add_u32 s64, s64, s32
	s_lshl_b32 s64, s64, 16
	s_add_u32 s44, s4, s64
	s_addc_u32 s45, s5, 0
	global_load_dwordx4 a[0:3], v192, s[44:45] offset:0
	global_load_dwordx4 a[4:7], v192, s[44:45] offset:1024
	global_load_dwordx4 a[8:11], v192, s[44:45] offset:2048
	global_load_dwordx4 a[12:15], v192, s[44:45] offset:3072
	s_add_u32 s44, s44, 0x1000
	s_addc_u32 s45, s45, 0
	global_load_dwordx4 a[16:19], v192, s[44:45] offset:0
	global_load_dwordx4 a[20:23], v192, s[44:45] offset:1024
	global_load_dwordx4 a[24:27], v192, s[44:45] offset:2048
	global_load_dwordx4 a[28:31], v192, s[44:45] offset:3072
	s_add_u32 s44, s44, 0x1000
	s_addc_u32 s45, s45, 0
	global_load_dwordx4 a[32:35], v192, s[44:45] offset:0
	global_load_dwordx4 a[36:39], v192, s[44:45] offset:1024
	global_load_dwordx4 a[40:43], v192, s[44:45] offset:2048
	global_load_dwordx4 a[44:47], v192, s[44:45] offset:3072
	s_add_u32 s44, s44, 0x1000
	s_addc_u32 s45, s45, 0
	global_load_dwordx4 a[48:51], v192, s[44:45] offset:0
	global_load_dwordx4 a[52:55], v192, s[44:45] offset:1024
	global_load_dwordx4 a[56:59], v192, s[44:45] offset:2048
	global_load_dwordx4 a[60:63], v192, s[44:45] offset:3072
	s_add_u32 s44, s44, 0x1000
	s_addc_u32 s45, s45, 0
	global_load_dwordx4 a[64:67], v192, s[44:45] offset:0
	global_load_dwordx4 a[68:71], v192, s[44:45] offset:1024
	global_load_dwordx4 a[72:75], v192, s[44:45] offset:2048
	global_load_dwordx4 a[76:79], v192, s[44:45] offset:3072
	s_add_u32 s44, s44, 0x1000
	s_addc_u32 s45, s45, 0
	global_load_dwordx4 a[80:83], v192, s[44:45] offset:0
	global_load_dwordx4 a[84:87], v192, s[44:45] offset:1024
	global_load_dwordx4 a[88:91], v192, s[44:45] offset:2048
	global_load_dwordx4 a[92:95], v192, s[44:45] offset:3072
	s_add_u32 s44, s44, 0x1000
	s_addc_u32 s45, s45, 0
	global_load_dwordx4 a[96:99], v192, s[44:45] offset:0
	global_load_dwordx4 a[100:103], v192, s[44:45] offset:1024
	global_load_dwordx4 a[104:107], v192, s[44:45] offset:2048
	global_load_dwordx4 a[108:111], v192, s[44:45] offset:3072
	s_add_u32 s44, s44, 0x1000
	s_addc_u32 s45, s45, 0
	global_load_dwordx4 a[112:115], v192, s[44:45] offset:0
	global_load_dwordx4 a[116:119], v192, s[44:45] offset:1024
	global_load_dwordx4 a[120:123], v192, s[44:45] offset:2048
	global_load_dwordx4 a[124:127], v192, s[44:45] offset:3072
	s_add_u32 s44, s44, 0x1000
	s_addc_u32 s45, s45, 0
	s_waitcnt vmcnt(16)
	global_load_dwordx4 a[128:131], v192, s[44:45] offset:0
	global_load_dwordx4 a[132:135], v192, s[44:45] offset:1024
	global_load_dwordx4 a[136:139], v192, s[44:45] offset:2048
	global_load_dwordx4 a[140:143], v192, s[44:45] offset:3072
	s_add_u32 s44, s44, 0x1000
	s_addc_u32 s45, s45, 0
	global_load_dwordx4 a[144:147], v192, s[44:45] offset:0
	global_load_dwordx4 a[148:151], v192, s[44:45] offset:1024
	global_load_dwordx4 a[152:155], v192, s[44:45] offset:2048
	global_load_dwordx4 a[156:159], v192, s[44:45] offset:3072
	s_add_u32 s44, s44, 0x1000
	s_addc_u32 s45, s45, 0
	global_load_dwordx4 a[160:163], v192, s[44:45] offset:0
	global_load_dwordx4 a[164:167], v192, s[44:45] offset:1024
	global_load_dwordx4 a[168:171], v192, s[44:45] offset:2048
	global_load_dwordx4 a[172:175], v192, s[44:45] offset:3072
	s_add_u32 s44, s44, 0x1000
	s_addc_u32 s45, s45, 0
	global_load_dwordx4 a[176:179], v192, s[44:45] offset:0
	global_load_dwordx4 a[180:183], v192, s[44:45] offset:1024
	global_load_dwordx4 a[184:187], v192, s[44:45] offset:2048
	global_load_dwordx4 a[188:191], v192, s[44:45] offset:3072
	s_add_u32 s44, s44, 0x1000
	s_addc_u32 s45, s45, 0
	global_load_dwordx4 a[192:195], v192, s[44:45] offset:0
	global_load_dwordx4 a[196:199], v192, s[44:45] offset:1024
	global_load_dwordx4 a[200:203], v192, s[44:45] offset:2048
	global_load_dwordx4 a[204:207], v192, s[44:45] offset:3072
	s_add_u32 s44, s44, 0x1000
	s_addc_u32 s45, s45, 0
	global_load_dwordx4 a[208:211], v192, s[44:45] offset:0
	global_load_dwordx4 a[212:215], v192, s[44:45] offset:1024
	global_load_dwordx4 a[216:219], v192, s[44:45] offset:2048
	global_load_dwordx4 a[220:223], v192, s[44:45] offset:3072
	s_add_u32 s44, s44, 0x1000
	s_addc_u32 s45, s45, 0
	global_load_dwordx4 a[224:227], v192, s[44:45] offset:0
	global_load_dwordx4 a[228:231], v192, s[44:45] offset:1024
	global_load_dwordx4 a[232:235], v192, s[44:45] offset:2048
	global_load_dwordx4 a[236:239], v192, s[44:45] offset:3072
	s_add_u32 s44, s44, 0x1000
	s_addc_u32 s45, s45, 0
	global_load_dwordx4 a[240:243], v192, s[44:45] offset:0
	global_load_dwordx4 a[244:247], v192, s[44:45] offset:1024
	global_load_dwordx4 a[248:251], v192, s[44:45] offset:2048
	global_load_dwordx4 a[252:255], v192, s[44:45] offset:3072
	s_add_u32 s44, s44, 0x1000
	s_addc_u32 s45, s45, 0
	v_mov_b32_e32 v128, 0
	v_mov_b32_e32 v129, 0
	v_mov_b32_e32 v130, 0
	v_mov_b32_e32 v131, 0
	v_mov_b32_e32 v132, 0
	v_mov_b32_e32 v133, 0
	v_mov_b32_e32 v134, 0
	v_mov_b32_e32 v135, 0
	v_mov_b32_e32 v136, 0
	v_mov_b32_e32 v137, 0
	v_mov_b32_e32 v138, 0
	v_mov_b32_e32 v139, 0
	v_mov_b32_e32 v140, 0
	v_mov_b32_e32 v141, 0
	v_mov_b32_e32 v142, 0
	v_mov_b32_e32 v143, 0
	v_mov_b32_e32 v144, 0
	v_mov_b32_e32 v145, 0
	v_mov_b32_e32 v146, 0
	v_mov_b32_e32 v147, 0
	v_mov_b32_e32 v148, 0
	v_mov_b32_e32 v149, 0
	v_mov_b32_e32 v150, 0
	v_mov_b32_e32 v151, 0
	v_mov_b32_e32 v152, 0
	v_mov_b32_e32 v153, 0
	v_mov_b32_e32 v154, 0
	v_mov_b32_e32 v155, 0
	v_mov_b32_e32 v156, 0
	v_mov_b32_e32 v157, 0
	v_mov_b32_e32 v158, 0
	v_mov_b32_e32 v159, 0
	s_lshl_b32 s64, s30, 5
	s_lshl_b32 s65, s32, 3
	s_add_u32 s64, s64, s65
	v_lshlrev_b32_e32 v255, 2, v254
	v_add_u32_e32 v255, s64, v255
	v_lshl_add_u32 v248, s32, 1, v254
	v_mul_u32_u24_e32 v248, 192, v248
	v_add_u32_e32 v248, 0x20000, v248
	v_lshlrev_b32_e32 v249, 3, v253
	v_lshlrev_b32_e32 v250, 12, v253
	v_lshl_add_u32 v250, v254, 4, v250
	v_lshlrev_b32_e32 v200, 3, v255
	v_lshlrev_b32_e32 v201, 2, v255
	v_add_u32_e32 v202, 0x0, v200
	v_add_u32_e32 v203, 0x0, v201
	global_load_dwordx4 v[204:207], v202, s[14:15]
	global_load_dwordx4 v[208:211], v202, s[14:15] offset:16
	global_load_dwordx4 v[212:215], v203, s[16:17]
	s_waitcnt vmcnt(0)
	s_mov_b32 s65, 0xbfb8aa3b
	v_mul_f32_e32 v204, s65, v204
	v_mul_f32_e32 v205, s65, v205
	v_mul_f32_e32 v206, s65, v206
	v_mul_f32_e32 v207, s65, v207
	v_mul_f32_e32 v208, s65, v208
	v_mul_f32_e32 v209, s65, v209
	v_mul_f32_e32 v210, s65, v210
	v_mul_f32_e32 v211, s65, v211
	v_mul_f32_e32 v212, s65, v212
	v_mul_f32_e32 v213, s65, v213
	v_mul_f32_e32 v214, s65, v214
	v_mul_f32_e32 v215, s65, v215
	ds_write_b128 v248, v[204:207] offset:0
	ds_write_b128 v248, v[208:211] offset:16
	ds_write_b128 v248, v[212:215] offset:32
	s_waitcnt lgkmcnt(0)
	v_add_u32_e32 v202, 0x2000, v200
	v_add_u32_e32 v203, 0x1000, v201
	global_load_dwordx4 v[204:207], v202, s[14:15]
	global_load_dwordx4 v[208:211], v202, s[14:15] offset:16
	global_load_dwordx4 v[212:215], v203, s[16:17]
	s_waitcnt vmcnt(0)
	s_mov_b32 s65, 0xbfb8aa3b
	v_mul_f32_e32 v204, s65, v204
	v_mul_f32_e32 v205, s65, v205
	v_mul_f32_e32 v206, s65, v206
	v_mul_f32_e32 v207, s65, v207
	v_mul_f32_e32 v208, s65, v208
	v_mul_f32_e32 v209, s65, v209
	v_mul_f32_e32 v210, s65, v210
	v_mul_f32_e32 v211, s65, v211
	v_mul_f32_e32 v212, s65, v212
	v_mul_f32_e32 v213, s65, v213
	v_mul_f32_e32 v214, s65, v214
	v_mul_f32_e32 v215, s65, v215
	ds_write_b128 v248, v[204:207] offset:48
	ds_write_b128 v248, v[208:211] offset:64
	ds_write_b128 v248, v[212:215] offset:80
	s_waitcnt lgkmcnt(0)
	v_add_u32_e32 v202, 0x4000, v200
	v_add_u32_e32 v203, 0x2000, v201
	global_load_dwordx4 v[204:207], v202, s[14:15]
	global_load_dwordx4 v[208:211], v202, s[14:15] offset:16
	global_load_dwordx4 v[212:215], v203, s[16:17]
	s_waitcnt vmcnt(0)
	s_mov_b32 s65, 0xc038aa3b
	v_mul_f32_e32 v204, s65, v204
	v_mul_f32_e32 v205, s65, v205
	v_mul_f32_e32 v206, s65, v206
	v_mul_f32_e32 v207, s65, v207
	v_mul_f32_e32 v208, s65, v208
	v_mul_f32_e32 v209, s65, v209
	v_mul_f32_e32 v210, s65, v210
	v_mul_f32_e32 v211, s65, v211
	v_mul_f32_e32 v212, s65, v212
	v_mul_f32_e32 v213, s65, v213
	v_mul_f32_e32 v214, s65, v214
	v_mul_f32_e32 v215, s65, v215
	ds_write_b128 v248, v[204:207] offset:96
	ds_write_b128 v248, v[208:211] offset:112
	ds_write_b128 v248, v[212:215] offset:128
	s_waitcnt lgkmcnt(0)
	v_add_u32_e32 v202, 0x6000, v200
	v_add_u32_e32 v203, 0x3000, v201
	global_load_dwordx4 v[204:207], v202, s[14:15]
	global_load_dwordx4 v[208:211], v202, s[14:15] offset:16
	global_load_dwordx4 v[212:215], v203, s[16:17]
	s_waitcnt vmcnt(0)
	s_mov_b32 s65, 0xbfb8aa3b
	v_mul_f32_e32 v204, s65, v204
	v_mul_f32_e32 v205, s65, v205
	v_mul_f32_e32 v206, s65, v206
	v_mul_f32_e32 v207, s65, v207
	v_mul_f32_e32 v208, s65, v208
	v_mul_f32_e32 v209, s65, v209
	v_mul_f32_e32 v210, s65, v210
	v_mul_f32_e32 v211, s65, v211
	v_mul_f32_e32 v212, s65, v212
	v_mul_f32_e32 v213, s65, v213
	v_mul_f32_e32 v214, s65, v214
	v_mul_f32_e32 v215, s65, v215
	ds_write_b128 v248, v[204:207] offset:144
	ds_write_b128 v248, v[208:211] offset:160
	ds_write_b128 v248, v[212:215] offset:176
	s_waitcnt lgkmcnt(0)
	s_lshl_b32 s65, s29, 20
	s_lshl_b32 s66, s64, 2
	s_add_u32 s65, s65, s66
	s_add_u32 s62, s26, s65
	s_addc_u32 s63, s27, 0
	s_waitcnt vmcnt(0)
	s_mov_b32 s33, 0
	s_lshl_b32 s64, s33, 11
	s_lshl_b32 s65, s29, 8
	s_add_u32 s64, s64, s65
	s_lshl_b32 s64, s64, 3
	s_add_u32 s42, s12, s64
	s_addc_u32 s43, s13, 0
	global_load_dwordx2 v[228:229], v249, s[42:43] offset:0
	global_load_dwordx2 v[230:231], v249, s[42:43] offset:256
	ds_read_b128 v[236:239], v248 offset:0
	ds_read_b128 v[240:243], v248 offset:16
	ds_read_b128 v[244:247], v248 offset:32
	ds_read_b128 v[200:203], v248 offset:48
	ds_read_b128 v[204:207], v248 offset:64
	ds_read_b128 v[208:211], v248 offset:80
	s_waitcnt lgkmcnt(3)
	s_waitcnt vmcnt(0)
	v_fma_f32 v0, v229, v237, v244
	v_fma_f32 v1, v229, v239, v245
	v_fma_f32 v2, v229, v241, v246
	v_fma_f32 v3, v229, v243, v247
	v_fmac_f32_e32 v0, v228, v236
	v_fmac_f32_e32 v1, v228, v238
	v_fmac_f32_e32 v2, v228, v240
	v_fmac_f32_e32 v3, v228, v242
	v_fma_f32 v16, v231, v237, v244
	v_fma_f32 v17, v231, v239, v245
	v_fma_f32 v18, v231, v241, v246
	v_fma_f32 v19, v231, v243, v247
	v_fmac_f32_e32 v16, v230, v236
	v_fmac_f32_e32 v17, v230, v238
	v_fmac_f32_e32 v18, v230, v240
	v_fmac_f32_e32 v19, v230, v242
	ds_read_b128 v[236:239], v248 offset:96
	ds_read_b128 v[240:243], v248 offset:112
	ds_read_b128 v[244:247], v248 offset:128
	s_waitcnt lgkmcnt(3)
	v_fma_f32 v4, v229, v201, v208
	v_fma_f32 v5, v229, v203, v209
	v_fma_f32 v6, v229, v205, v210
	v_fma_f32 v7, v229, v207, v211
	v_fmac_f32_e32 v4, v228, v200
	v_fmac_f32_e32 v5, v228, v202
	v_fmac_f32_e32 v6, v228, v204
	v_fmac_f32_e32 v7, v228, v206
	v_fma_f32 v20, v231, v201, v208
	v_fma_f32 v21, v231, v203, v209
	v_fma_f32 v22, v231, v205, v210
	v_fma_f32 v23, v231, v207, v211
	v_fmac_f32_e32 v20, v230, v200
	v_fmac_f32_e32 v21, v230, v202
	v_fmac_f32_e32 v22, v230, v204
	v_fmac_f32_e32 v23, v230, v206
	ds_read_b128 v[200:203], v248 offset:144
	ds_read_b128 v[204:207], v248 offset:160
	ds_read_b128 v[208:211], v248 offset:176
	s_waitcnt lgkmcnt(3)
	v_fma_f32 v8, v229, v237, v244
	v_fma_f32 v9, v229, v239, v245
	v_fma_f32 v10, v229, v241, v246
	v_fma_f32 v11, v229, v243, v247
	v_fmac_f32_e32 v8, v228, v236
	v_fmac_f32_e32 v9, v228, v238
	v_fmac_f32_e32 v10, v228, v240
	v_fmac_f32_e32 v11, v228, v242
	v_fma_f32 v24, v231, v237, v244
	v_fma_f32 v25, v231, v239, v245
	v_fma_f32 v26, v231, v241, v246
	v_fma_f32 v27, v231, v243, v247
	v_fmac_f32_e32 v24, v230, v236
	v_fmac_f32_e32 v25, v230, v238
	v_fmac_f32_e32 v26, v230, v240
	v_fmac_f32_e32 v27, v230, v242
	s_waitcnt lgkmcnt(0)
	v_fma_f32 v12, v229, v201, v208
	v_fma_f32 v13, v229, v203, v209
	v_fma_f32 v14, v229, v205, v210
	v_fma_f32 v15, v229, v207, v211
	v_fmac_f32_e32 v12, v228, v200
	v_fmac_f32_e32 v13, v228, v202
	v_fmac_f32_e32 v14, v228, v204
	v_fmac_f32_e32 v15, v228, v206
	v_fma_f32 v28, v231, v201, v208
	v_fma_f32 v29, v231, v203, v209
	v_fma_f32 v30, v231, v205, v210
	v_fma_f32 v31, v231, v207, v211
	v_fmac_f32_e32 v28, v230, v200
	v_fmac_f32_e32 v29, v230, v202
	v_fmac_f32_e32 v30, v230, v204
	v_fmac_f32_e32 v31, v230, v206
	s_lshl_b32 s64, s33, 11
	s_lshl_b32 s65, s29, 8
	s_add_u32 s64, s64, s65
	s_add_u32 s64, s64, 64
	s_lshl_b32 s64, s64, 3
	s_add_u32 s42, s12, s64
	s_addc_u32 s43, s13, 0
	global_load_dwordx2 v[228:229], v249, s[42:43] offset:0
	global_load_dwordx2 v[230:231], v249, s[42:43] offset:256
	ds_read_b128 v[236:239], v248 offset:0
	ds_read_b128 v[240:243], v248 offset:16
	ds_read_b128 v[244:247], v248 offset:32
	ds_read_b128 v[200:203], v248 offset:48
	ds_read_b128 v[204:207], v248 offset:64
	ds_read_b128 v[208:211], v248 offset:80
	s_waitcnt lgkmcnt(3)
	s_waitcnt vmcnt(0)
	v_fma_f32 v32, v229, v237, v244
	v_fma_f32 v33, v229, v239, v245
	v_fma_f32 v34, v229, v241, v246
	v_fma_f32 v35, v229, v243, v247
	v_fmac_f32_e32 v32, v228, v236
	v_fmac_f32_e32 v33, v228, v238
	v_fmac_f32_e32 v34, v228, v240
	v_fmac_f32_e32 v35, v228, v242
	v_fma_f32 v48, v231, v237, v244
	v_fma_f32 v49, v231, v239, v245
	v_fma_f32 v50, v231, v241, v246
	v_fma_f32 v51, v231, v243, v247
	v_fmac_f32_e32 v48, v230, v236
	v_fmac_f32_e32 v49, v230, v238
	v_fmac_f32_e32 v50, v230, v240
	v_fmac_f32_e32 v51, v230, v242
	ds_read_b128 v[236:239], v248 offset:96
	ds_read_b128 v[240:243], v248 offset:112
	ds_read_b128 v[244:247], v248 offset:128
	s_waitcnt lgkmcnt(3)
	v_fma_f32 v36, v229, v201, v208
	v_fma_f32 v37, v229, v203, v209
	v_fma_f32 v38, v229, v205, v210
	v_fma_f32 v39, v229, v207, v211
	v_fmac_f32_e32 v36, v228, v200
	v_fmac_f32_e32 v37, v228, v202
	v_fmac_f32_e32 v38, v228, v204
	v_fmac_f32_e32 v39, v228, v206
	v_fma_f32 v52, v231, v201, v208
	v_fma_f32 v53, v231, v203, v209
	v_fma_f32 v54, v231, v205, v210
	v_fma_f32 v55, v231, v207, v211
	v_fmac_f32_e32 v52, v230, v200
	v_fmac_f32_e32 v53, v230, v202
	v_fmac_f32_e32 v54, v230, v204
	v_fmac_f32_e32 v55, v230, v206
	ds_read_b128 v[200:203], v248 offset:144
	ds_read_b128 v[204:207], v248 offset:160
	ds_read_b128 v[208:211], v248 offset:176
	s_waitcnt lgkmcnt(3)
	v_fma_f32 v40, v229, v237, v244
	v_fma_f32 v41, v229, v239, v245
	v_fma_f32 v42, v229, v241, v246
	v_fma_f32 v43, v229, v243, v247
	v_fmac_f32_e32 v40, v228, v236
	v_fmac_f32_e32 v41, v228, v238
	v_fmac_f32_e32 v42, v228, v240
	v_fmac_f32_e32 v43, v228, v242
	v_fma_f32 v56, v231, v237, v244
	v_fma_f32 v57, v231, v239, v245
	v_fma_f32 v58, v231, v241, v246
	v_fma_f32 v59, v231, v243, v247
	v_fmac_f32_e32 v56, v230, v236
	v_fmac_f32_e32 v57, v230, v238
	v_fmac_f32_e32 v58, v230, v240
	v_fmac_f32_e32 v59, v230, v242
	s_waitcnt lgkmcnt(0)
	v_fma_f32 v44, v229, v201, v208
	v_fma_f32 v45, v229, v203, v209
	v_fma_f32 v46, v229, v205, v210
	v_fma_f32 v47, v229, v207, v211
	v_fmac_f32_e32 v44, v228, v200
	v_fmac_f32_e32 v45, v228, v202
	v_fmac_f32_e32 v46, v228, v204
	v_fmac_f32_e32 v47, v228, v206
	v_fma_f32 v60, v231, v201, v208
	v_fma_f32 v61, v231, v203, v209
	v_fma_f32 v62, v231, v205, v210
	v_fma_f32 v63, v231, v207, v211
	v_fmac_f32_e32 v60, v230, v200
	v_fmac_f32_e32 v61, v230, v202
	v_fmac_f32_e32 v62, v230, v204
	v_fmac_f32_e32 v63, v230, v206
	s_lshl_b32 s64, s33, 11
	s_lshl_b32 s65, s29, 8
	s_add_u32 s64, s64, s65
	s_add_u32 s64, s64, 128
	s_lshl_b32 s64, s64, 3
	s_add_u32 s42, s12, s64
	s_addc_u32 s43, s13, 0
	global_load_dwordx2 v[228:229], v249, s[42:43] offset:0
	global_load_dwordx2 v[230:231], v249, s[42:43] offset:256
	ds_read_b128 v[236:239], v248 offset:0
	ds_read_b128 v[240:243], v248 offset:16
	ds_read_b128 v[244:247], v248 offset:32
	ds_read_b128 v[200:203], v248 offset:48
	ds_read_b128 v[204:207], v248 offset:64
	ds_read_b128 v[208:211], v248 offset:80
	s_waitcnt lgkmcnt(3)
	s_waitcnt vmcnt(0)
	v_fma_f32 v64, v229, v237, v244
	v_fma_f32 v65, v229, v239, v245
	v_fma_f32 v66, v229, v241, v246
	v_fma_f32 v67, v229, v243, v247
	v_fmac_f32_e32 v64, v228, v236
	v_fmac_f32_e32 v65, v228, v238
	v_fmac_f32_e32 v66, v228, v240
	v_fmac_f32_e32 v67, v228, v242
	v_fma_f32 v80, v231, v237, v244
	v_fma_f32 v81, v231, v239, v245
	v_fma_f32 v82, v231, v241, v246
	v_fma_f32 v83, v231, v243, v247
	v_fmac_f32_e32 v80, v230, v236
	v_fmac_f32_e32 v81, v230, v238
	v_fmac_f32_e32 v82, v230, v240
	v_fmac_f32_e32 v83, v230, v242
	ds_read_b128 v[236:239], v248 offset:96
	ds_read_b128 v[240:243], v248 offset:112
	ds_read_b128 v[244:247], v248 offset:128
	s_waitcnt lgkmcnt(3)
	v_fma_f32 v68, v229, v201, v208
	v_fma_f32 v69, v229, v203, v209
	v_fma_f32 v70, v229, v205, v210
	v_fma_f32 v71, v229, v207, v211
	v_fmac_f32_e32 v68, v228, v200
	v_fmac_f32_e32 v69, v228, v202
	v_fmac_f32_e32 v70, v228, v204
	v_fmac_f32_e32 v71, v228, v206
	v_fma_f32 v84, v231, v201, v208
	v_fma_f32 v85, v231, v203, v209
	v_fma_f32 v86, v231, v205, v210
	v_fma_f32 v87, v231, v207, v211
	v_fmac_f32_e32 v84, v230, v200
	v_fmac_f32_e32 v85, v230, v202
	v_fmac_f32_e32 v86, v230, v204
	v_fmac_f32_e32 v87, v230, v206
	ds_read_b128 v[200:203], v248 offset:144
	ds_read_b128 v[204:207], v248 offset:160
	ds_read_b128 v[208:211], v248 offset:176
	s_waitcnt lgkmcnt(3)
	v_fma_f32 v72, v229, v237, v244
	v_fma_f32 v73, v229, v239, v245
	v_fma_f32 v74, v229, v241, v246
	v_fma_f32 v75, v229, v243, v247
	v_fmac_f32_e32 v72, v228, v236
	v_fmac_f32_e32 v73, v228, v238
	v_fmac_f32_e32 v74, v228, v240
	v_fmac_f32_e32 v75, v228, v242
	v_fma_f32 v88, v231, v237, v244
	v_fma_f32 v89, v231, v239, v245
	v_fma_f32 v90, v231, v241, v246
	v_fma_f32 v91, v231, v243, v247
	v_fmac_f32_e32 v88, v230, v236
	v_fmac_f32_e32 v89, v230, v238
	v_fmac_f32_e32 v90, v230, v240
	v_fmac_f32_e32 v91, v230, v242
	s_waitcnt lgkmcnt(0)
	v_fma_f32 v76, v229, v201, v208
	v_fma_f32 v77, v229, v203, v209
	v_fma_f32 v78, v229, v205, v210
	v_fma_f32 v79, v229, v207, v211
	v_fmac_f32_e32 v76, v228, v200
	v_fmac_f32_e32 v77, v228, v202
	v_fmac_f32_e32 v78, v228, v204
	v_fmac_f32_e32 v79, v228, v206
	v_fma_f32 v92, v231, v201, v208
	v_fma_f32 v93, v231, v203, v209
	v_fma_f32 v94, v231, v205, v210
	v_fma_f32 v95, v231, v207, v211
	v_fmac_f32_e32 v92, v230, v200
	v_fmac_f32_e32 v93, v230, v202
	v_fmac_f32_e32 v94, v230, v204
	v_fmac_f32_e32 v95, v230, v206
	s_lshl_b32 s64, s33, 11
	s_lshl_b32 s65, s29, 8
	s_add_u32 s64, s64, s65
	s_add_u32 s64, s64, 192
	s_lshl_b32 s64, s64, 3
	s_add_u32 s42, s12, s64
	s_addc_u32 s43, s13, 0
	global_load_dwordx2 v[228:229], v249, s[42:43] offset:0
	global_load_dwordx2 v[230:231], v249, s[42:43] offset:256
	ds_read_b128 v[236:239], v248 offset:0
	ds_read_b128 v[240:243], v248 offset:16
	ds_read_b128 v[244:247], v248 offset:32
	ds_read_b128 v[200:203], v248 offset:48
	ds_read_b128 v[204:207], v248 offset:64
	ds_read_b128 v[208:211], v248 offset:80
	s_waitcnt lgkmcnt(3)
	s_waitcnt vmcnt(0)
	v_fma_f32 v96, v229, v237, v244
	v_fma_f32 v97, v229, v239, v245
	v_fma_f32 v98, v229, v241, v246
	v_fma_f32 v99, v229, v243, v247
	v_fmac_f32_e32 v96, v228, v236
	v_fmac_f32_e32 v97, v228, v238
	v_fmac_f32_e32 v98, v228, v240
	v_fmac_f32_e32 v99, v228, v242
	v_fma_f32 v112, v231, v237, v244
	v_fma_f32 v113, v231, v239, v245
	v_fma_f32 v114, v231, v241, v246
	v_fma_f32 v115, v231, v243, v247
	v_fmac_f32_e32 v112, v230, v236
	v_fmac_f32_e32 v113, v230, v238
	v_fmac_f32_e32 v114, v230, v240
	v_fmac_f32_e32 v115, v230, v242
	ds_read_b128 v[236:239], v248 offset:96
	ds_read_b128 v[240:243], v248 offset:112
	ds_read_b128 v[244:247], v248 offset:128
	s_waitcnt lgkmcnt(3)
	v_fma_f32 v100, v229, v201, v208
	v_fma_f32 v101, v229, v203, v209
	v_fma_f32 v102, v229, v205, v210
	v_fma_f32 v103, v229, v207, v211
	v_fmac_f32_e32 v100, v228, v200
	v_fmac_f32_e32 v101, v228, v202
	v_fmac_f32_e32 v102, v228, v204
	v_fmac_f32_e32 v103, v228, v206
	v_fma_f32 v116, v231, v201, v208
	v_fma_f32 v117, v231, v203, v209
	v_fma_f32 v118, v231, v205, v210
	v_fma_f32 v119, v231, v207, v211
	v_fmac_f32_e32 v116, v230, v200
	v_fmac_f32_e32 v117, v230, v202
	v_fmac_f32_e32 v118, v230, v204
	v_fmac_f32_e32 v119, v230, v206
	ds_read_b128 v[200:203], v248 offset:144
	ds_read_b128 v[204:207], v248 offset:160
	ds_read_b128 v[208:211], v248 offset:176
	s_waitcnt lgkmcnt(3)
	v_fma_f32 v104, v229, v237, v244
	v_fma_f32 v105, v229, v239, v245
	v_fma_f32 v106, v229, v241, v246
	v_fma_f32 v107, v229, v243, v247
	v_fmac_f32_e32 v104, v228, v236
	v_fmac_f32_e32 v105, v228, v238
	v_fmac_f32_e32 v106, v228, v240
	v_fmac_f32_e32 v107, v228, v242
	v_fma_f32 v120, v231, v237, v244
	v_fma_f32 v121, v231, v239, v245
	v_fma_f32 v122, v231, v241, v246
	v_fma_f32 v123, v231, v243, v247
	v_fmac_f32_e32 v120, v230, v236
	v_fmac_f32_e32 v121, v230, v238
	v_fmac_f32_e32 v122, v230, v240
	v_fmac_f32_e32 v123, v230, v242
	s_waitcnt lgkmcnt(0)
	v_fma_f32 v108, v229, v201, v208
	v_fma_f32 v109, v229, v203, v209
	v_fma_f32 v110, v229, v205, v210
	v_fma_f32 v111, v229, v207, v211
	v_fmac_f32_e32 v108, v228, v200
	v_fmac_f32_e32 v109, v228, v202
	v_fmac_f32_e32 v110, v228, v204
	v_fmac_f32_e32 v111, v228, v206
	v_fma_f32 v124, v231, v201, v208
	v_fma_f32 v125, v231, v203, v209
	v_fma_f32 v126, v231, v205, v210
	v_fma_f32 v127, v231, v207, v211
	v_fmac_f32_e32 v124, v230, v200
	v_fmac_f32_e32 v125, v230, v202
	v_fmac_f32_e32 v126, v230, v204
	v_fmac_f32_e32 v127, v230, v206
	s_waitcnt vmcnt(0)
	s_waitcnt lgkmcnt(0)
	s_lshl_b32 s64, s33, 3
	s_add_u32 s64, s64, s29
	s_lshl_b32 s64, s64, 5
	s_add_u32 s64, s64, s30
	s_lshl_b32 s64, s64, 2
	s_add_u32 s40, s8, s64
	s_addc_u32 s41, s9, 0
	s_and_b32 s64, s33, 1
	s_lshl_b32 s64, s64, 22
	s_add_u32 s64, s64, s50
	s_add_u32 s36, s6, s64
	s_addc_u32 s37, s7, 0
	v_exp_f32_e32 v200, v0
	v_exp_f32_e32 v201, v1
	v_exp_f32_e32 v202, v2
	v_exp_f32_e32 v203, v3
	v_exp_f32_e32 v204, v4
	v_exp_f32_e32 v205, v5
	v_exp_f32_e32 v206, v6
	v_exp_f32_e32 v207, v7
	v_exp_f32_e32 v208, v8
	v_exp_f32_e32 v209, v9
	v_exp_f32_e32 v210, v10
	v_exp_f32_e32 v211, v11
	v_exp_f32_e32 v212, v12
	v_exp_f32_e32 v213, v13
	v_exp_f32_e32 v214, v14
	v_exp_f32_e32 v215, v15
	v_add_f32_e32 v200, 1.0, v200
	v_add_f32_e32 v201, 1.0, v201
	v_add_f32_e32 v202, 1.0, v202
	v_add_f32_e32 v203, 1.0, v203
	v_add_f32_e32 v204, 1.0, v204
	v_add_f32_e32 v205, 1.0, v205
	v_add_f32_e32 v206, 1.0, v206
	v_add_f32_e32 v207, 1.0, v207
	v_add_f32_e32 v208, 1.0, v208
	v_add_f32_e32 v209, 1.0, v209
	v_add_f32_e32 v210, 1.0, v210
	v_add_f32_e32 v211, 1.0, v211
	v_add_f32_e32 v212, 1.0, v212
	v_add_f32_e32 v213, 1.0, v213
	v_add_f32_e32 v214, 1.0, v214
	v_add_f32_e32 v215, 1.0, v215
	v_rcp_f32_e32 v200, v200
	v_rcp_f32_e32 v201, v201
	v_rcp_f32_e32 v202, v202
	v_rcp_f32_e32 v203, v203
	v_rcp_f32_e32 v204, v204
	v_rcp_f32_e32 v205, v205
	v_rcp_f32_e32 v206, v206
	v_rcp_f32_e32 v207, v207
	v_rcp_f32_e32 v208, v208
	v_rcp_f32_e32 v209, v209
	v_rcp_f32_e32 v210, v210
	v_rcp_f32_e32 v211, v211
	v_rcp_f32_e32 v212, v212
	v_rcp_f32_e32 v213, v213
	v_rcp_f32_e32 v214, v214
	v_rcp_f32_e32 v215, v215
	v_fmamk_f32 v208, v208, 0xc0b8aa3b, v198
	v_fmamk_f32 v209, v209, 0xc0b8aa3b, v198
	v_fmamk_f32 v210, v210, 0xc0b8aa3b, v198
	v_fmamk_f32 v211, v211, 0xc0b8aa3b, v198
	v_mul_f32_e32 v204, v204, v128
	v_mul_f32_e32 v205, v205, v129
	v_mul_f32_e32 v206, v206, v130
	v_mul_f32_e32 v207, v207, v131
	v_fma_f32 v128, v200, v208, v204
	v_fma_f32 v129, v201, v209, v205
	v_fma_f32 v130, v202, v210, v206
	v_fma_f32 v131, v203, v211, v207
	v_exp_f32_e32 v200, v128
	v_exp_f32_e32 v201, v129
	v_exp_f32_e32 v202, v130
	v_exp_f32_e32 v203, v131
	v_add_f32_e32 v200, 1.0, v200
	v_add_f32_e32 v201, 1.0, v201
	v_add_f32_e32 v202, 1.0, v202
	v_add_f32_e32 v203, 1.0, v203
	v_rcp_f32_e32 v200, v200
	v_rcp_f32_e32 v201, v201
	v_rcp_f32_e32 v202, v202
	v_rcp_f32_e32 v203, v203
	v_fma_f32 v200, v200, 2.0, -1.0
	v_fma_f32 v201, v201, 2.0, -1.0
	v_fma_f32 v202, v202, 2.0, -1.0
	v_fma_f32 v203, v203, 2.0, -1.0
	v_mul_f32_e32 v216, v212, v200
	v_mul_f32_e32 v217, v213, v201
	v_mul_f32_e32 v218, v214, v202
	v_mul_f32_e32 v219, v215, v203
	v_cvt_pk_f16_f32 v220, v216, v217
	v_cvt_pk_f16_f32 v221, v218, v219
	v_exp_f32_e32 v200, v16
	v_exp_f32_e32 v201, v17
	v_exp_f32_e32 v202, v18
	v_exp_f32_e32 v203, v19
	v_exp_f32_e32 v204, v20
	v_exp_f32_e32 v205, v21
	v_exp_f32_e32 v206, v22
	v_exp_f32_e32 v207, v23
	v_exp_f32_e32 v208, v24
	v_exp_f32_e32 v209, v25
	v_exp_f32_e32 v210, v26
	v_exp_f32_e32 v211, v27
	v_exp_f32_e32 v212, v28
	v_exp_f32_e32 v213, v29
	v_exp_f32_e32 v214, v30
	v_exp_f32_e32 v215, v31
	v_add_f32_e32 v200, 1.0, v200
	v_add_f32_e32 v201, 1.0, v201
	v_add_f32_e32 v202, 1.0, v202
	v_add_f32_e32 v203, 1.0, v203
	v_add_f32_e32 v204, 1.0, v204
	v_add_f32_e32 v205, 1.0, v205
	v_add_f32_e32 v206, 1.0, v206
	v_add_f32_e32 v207, 1.0, v207
	v_add_f32_e32 v208, 1.0, v208
	v_add_f32_e32 v209, 1.0, v209
	v_add_f32_e32 v210, 1.0, v210
	v_add_f32_e32 v211, 1.0, v211
	v_add_f32_e32 v212, 1.0, v212
	v_add_f32_e32 v213, 1.0, v213
	v_add_f32_e32 v214, 1.0, v214
	v_add_f32_e32 v215, 1.0, v215
	v_rcp_f32_e32 v200, v200
	v_rcp_f32_e32 v201, v201
	v_rcp_f32_e32 v202, v202
	v_rcp_f32_e32 v203, v203
	v_rcp_f32_e32 v204, v204
	v_rcp_f32_e32 v205, v205
	v_rcp_f32_e32 v206, v206
	v_rcp_f32_e32 v207, v207
	v_rcp_f32_e32 v208, v208
	v_rcp_f32_e32 v209, v209
	v_rcp_f32_e32 v210, v210
	v_rcp_f32_e32 v211, v211
	v_rcp_f32_e32 v212, v212
	v_rcp_f32_e32 v213, v213
	v_rcp_f32_e32 v214, v214
	v_rcp_f32_e32 v215, v215
	v_fmamk_f32 v208, v208, 0xc0b8aa3b, v198
	v_fmamk_f32 v209, v209, 0xc0b8aa3b, v198
	v_fmamk_f32 v210, v210, 0xc0b8aa3b, v198
	v_fmamk_f32 v211, v211, 0xc0b8aa3b, v198
	v_mul_f32_e32 v204, v204, v132
	v_mul_f32_e32 v205, v205, v133
	v_mul_f32_e32 v206, v206, v134
	v_mul_f32_e32 v207, v207, v135
	v_fma_f32 v132, v200, v208, v204
	v_fma_f32 v133, v201, v209, v205
	v_fma_f32 v134, v202, v210, v206
	v_fma_f32 v135, v203, v211, v207
	v_exp_f32_e32 v200, v132
	v_exp_f32_e32 v201, v133
	v_exp_f32_e32 v202, v134
	v_exp_f32_e32 v203, v135
	v_add_f32_e32 v200, 1.0, v200
	v_add_f32_e32 v201, 1.0, v201
	v_add_f32_e32 v202, 1.0, v202
	v_add_f32_e32 v203, 1.0, v203
	v_rcp_f32_e32 v200, v200
	v_rcp_f32_e32 v201, v201
	v_rcp_f32_e32 v202, v202
	v_rcp_f32_e32 v203, v203
	v_fma_f32 v200, v200, 2.0, -1.0
	v_fma_f32 v201, v201, 2.0, -1.0
	v_fma_f32 v202, v202, 2.0, -1.0
	v_fma_f32 v203, v203, 2.0, -1.0
	v_mul_f32_e32 v216, v212, v200
	v_mul_f32_e32 v217, v213, v201
	v_mul_f32_e32 v218, v214, v202
	v_mul_f32_e32 v219, v215, v203
	v_cvt_pk_f16_f32 v222, v216, v217
	v_cvt_pk_f16_f32 v223, v218, v219
	s_nop 1
	v_permlane32_swap_b32_e32 v220, v222
	v_permlane32_swap_b32_e32 v221, v223
	s_cmp_eq_u32 s31, 0
	s_cbranch_scc1 .LE_slow4
	global_store_dwordx4 v195, v[220:223], s[36:37] offset:0
	s_branch .LE_join5

.LE_loop16:
	s_sub_u32 s71, s33, 1
	s_add_u32 s61, s33, 1
	s_min_u32 s61, s61, s60
	s_and_b32 s64, s71, 1
	s_lshl_b32 s64, s64, 22
	s_add_u32 s64, s64, s50
	s_add_u32 s64, s64, 0x60000
	s_add_u32 s36, s6, s64
	s_addc_u32 s37, s7, 0
	s_lshl_b32 s64, s71, 3
	s_add_u32 s64, s64, s29
	s_lshl_b32 s64, s64, 5
	s_add_u32 s64, s64, s30
	s_lshl_b32 s64, s64, 2
	s_add_u32 s40, s8, s64
	s_addc_u32 s41, s9, 0
	s_lshl_b32 s64, s33, 11
	s_lshl_b32 s65, s29, 8
	s_add_u32 s64, s64, s65
	s_add_u32 s64, s64, 128
	s_lshl_b32 s64, s64, 3
	s_add_u32 s42, s12, s64
	s_addc_u32 s43, s13, 0
	s_nop 3
	global_load_dwordx2 v[228:229], v249, s[42:43] offset:0
	global_load_dwordx2 v[230:231], v249, s[42:43] offset:256
	s_waitcnt lgkmcnt(4)
	v_mfma_f32_32x32x16_f16 v[0:15], a[0:3], v[160:163], v[0:15]
	ds_read_b128 v[160:163], v192 offset:8192
	v_exp_f32_e32 v200, v96
	v_mfma_f32_32x32x16_f16 v[16:31], a[0:3], v[164:167], v[16:31]
	ds_read_b128 v[164:167], v192 offset:9216
	v_exp_f32_e32 v201, v97
	v_add_f32_e32 v200, 1.0, v200
	v_mfma_f32_32x32x16_f16 v[0:15], a[4:7], v[168:171], v[0:15]
	ds_read_b128 v[168:171], v192 offset:10240
	v_exp_f32_e32 v202, v98
	v_add_f32_e32 v201, 1.0, v201
	v_mfma_f32_32x32x16_f16 v[16:31], a[4:7], v[172:175], v[16:31]
	ds_read_b128 v[172:175], v192 offset:11264
	global_load_lds_dwordx4 v192, s[44:45] offset:1024 sc1
	v_exp_f32_e32 v203, v99
	v_add_f32_e32 v202, 1.0, v202
	s_waitcnt lgkmcnt(4)
	v_mfma_f32_32x32x16_f16 v[0:15], a[8:11], v[176:179], v[0:15]
	ds_read_b128 v[176:179], v192 offset:12288
	v_exp_f32_e32 v204, v100
	v_add_f32_e32 v203, 1.0, v203
	v_mfma_f32_32x32x16_f16 v[16:31], a[8:11], v[180:183], v[16:31]
	ds_read_b128 v[180:183], v192 offset:13312
	v_exp_f32_e32 v205, v101
	v_add_f32_e32 v204, 1.0, v204
	v_mfma_f32_32x32x16_f16 v[0:15], a[12:15], v[184:187], v[0:15]
	ds_read_b128 v[184:187], v192 offset:14336
	v_exp_f32_e32 v206, v102
	v_add_f32_e32 v205, 1.0, v205
	v_mfma_f32_32x32x16_f16 v[16:31], a[12:15], v[188:191], v[16:31]
	ds_read_b128 v[188:191], v192 offset:15360
	global_load_lds_dwordx4 v192, s[44:45] offset:2048 sc1
	v_exp_f32_e32 v207, v103
	v_add_f32_e32 v206, 1.0, v206
	s_waitcnt lgkmcnt(4)
	v_mfma_f32_32x32x16_f16 v[0:15], a[16:19], v[160:163], v[0:15]
	ds_read_b128 v[160:163], v192 offset:16384
	v_exp_f32_e32 v208, v104
	v_add_f32_e32 v207, 1.0, v207
	v_mfma_f32_32x32x16_f16 v[16:31], a[16:19], v[164:167], v[16:31]
	ds_read_b128 v[164:167], v192 offset:17408
	v_exp_f32_e32 v209, v105
	v_add_f32_e32 v208, 1.0, v208
	v_mfma_f32_32x32x16_f16 v[0:15], a[20:23], v[168:171], v[0:15]
	ds_read_b128 v[168:171], v192 offset:18432
	v_exp_f32_e32 v210, v106
	v_add_f32_e32 v209, 1.0, v209
	v_mfma_f32_32x32x16_f16 v[16:31], a[20:23], v[172:175], v[16:31]
	ds_read_b128 v[172:175], v192 offset:19456
	global_load_lds_dwordx4 v192, s[44:45] offset:3072 sc1
	v_exp_f32_e32 v211, v107
	v_add_f32_e32 v210, 1.0, v210
	s_waitcnt lgkmcnt(4)
	v_mfma_f32_32x32x16_f16 v[0:15], a[24:27], v[176:179], v[0:15]
	ds_read_b128 v[176:179], v192 offset:20480
	v_exp_f32_e32 v212, v108
	v_add_f32_e32 v211, 1.0, v211
	v_mfma_f32_32x32x16_f16 v[16:31], a[24:27], v[180:183], v[16:31]
	ds_read_b128 v[180:183], v192 offset:21504
	v_exp_f32_e32 v213, v109
	v_add_f32_e32 v212, 1.0, v212
	v_mfma_f32_32x32x16_f16 v[0:15], a[28:31], v[184:187], v[0:15]
	ds_read_b128 v[184:187], v192 offset:22528
	v_exp_f32_e32 v214, v110
	v_add_f32_e32 v213, 1.0, v213
	v_mfma_f32_32x32x16_f16 v[16:31], a[28:31], v[188:191], v[16:31]
	ds_read_b128 v[188:191], v192 offset:23552
	s_add_u32 s44, s34, 0x11000
	s_addc_u32 s45, s35, 0
	s_mov_b32 m0, s57
	s_nop 0
	global_load_lds_dwordx4 v192, s[44:45] sc1
	v_exp_f32_e32 v215, v111
	v_add_f32_e32 v214, 1.0, v214
	s_waitcnt lgkmcnt(4)
	v_mfma_f32_32x32x16_f16 v[0:15], a[32:35], v[160:163], v[0:15]
	ds_read_b128 v[160:163], v192 offset:24576
	v_add_f32_e32 v215, 1.0, v215
	v_rcp_f32_e32 v200, v200
	v_mfma_f32_32x32x16_f16 v[16:31], a[32:35], v[164:167], v[16:31]
	ds_read_b128 v[164:167], v192 offset:25600
	v_rcp_f32_e32 v201, v201
	v_mfma_f32_32x32x16_f16 v[0:15], a[36:39], v[168:171], v[0:15]
	ds_read_b128 v[168:171], v192 offset:26624
	v_rcp_f32_e32 v202, v202
	v_mfma_f32_32x32x16_f16 v[16:31], a[36:39], v[172:175], v[16:31]
	ds_read_b128 v[172:175], v192 offset:27648
	global_load_lds_dwordx4 v192, s[44:45] offset:1024 sc1
	v_rcp_f32_e32 v203, v203
	s_waitcnt lgkmcnt(4)
	v_mfma_f32_32x32x16_f16 v[0:15], a[40:43], v[176:179], v[0:15]
	ds_read_b128 v[176:179], v192 offset:28672
	v_rcp_f32_e32 v204, v204
	v_mfma_f32_32x32x16_f16 v[16:31], a[40:43], v[180:183], v[16:31]
	ds_read_b128 v[180:183], v192 offset:29696
	v_rcp_f32_e32 v205, v205
	v_mul_f32_e32 v204, v204, v152
	v_mfma_f32_32x32x16_f16 v[0:15], a[44:47], v[184:187], v[0:15]
	ds_read_b128 v[184:187], v192 offset:30720
	v_rcp_f32_e32 v206, v206
	v_mul_f32_e32 v205, v205, v153
	v_mfma_f32_32x32x16_f16 v[16:31], a[44:47], v[188:191], v[16:31]
	ds_read_b128 v[188:191], v192 offset:31744
	global_load_lds_dwordx4 v192, s[44:45] offset:2048 sc1
	v_rcp_f32_e32 v207, v207
	v_mul_f32_e32 v206, v206, v154
	s_waitcnt vmcnt(9)
	s_barrier
	s_waitcnt lgkmcnt(4)
	v_mfma_f32_32x32x16_f16 v[0:15], a[48:51], v[160:163], v[0:15]
	ds_read_b128 v[160:163], v192 offset:32768
	v_rcp_f32_e32 v208, v208
	v_mul_f32_e32 v207, v207, v155
	ds_read_b128 v[236:239], v248 offset:0
	ds_read_b64 v[240:241], v248 offset:32
	ds_read_b128 v[242:245], v248 offset:16
	ds_read_b64 v[246:247], v248 offset:40
	v_mfma_f32_32x32x16_f16 v[16:31], a[48:51], v[164:167], v[16:31]
	ds_read_b128 v[164:167], v192 offset:33792
	v_rcp_f32_e32 v209, v209
	v_fmamk_f32 v208, v208, 0xc0b8aa3b, v198
	s_waitcnt lgkmcnt(3)
	s_waitcnt vmcnt(6)
	v_fma_f32 v64, v229, v237, v240
	v_mfma_f32_32x32x16_f16 v[0:15], a[52:55], v[168:171], v[0:15]
	ds_read_b128 v[168:171], v192 offset:34816
	v_rcp_f32_e32 v210, v210
	v_fmamk_f32 v209, v209, 0xc0b8aa3b, v198
	v_fma_f32 v152, v200, v208, v204
	v_fma_f32 v65, v229, v239, v241
	v_fmac_f32_e32 v64, v228, v236
	v_mfma_f32_32x32x16_f16 v[16:31], a[52:55], v[172:175], v[16:31]
	ds_read_b128 v[172:175], v192 offset:35840
	global_load_lds_dwordx4 v192, s[44:45] offset:3072 sc1
	v_rcp_f32_e32 v211, v211
	v_fmamk_f32 v210, v210, 0xc0b8aa3b, v198
	v_fma_f32 v153, v201, v209, v205
	v_fmac_f32_e32 v65, v228, v238
	v_fma_f32 v80, v231, v237, v240
	v_mfma_f32_32x32x16_f16 v[0:15], a[56:59], v[176:179], v[0:15]
	ds_read_b128 v[176:179], v192 offset:36864
	v_rcp_f32_e32 v212, v212
	v_fmamk_f32 v211, v211, 0xc0b8aa3b, v198
	v_fma_f32 v154, v202, v210, v206
	v_fma_f32 v81, v231, v239, v241
	v_fmac_f32_e32 v80, v230, v236
	v_mfma_f32_32x32x16_f16 v[16:31], a[56:59], v[180:183], v[16:31]
	ds_read_b128 v[180:183], v192 offset:37888
	v_rcp_f32_e32 v213, v213
	v_fma_f32 v155, v203, v211, v207
	v_fmac_f32_e32 v81, v230, v238
	ds_read_b128 v[236:239], v248 offset:48
	ds_read_b64 v[240:241], v248 offset:80
	v_mfma_f32_32x32x16_f16 v[0:15], a[60:63], v[184:187], v[0:15]
	ds_read_b128 v[184:187], v192 offset:38912
	v_rcp_f32_e32 v214, v214
	s_waitcnt lgkmcnt(8)
	v_fma_f32 v66, v229, v243, v246
	v_mfma_f32_32x32x16_f16 v[16:31], a[60:63], v[188:191], v[16:31]
	ds_read_b128 v[188:191], v192 offset:39936
	s_add_u32 s44, s34, 0x18000
	s_addc_u32 s45, s35, 0
	s_mov_b32 m0, s58
	s_nop 0
	global_load_lds_dwordx4 v192, s[44:45] sc1
	v_rcp_f32_e32 v215, v215
	v_fma_f32 v67, v229, v245, v247
	v_fmac_f32_e32 v66, v228, v242
	s_waitcnt lgkmcnt(6)
	v_mfma_f32_32x32x16_f16 v[0:15], a[64:67], v[160:163], v[0:15]
	ds_read_b128 v[160:163], v192 offset:40960
	v_exp_f32_e32 v200, v152
	v_fmac_f32_e32 v67, v228, v244
	v_fma_f32 v82, v231, v243, v246
	v_mfma_f32_32x32x16_f16 v[16:31], a[64:67], v[164:167], v[16:31]
	ds_read_b128 v[164:167], v192 offset:41984
	v_exp_f32_e32 v201, v153
	v_add_f32_e32 v200, 1.0, v200
	v_fma_f32 v83, v231, v245, v247
	v_fmac_f32_e32 v82, v230, v242
	v_mfma_f32_32x32x16_f16 v[0:15], a[68:71], v[168:171], v[0:15]
	ds_read_b128 v[168:171], v192 offset:43008
	v_exp_f32_e32 v202, v154
	v_add_f32_e32 v201, 1.0, v201
	v_fmac_f32_e32 v83, v230, v244
	ds_read_b128 v[242:245], v248 offset:64
	ds_read_b64 v[246:247], v248 offset:88
	v_mfma_f32_32x32x16_f16 v[16:31], a[68:71], v[172:175], v[16:31]
	ds_read_b128 v[172:175], v192 offset:44032
	global_load_lds_dwordx4 v192, s[44:45] offset:1024 sc1
	v_exp_f32_e32 v203, v155
	v_add_f32_e32 v202, 1.0, v202
	s_waitcnt lgkmcnt(8)
	v_fma_f32 v68, v229, v237, v240
	s_waitcnt lgkmcnt(6)
	v_mfma_f32_32x32x16_f16 v[0:15], a[72:75], v[176:179], v[0:15]
	ds_read_b128 v[176:179], v192 offset:45056
	v_add_f32_e32 v203, 1.0, v203
	v_rcp_f32_e32 v200, v200
	v_fma_f32 v69, v229, v239, v241
	v_fmac_f32_e32 v68, v228, v236
	v_mfma_f32_32x32x16_f16 v[16:31], a[72:75], v[180:183], v[16:31]
	ds_read_b128 v[180:183], v192 offset:46080
	v_rcp_f32_e32 v201, v201
	v_fma_f32 v200, v200, 2.0, -1.0
	v_fmac_f32_e32 v69, v228, v238
	v_fma_f32 v84, v231, v237, v240
	v_mfma_f32_32x32x16_f16 v[0:15], a[76:79], v[184:187], v[0:15]
	ds_read_b128 v[184:187], v192 offset:47104
	v_rcp_f32_e32 v202, v202
	v_fma_f32 v201, v201, 2.0, -1.0
	v_mul_f32_e32 v216, v212, v200
	v_fma_f32 v85, v231, v239, v241
	v_fmac_f32_e32 v84, v230, v236
	v_mfma_f32_32x32x16_f16 v[16:31], a[76:79], v[188:191], v[16:31]
	ds_read_b128 v[188:191], v192 offset:48128
	global_load_lds_dwordx4 v192, s[44:45] offset:2048 sc1
	v_rcp_f32_e32 v203, v203
	v_fma_f32 v202, v202, 2.0, -1.0
	v_mul_f32_e32 v217, v213, v201
	v_fmac_f32_e32 v85, v230, v238
	ds_read_b128 v[236:239], v248 offset:96
	ds_read_b64 v[240:241], v248 offset:128
	s_waitcnt lgkmcnt(6)
	v_mfma_f32_32x32x16_f16 v[0:15], a[80:83], v[160:163], v[0:15]
	ds_read_b128 v[160:163], v192 offset:49152
	v_fma_f32 v203, v203, 2.0, -1.0
	v_mul_f32_e32 v218, v214, v202
	v_exp_f32_e32 v200, v112
	v_fma_f32 v70, v229, v243, v246
	v_mfma_f32_32x32x16_f16 v[16:31], a[80:83], v[164:167], v[16:31]
	ds_read_b128 v[164:167], v192 offset:50176
	v_mul_f32_e32 v219, v215, v203
	v_cvt_pk_f16_f32 v220, v216, v217
	v_exp_f32_e32 v201, v113
	v_fma_f32 v71, v229, v245, v247
	v_fmac_f32_e32 v70, v228, v242
	v_mfma_f32_32x32x16_f16 v[0:15], a[84:87], v[168:171], v[0:15]
	ds_read_b128 v[168:171], v192 offset:51200
	v_cvt_pk_f16_f32 v221, v218, v219
	v_exp_f32_e32 v202, v114
	v_add_f32_e32 v200, 1.0, v200
	v_fmac_f32_e32 v71, v228, v244
	v_fma_f32 v86, v231, v243, v246
	v_mfma_f32_32x32x16_f16 v[16:31], a[84:87], v[172:175], v[16:31]
	ds_read_b128 v[172:175], v192 offset:52224
	global_load_lds_dwordx4 v192, s[44:45] offset:3072 sc1
	v_exp_f32_e32 v203, v115
	v_add_f32_e32 v201, 1.0, v201
	v_add_f32_e32 v202, 1.0, v202
	v_fma_f32 v87, v231, v245, v247
	v_fmac_f32_e32 v86, v230, v242
	s_waitcnt lgkmcnt(6)
	v_mfma_f32_32x32x16_f16 v[0:15], a[88:91], v[176:179], v[0:15]
	ds_read_b128 v[176:179], v192 offset:53248
	v_exp_f32_e32 v204, v116
	v_add_f32_e32 v203, 1.0, v203
	v_fmac_f32_e32 v87, v230, v244
	ds_read_b128 v[242:245], v248 offset:112
	ds_read_b64 v[246:247], v248 offset:136
	v_mfma_f32_32x32x16_f16 v[16:31], a[88:91], v[180:183], v[16:31]
	ds_read_b128 v[180:183], v192 offset:54272
	v_exp_f32_e32 v205, v117
	v_add_f32_e32 v204, 1.0, v204
	s_waitcnt lgkmcnt(8)
	v_fma_f32 v72, v229, v237, v240
	v_mfma_f32_32x32x16_f16 v[0:15], a[92:95], v[184:187], v[0:15]
	ds_read_b128 v[184:187], v192 offset:55296
	v_exp_f32_e32 v206, v118
	v_add_f32_e32 v205, 1.0, v205
	v_fma_f32 v73, v229, v239, v241
	v_fmac_f32_e32 v72, v228, v236
	v_mfma_f32_32x32x16_f16 v[16:31], a[92:95], v[188:191], v[16:31]
	ds_read_b128 v[188:191], v192 offset:56320
	s_add_u32 s44, s34, 0x19000
	s_addc_u32 s45, s35, 0
	s_mov_b32 m0, s59
	s_nop 0
	global_load_lds_dwordx4 v192, s[44:45] sc1
	s_lshl_b32 s64, s71, 3
	s_add_u32 s64, s64, s29
	s_lshl_b32 s64, s64, 7
	s_add_u32 s38, s8, s64
	s_addc_u32 s39, s9, 0
	global_load_dword v251, v196, s[38:39] sc1
	v_exp_f32_e32 v207, v119
	v_add_f32_e32 v206, 1.0, v206
	v_fmac_f32_e32 v73, v228, v238
	v_fma_f32 v88, v231, v237, v240
	s_waitcnt lgkmcnt(6)
	v_mfma_f32_32x32x16_f16 v[0:15], a[96:99], v[160:163], v[0:15]
	ds_read_b128 v[160:163], v192 offset:57344
	v_exp_f32_e32 v208, v120
	v_add_f32_e32 v207, 1.0, v207
	v_fma_f32 v89, v231, v239, v241
	v_fmac_f32_e32 v88, v230, v236
	v_mfma_f32_32x32x16_f16 v[16:31], a[96:99], v[164:167], v[16:31]
	ds_read_b128 v[164:167], v192 offset:58368
	v_exp_f32_e32 v209, v121
	v_add_f32_e32 v208, 1.0, v208
	v_fmac_f32_e32 v89, v230, v238
	ds_read_b128 v[236:239], v248 offset:144
	ds_read_b64 v[240:241], v248 offset:176
	v_mfma_f32_32x32x16_f16 v[0:15], a[100:103], v[168:171], v[0:15]
	ds_read_b128 v[168:171], v192 offset:59392
	v_exp_f32_e32 v210, v122
	v_add_f32_e32 v209, 1.0, v209
	s_waitcnt lgkmcnt(8)
	v_fma_f32 v74, v229, v243, v246
	v_mfma_f32_32x32x16_f16 v[16:31], a[100:103], v[172:175], v[16:31]
	ds_read_b128 v[172:175], v192 offset:60416
	global_load_lds_dwordx4 v192, s[44:45] offset:1024 sc1
	v_exp_f32_e32 v211, v123
	v_add_f32_e32 v210, 1.0, v210
	v_fma_f32 v75, v229, v245, v247
	v_fmac_f32_e32 v74, v228, v242
	s_waitcnt lgkmcnt(6)
	v_mfma_f32_32x32x16_f16 v[0:15], a[104:107], v[176:179], v[0:15]
	ds_read_b128 v[176:179], v192 offset:61440
	v_exp_f32_e32 v212, v124
	v_add_f32_e32 v211, 1.0, v211
	v_fmac_f32_e32 v75, v228, v244
	v_fma_f32 v90, v231, v243, v246
	v_mfma_f32_32x32x16_f16 v[16:31], a[104:107], v[180:183], v[16:31]
	ds_read_b128 v[180:183], v192 offset:62464
	v_exp_f32_e32 v213, v125
	v_add_f32_e32 v212, 1.0, v212
	v_fma_f32 v91, v231, v245, v247
	v_fmac_f32_e32 v90, v230, v242
	v_mfma_f32_32x32x16_f16 v[0:15], a[108:111], v[184:187], v[0:15]
	ds_read_b128 v[184:187], v192 offset:63488
	v_exp_f32_e32 v214, v126
	v_add_f32_e32 v213, 1.0, v213
	v_fmac_f32_e32 v91, v230, v244
	ds_read_b128 v[242:245], v248 offset:160
	ds_read_b64 v[246:247], v248 offset:184
	v_mfma_f32_32x32x16_f16 v[16:31], a[108:111], v[188:191], v[16:31]
	ds_read_b128 v[188:191], v192 offset:64512
	global_load_lds_dwordx4 v192, s[44:45] offset:2048 sc1
	v_exp_f32_e32 v215, v127
	v_add_f32_e32 v214, 1.0, v214
	s_waitcnt lgkmcnt(8)
	v_fma_f32 v76, v229, v237, v240
	s_waitcnt vmcnt(8)
	s_barrier
	s_waitcnt lgkmcnt(6)
	v_mfma_f32_32x32x16_f16 v[0:15], a[112:115], v[160:163], v[0:15]
	ds_read_b128 v[160:163], v193 offset:0
	v_add_f32_e32 v215, 1.0, v215
	v_rcp_f32_e32 v200, v200
	v_fma_f32 v77, v229, v239, v241
	v_fmac_f32_e32 v76, v228, v236
	v_mfma_f32_32x32x16_f16 v[16:31], a[112:115], v[164:167], v[16:31]
	ds_read_b128 v[164:167], v193 offset:1024
	v_rcp_f32_e32 v201, v201
	v_fmac_f32_e32 v77, v228, v238
	v_fma_f32 v92, v231, v237, v240
	v_mfma_f32_32x32x16_f16 v[0:15], a[116:119], v[168:171], v[0:15]
	ds_read_b128 v[168:171], v193 offset:2048
	v_rcp_f32_e32 v202, v202
	v_fma_f32 v93, v231, v239, v241
	v_fmac_f32_e32 v92, v230, v236
	v_mfma_f32_32x32x16_f16 v[16:31], a[116:119], v[172:175], v[16:31]
	ds_read_b128 v[172:175], v193 offset:3072
	global_load_lds_dwordx4 v192, s[44:45] offset:3072 sc1
	v_rcp_f32_e32 v203, v203
	v_fmac_f32_e32 v93, v230, v238
	s_waitcnt lgkmcnt(5)
	s_waitcnt lgkmcnt(4)
	v_mfma_f32_32x32x16_f16 v[0:15], a[120:123], v[176:179], v[0:15]
	ds_read_b128 v[176:179], v193 offset:4096
	v_rcp_f32_e32 v204, v204
	v_fma_f32 v78, v229, v243, v246
	v_fma_f32 v79, v229, v245, v247
	v_mfma_f32_32x32x16_f16 v[16:31], a[120:123], v[180:183], v[16:31]
	ds_read_b128 v[180:183], v193 offset:5120
	v_rcp_f32_e32 v205, v205
	v_mul_f32_e32 v204, v204, v156
	v_fmac_f32_e32 v78, v228, v242
	v_fmac_f32_e32 v79, v228, v244
	v_mfma_f32_32x32x16_f16 v[0:15], a[124:127], v[184:187], v[0:15]
	ds_read_b128 v[184:187], v193 offset:6144
	v_rcp_f32_e32 v206, v206
	v_mul_f32_e32 v205, v205, v157
	v_fma_f32 v94, v231, v243, v246
	v_fma_f32 v95, v231, v245, v247
	v_mfma_f32_32x32x16_f16 v[16:31], a[124:127], v[188:191], v[16:31]
	ds_read_b128 v[188:191], v193 offset:7168
	s_waitcnt vmcnt(3)
	v_cmp_gt_u32_e32 vcc, 2, v251
	s_cbranch_vccz .LE_tok20

.LE_tok20:
	s_and_b32 s64, s71, 1
	s_lshl_b32 s64, s64, 22
	s_add_u32 s64, s64, s49
	s_add_u32 s64, s64, 0x20000
	s_add_u32 s34, s6, s64
	s_addc_u32 s35, s7, 0
	s_add_u32 s44, s34, 0x0
	s_addc_u32 s45, s35, 0
	s_mov_b32 m0, s52
	s_nop 0
	global_load_lds_dwordx4 v192, s[44:45] sc1
	v_rcp_f32_e32 v207, v207
	v_mul_f32_e32 v206, v206, v158
	v_fmac_f32_e32 v94, v230, v242
	v_fmac_f32_e32 v95, v230, v244
	s_waitcnt lgkmcnt(4)
	v_mfma_f32_32x32x16_f16 v[0:15], a[128:131], v[160:163], v[0:15]
	ds_read_b128 v[160:163], v193 offset:8192
	v_rcp_f32_e32 v208, v208
	v_mul_f32_e32 v207, v207, v159
	v_mfma_f32_32x32x16_f16 v[16:31], a[128:131], v[164:167], v[16:31]
	ds_read_b128 v[164:167], v193 offset:9216
	v_rcp_f32_e32 v209, v209
	v_fmamk_f32 v208, v208, 0xc0b8aa3b, v198
	v_mfma_f32_32x32x16_f16 v[0:15], a[132:135], v[168:171], v[0:15]
	ds_read_b128 v[168:171], v193 offset:10240
	v_rcp_f32_e32 v210, v210
	v_fmamk_f32 v209, v209, 0xc0b8aa3b, v198
	v_fma_f32 v156, v200, v208, v204
	v_mfma_f32_32x32x16_f16 v[16:31], a[132:135], v[172:175], v[16:31]
	ds_read_b128 v[172:175], v193 offset:11264
	global_load_lds_dwordx4 v192, s[44:45] offset:1024 sc1
	v_rcp_f32_e32 v211, v211
	v_fmamk_f32 v210, v210, 0xc0b8aa3b, v198
	v_fma_f32 v157, v201, v209, v205
	s_waitcnt lgkmcnt(4)
	v_mfma_f32_32x32x16_f16 v[0:15], a[136:139], v[176:179], v[0:15]
	ds_read_b128 v[176:179], v193 offset:12288
	v_rcp_f32_e32 v212, v212
	v_fmamk_f32 v211, v211, 0xc0b8aa3b, v198
	v_fma_f32 v158, v202, v210, v206
	v_mfma_f32_32x32x16_f16 v[16:31], a[136:139], v[180:183], v[16:31]
	ds_read_b128 v[180:183], v193 offset:13312
	v_rcp_f32_e32 v213, v213
	v_fma_f32 v159, v203, v211, v207
	v_mfma_f32_32x32x16_f16 v[0:15], a[140:143], v[184:187], v[0:15]
	ds_read_b128 v[184:187], v193 offset:14336
	v_rcp_f32_e32 v214, v214
	v_mfma_f32_32x32x16_f16 v[16:31], a[140:143], v[188:191], v[16:31]
	ds_read_b128 v[188:191], v193 offset:15360
	global_load_lds_dwordx4 v192, s[44:45] offset:2048 sc1
	v_rcp_f32_e32 v215, v215
	s_waitcnt lgkmcnt(4)
	v_mfma_f32_32x32x16_f16 v[0:15], a[144:147], v[160:163], v[0:15]
	ds_read_b128 v[160:163], v193 offset:16384
	v_exp_f32_e32 v200, v156
	v_mfma_f32_32x32x16_f16 v[16:31], a[144:147], v[164:167], v[16:31]
	ds_read_b128 v[164:167], v193 offset:17408
	v_exp_f32_e32 v201, v157
	v_add_f32_e32 v200, 1.0, v200
	v_mfma_f32_32x32x16_f16 v[0:15], a[148:151], v[168:171], v[0:15]
	ds_read_b128 v[168:171], v193 offset:18432
	v_exp_f32_e32 v202, v158
	v_add_f32_e32 v201, 1.0, v201
	v_mfma_f32_32x32x16_f16 v[16:31], a[148:151], v[172:175], v[16:31]
	ds_read_b128 v[172:175], v193 offset:19456
	global_load_lds_dwordx4 v192, s[44:45] offset:3072 sc1
	v_exp_f32_e32 v203, v159
	v_add_f32_e32 v202, 1.0, v202
	s_waitcnt lgkmcnt(4)
	v_mfma_f32_32x32x16_f16 v[0:15], a[152:155], v[176:179], v[0:15]
	ds_read_b128 v[176:179], v193 offset:20480
	v_add_f32_e32 v203, 1.0, v203
	v_rcp_f32_e32 v200, v200
	v_mfma_f32_32x32x16_f16 v[16:31], a[152:155], v[180:183], v[16:31]
	ds_read_b128 v[180:183], v193 offset:21504
	v_rcp_f32_e32 v201, v201
	v_fma_f32 v200, v200, 2.0, -1.0
	v_mfma_f32_32x32x16_f16 v[0:15], a[156:159], v[184:187], v[0:15]
	ds_read_b128 v[184:187], v193 offset:22528
	v_rcp_f32_e32 v202, v202
	v_fma_f32 v201, v201, 2.0, -1.0
	v_mul_f32_e32 v216, v212, v200
	v_mfma_f32_32x32x16_f16 v[16:31], a[156:159], v[188:191], v[16:31]
	ds_read_b128 v[188:191], v193 offset:23552
	s_add_u32 s44, s34, 0x1000
	s_addc_u32 s45, s35, 0
	s_mov_b32 m0, s53
	s_nop 0
	global_load_lds_dwordx4 v192, s[44:45] sc1
	v_rcp_f32_e32 v203, v203
	v_fma_f32 v202, v202, 2.0, -1.0
	v_mul_f32_e32 v217, v213, v201
	s_waitcnt lgkmcnt(4)
	v_mfma_f32_32x32x16_f16 v[0:15], a[160:163], v[160:163], v[0:15]
	ds_read_b128 v[160:163], v193 offset:24576
	v_fma_f32 v203, v203, 2.0, -1.0
	v_mul_f32_e32 v218, v214, v202
	v_mfma_f32_32x32x16_f16 v[16:31], a[160:163], v[164:167], v[16:31]
	ds_read_b128 v[164:167], v193 offset:25600
	v_mul_f32_e32 v219, v215, v203
	v_cvt_pk_f16_f32 v222, v216, v217
	v_mfma_f32_32x32x16_f16 v[0:15], a[164:167], v[168:171], v[0:15]
	ds_read_b128 v[168:171], v193 offset:26624
	v_cvt_pk_f16_f32 v223, v218, v219
	v_mfma_f32_32x32x16_f16 v[16:31], a[164:167], v[172:175], v[16:31]
	ds_read_b128 v[172:175], v193 offset:27648
	global_load_lds_dwordx4 v192, s[44:45] offset:1024 sc1
	s_nop 1
	v_permlane32_swap_b32_e32 v220, v222
	v_permlane32_swap_b32_e32 v221, v223
	s_cmp_eq_u32 s31, 0
	s_cbranch_scc1 .LE_slow22
	global_store_dwordx4 v195, v[220:223], s[36:37] offset:0
	s_branch .LE_join23

.LE_join23:
	s_waitcnt lgkmcnt(4)
	v_mfma_f32_32x32x16_f16 v[0:15], a[168:171], v[176:179], v[0:15]
	ds_read_b128 v[176:179], v193 offset:28672
	v_mfma_f32_32x32x16_f16 v[16:31], a[168:171], v[180:183], v[16:31]
	ds_read_b128 v[180:183], v193 offset:29696
	v_mfma_f32_32x32x16_f16 v[0:15], a[172:175], v[184:187], v[0:15]
	ds_read_b128 v[184:187], v193 offset:30720
	v_mfma_f32_32x32x16_f16 v[16:31], a[172:175], v[188:191], v[16:31]
	ds_read_b128 v[188:191], v193 offset:31744
	global_load_lds_dwordx4 v192, s[44:45] offset:2048 sc1
	s_waitcnt vmcnt(8)
	s_barrier
	s_waitcnt lgkmcnt(4)
	v_mfma_f32_32x32x16_f16 v[0:15], a[176:179], v[160:163], v[0:15]
	ds_read_b128 v[160:163], v193 offset:32768
	v_mfma_f32_32x32x16_f16 v[16:31], a[176:179], v[164:167], v[16:31]
	ds_read_b128 v[164:167], v193 offset:33792
	v_mfma_f32_32x32x16_f16 v[0:15], a[180:183], v[168:171], v[0:15]
	ds_read_b128 v[168:171], v193 offset:34816
	v_mfma_f32_32x32x16_f16 v[16:31], a[180:183], v[172:175], v[16:31]
	ds_read_b128 v[172:175], v193 offset:35840
	global_load_lds_dwordx4 v192, s[44:45] offset:3072 sc1
	s_waitcnt lgkmcnt(4)
	v_mfma_f32_32x32x16_f16 v[0:15], a[184:187], v[176:179], v[0:15]
	ds_read_b128 v[176:179], v193 offset:36864
	v_mfma_f32_32x32x16_f16 v[16:31], a[184:187], v[180:183], v[16:31]
	ds_read_b128 v[180:183], v193 offset:37888
	v_mfma_f32_32x32x16_f16 v[0:15], a[188:191], v[184:187], v[0:15]
	ds_read_b128 v[184:187], v193 offset:38912
	v_mfma_f32_32x32x16_f16 v[16:31], a[188:191], v[188:191], v[16:31]
	ds_read_b128 v[188:191], v193 offset:39936
	s_add_u32 s44, s34, 0x8000
	s_addc_u32 s45, s35, 0
	s_mov_b32 m0, s54
	s_nop 0
	global_load_lds_dwordx4 v192, s[44:45] sc1
	s_waitcnt lgkmcnt(4)
	v_mfma_f32_32x32x16_f16 v[0:15], a[192:195], v[160:163], v[0:15]
	ds_read_b128 v[160:163], v193 offset:40960
	s_waitcnt vmcnt(3)
	s_barrier
	v_mov_b32_e32 v199, 4
	s_cmp_eq_u32 s31, 0
	s_cbranch_scc1 .LE_slow24
	global_store_dword v197, v199, s[40:41]
	s_branch .LE_join25

.LE_join25:
	v_mfma_f32_32x32x16_f16 v[16:31], a[192:195], v[164:167], v[16:31]
	ds_read_b128 v[164:167], v193 offset:41984
	v_mfma_f32_32x32x16_f16 v[0:15], a[196:199], v[168:171], v[0:15]
	ds_read_b128 v[168:171], v193 offset:43008
	v_mfma_f32_32x32x16_f16 v[16:31], a[196:199], v[172:175], v[16:31]
	ds_read_b128 v[172:175], v193 offset:44032
	global_load_lds_dwordx4 v192, s[44:45] offset:1024 sc1
	s_waitcnt lgkmcnt(4)
	v_mfma_f32_32x32x16_f16 v[0:15], a[200:203], v[176:179], v[0:15]
	ds_read_b128 v[176:179], v193 offset:45056
	v_mfma_f32_32x32x16_f16 v[16:31], a[200:203], v[180:183], v[16:31]
	ds_read_b128 v[180:183], v193 offset:46080
	v_mfma_f32_32x32x16_f16 v[0:15], a[204:207], v[184:187], v[0:15]
	ds_read_b128 v[184:187], v193 offset:47104
	v_mfma_f32_32x32x16_f16 v[16:31], a[204:207], v[188:191], v[16:31]
	ds_read_b128 v[188:191], v193 offset:48128
	global_load_lds_dwordx4 v192, s[44:45] offset:2048 sc1
	s_waitcnt lgkmcnt(4)
	v_mfma_f32_32x32x16_f16 v[0:15], a[208:211], v[160:163], v[0:15]
	ds_read_b128 v[160:163], v193 offset:49152
	v_mfma_f32_32x32x16_f16 v[16:31], a[208:211], v[164:167], v[16:31]
	ds_read_b128 v[164:167], v193 offset:50176
	v_mfma_f32_32x32x16_f16 v[0:15], a[212:215], v[168:171], v[0:15]
	ds_read_b128 v[168:171], v193 offset:51200
	v_mfma_f32_32x32x16_f16 v[16:31], a[212:215], v[172:175], v[16:31]
	ds_read_b128 v[172:175], v193 offset:52224
	global_load_lds_dwordx4 v192, s[44:45] offset:3072 sc1
	s_waitcnt lgkmcnt(4)
	v_mfma_f32_32x32x16_f16 v[0:15], a[216:219], v[176:179], v[0:15]
	ds_read_b128 v[176:179], v193 offset:53248
	v_mfma_f32_32x32x16_f16 v[16:31], a[216:219], v[180:183], v[16:31]
	ds_read_b128 v[180:183], v193 offset:54272
	v_mfma_f32_32x32x16_f16 v[0:15], a[220:223], v[184:187], v[0:15]
	ds_read_b128 v[184:187], v193 offset:55296
	v_mfma_f32_32x32x16_f16 v[16:31], a[220:223], v[188:191], v[16:31]
	ds_read_b128 v[188:191], v193 offset:56320
	s_add_u32 s44, s34, 0x9000
	s_addc_u32 s45, s35, 0
	s_mov_b32 m0, s55
	s_nop 0
	global_load_lds_dwordx4 v192, s[44:45] sc1
	s_waitcnt lgkmcnt(4)
	v_mfma_f32_32x32x16_f16 v[0:15], a[224:227], v[160:163], v[0:15]
	ds_read_b128 v[160:163], v193 offset:57344
	v_mfma_f32_32x32x16_f16 v[16:31], a[224:227], v[164:167], v[16:31]
	ds_read_b128 v[164:167], v193 offset:58368
	v_mfma_f32_32x32x16_f16 v[0:15], a[228:231], v[168:171], v[0:15]
	ds_read_b128 v[168:171], v193 offset:59392
	v_mfma_f32_32x32x16_f16 v[16:31], a[228:231], v[172:175], v[16:31]
	ds_read_b128 v[172:175], v193 offset:60416
	global_load_lds_dwordx4 v192, s[44:45] offset:1024 sc1
	s_waitcnt lgkmcnt(4)
	v_mfma_f32_32x32x16_f16 v[0:15], a[232:235], v[176:179], v[0:15]
	ds_read_b128 v[176:179], v193 offset:61440
	v_mfma_f32_32x32x16_f16 v[16:31], a[232:235], v[180:183], v[16:31]
	ds_read_b128 v[180:183], v193 offset:62464
	v_mfma_f32_32x32x16_f16 v[0:15], a[236:239], v[184:187], v[0:15]
	ds_read_b128 v[184:187], v193 offset:63488
	v_mfma_f32_32x32x16_f16 v[16:31], a[236:239], v[188:191], v[16:31]
	ds_read_b128 v[188:191], v193 offset:64512
	global_load_lds_dwordx4 v192, s[44:45] offset:2048 sc1
	s_waitcnt vmcnt(8)
	s_barrier
	s_waitcnt lgkmcnt(4)
	v_mfma_f32_32x32x16_f16 v[0:15], a[240:243], v[160:163], v[0:15]
	ds_read_b128 v[160:163], v192 offset:0
	v_mfma_f32_32x32x16_f16 v[16:31], a[240:243], v[164:167], v[16:31]
	ds_read_b128 v[164:167], v192 offset:1024
	v_mfma_f32_32x32x16_f16 v[0:15], a[244:247], v[168:171], v[0:15]
	ds_read_b128 v[168:171], v192 offset:2048
	v_mfma_f32_32x32x16_f16 v[16:31], a[244:247], v[172:175], v[16:31]
	ds_read_b128 v[172:175], v192 offset:3072
	global_load_lds_dwordx4 v192, s[44:45] offset:3072 sc1
	s_waitcnt lgkmcnt(4)
	v_mfma_f32_32x32x16_f16 v[0:15], a[248:251], v[176:179], v[0:15]
	ds_read_b128 v[176:179], v192 offset:4096
	v_mfma_f32_32x32x16_f16 v[16:31], a[248:251], v[180:183], v[16:31]
	ds_read_b128 v[180:183], v192 offset:5120
	v_mfma_f32_32x32x16_f16 v[0:15], a[252:255], v[184:187], v[0:15]
	ds_read_b128 v[184:187], v192 offset:6144
	v_mfma_f32_32x32x16_f16 v[16:31], a[252:255], v[188:191], v[16:31]
	ds_read_b128 v[188:191], v192 offset:7168
	s_add_u32 s44, s34, 0x10000
	s_addc_u32 s45, s35, 0
	s_mov_b32 m0, s56
	s_nop 0
	global_load_lds_dwordx4 v192, s[44:45] sc1
	s_and_b32 s64, s33, 1
	s_lshl_b32 s64, s64, 22
	s_add_u32 s64, s64, s50
	s_add_u32 s36, s6, s64
	s_addc_u32 s37, s7, 0
	s_lshl_b32 s64, s33, 3
	s_add_u32 s64, s64, s29
	s_lshl_b32 s64, s64, 5
	s_add_u32 s64, s64, s30
	s_lshl_b32 s64, s64, 2
	s_add_u32 s40, s8, s64
	s_addc_u32 s41, s9, 0
	s_lshl_b32 s64, s33, 11
	s_lshl_b32 s65, s29, 8
	s_add_u32 s64, s64, s65
	s_add_u32 s64, s64, 192
	s_lshl_b32 s64, s64, 3
	s_add_u32 s42, s12, s64
	s_addc_u32 s43, s13, 0
	s_nop 3
	global_load_dwordx2 v[228:229], v249, s[42:43] offset:0
	global_load_dwordx2 v[230:231], v249, s[42:43] offset:256
	s_waitcnt lgkmcnt(4)
	v_mfma_f32_32x32x16_f16 v[32:47], a[0:3], v[160:163], v[32:47]
	ds_read_b128 v[160:163], v192 offset:8192
	v_exp_f32_e32 v200, v0
	v_mfma_f32_32x32x16_f16 v[48:63], a[0:3], v[164:167], v[48:63]
	ds_read_b128 v[164:167], v192 offset:9216
	v_exp_f32_e32 v201, v1
	v_add_f32_e32 v200, 1.0, v200
	v_mfma_f32_32x32x16_f16 v[32:47], a[4:7], v[168:171], v[32:47]
	ds_read_b128 v[168:171], v192 offset:10240
	v_exp_f32_e32 v202, v2
	v_add_f32_e32 v201, 1.0, v201
	v_mfma_f32_32x32x16_f16 v[48:63], a[4:7], v[172:175], v[48:63]
	ds_read_b128 v[172:175], v192 offset:11264
	global_load_lds_dwordx4 v192, s[44:45] offset:1024 sc1
	v_exp_f32_e32 v203, v3
	v_add_f32_e32 v202, 1.0, v202
	s_waitcnt lgkmcnt(4)
	v_mfma_f32_32x32x16_f16 v[32:47], a[8:11], v[176:179], v[32:47]
	ds_read_b128 v[176:179], v192 offset:12288
	v_exp_f32_e32 v204, v4
	v_add_f32_e32 v203, 1.0, v203
	v_mfma_f32_32x32x16_f16 v[48:63], a[8:11], v[180:183], v[48:63]
	ds_read_b128 v[180:183], v192 offset:13312
	v_exp_f32_e32 v205, v5
	v_add_f32_e32 v204, 1.0, v204
	v_mfma_f32_32x32x16_f16 v[32:47], a[12:15], v[184:187], v[32:47]
	ds_read_b128 v[184:187], v192 offset:14336
	v_exp_f32_e32 v206, v6
	v_add_f32_e32 v205, 1.0, v205
	v_mfma_f32_32x32x16_f16 v[48:63], a[12:15], v[188:191], v[48:63]
	ds_read_b128 v[188:191], v192 offset:15360
	global_load_lds_dwordx4 v192, s[44:45] offset:2048 sc1
	v_exp_f32_e32 v207, v7
	v_add_f32_e32 v206, 1.0, v206
	s_waitcnt lgkmcnt(4)
	v_mfma_f32_32x32x16_f16 v[32:47], a[16:19], v[160:163], v[32:47]
	ds_read_b128 v[160:163], v192 offset:16384
	v_exp_f32_e32 v208, v8
	v_add_f32_e32 v207, 1.0, v207
	v_mfma_f32_32x32x16_f16 v[48:63], a[16:19], v[164:167], v[48:63]
	ds_read_b128 v[164:167], v192 offset:17408
	v_exp_f32_e32 v209, v9
	v_add_f32_e32 v208, 1.0, v208
	v_mfma_f32_32x32x16_f16 v[32:47], a[20:23], v[168:171], v[32:47]
	ds_read_b128 v[168:171], v192 offset:18432
	v_exp_f32_e32 v210, v10
	v_add_f32_e32 v209, 1.0, v209
	v_mfma_f32_32x32x16_f16 v[48:63], a[20:23], v[172:175], v[48:63]
	ds_read_b128 v[172:175], v192 offset:19456
	global_load_lds_dwordx4 v192, s[44:45] offset:3072 sc1
	v_exp_f32_e32 v211, v11
	v_add_f32_e32 v210, 1.0, v210
	s_waitcnt lgkmcnt(4)
	v_mfma_f32_32x32x16_f16 v[32:47], a[24:27], v[176:179], v[32:47]
	ds_read_b128 v[176:179], v192 offset:20480
	v_exp_f32_e32 v212, v12
	v_add_f32_e32 v211, 1.0, v211
	v_mfma_f32_32x32x16_f16 v[48:63], a[24:27], v[180:183], v[48:63]
	ds_read_b128 v[180:183], v192 offset:21504
	v_exp_f32_e32 v213, v13
	v_add_f32_e32 v212, 1.0, v212
	v_mfma_f32_32x32x16_f16 v[32:47], a[28:31], v[184:187], v[32:47]
	ds_read_b128 v[184:187], v192 offset:22528
	v_exp_f32_e32 v214, v14
	v_add_f32_e32 v213, 1.0, v213
	v_mfma_f32_32x32x16_f16 v[48:63], a[28:31], v[188:191], v[48:63]
	ds_read_b128 v[188:191], v192 offset:23552
	s_add_u32 s44, s34, 0x11000
	s_addc_u32 s45, s35, 0
	s_mov_b32 m0, s57
	s_nop 0
	global_load_lds_dwordx4 v192, s[44:45] sc1
	v_exp_f32_e32 v215, v15
	v_add_f32_e32 v214, 1.0, v214
	s_waitcnt lgkmcnt(4)
	v_mfma_f32_32x32x16_f16 v[32:47], a[32:35], v[160:163], v[32:47]
	ds_read_b128 v[160:163], v192 offset:24576
	v_add_f32_e32 v215, 1.0, v215
	v_rcp_f32_e32 v200, v200
	v_mfma_f32_32x32x16_f16 v[48:63], a[32:35], v[164:167], v[48:63]
	ds_read_b128 v[164:167], v192 offset:25600
	v_rcp_f32_e32 v201, v201
	v_mfma_f32_32x32x16_f16 v[32:47], a[36:39], v[168:171], v[32:47]
	ds_read_b128 v[168:171], v192 offset:26624
	v_rcp_f32_e32 v202, v202
	v_mfma_f32_32x32x16_f16 v[48:63], a[36:39], v[172:175], v[48:63]
	ds_read_b128 v[172:175], v192 offset:27648
	global_load_lds_dwordx4 v192, s[44:45] offset:1024 sc1
	v_rcp_f32_e32 v203, v203
	s_waitcnt lgkmcnt(4)
	v_mfma_f32_32x32x16_f16 v[32:47], a[40:43], v[176:179], v[32:47]
	ds_read_b128 v[176:179], v192 offset:28672
	v_rcp_f32_e32 v204, v204
	v_mfma_f32_32x32x16_f16 v[48:63], a[40:43], v[180:183], v[48:63]
	ds_read_b128 v[180:183], v192 offset:29696
	v_rcp_f32_e32 v205, v205
	v_mul_f32_e32 v204, v204, v128
	v_mfma_f32_32x32x16_f16 v[32:47], a[44:47], v[184:187], v[32:47]
	ds_read_b128 v[184:187], v192 offset:30720
	v_rcp_f32_e32 v206, v206
	v_mul_f32_e32 v205, v205, v129
	v_mfma_f32_32x32x16_f16 v[48:63], a[44:47], v[188:191], v[48:63]
	ds_read_b128 v[188:191], v192 offset:31744
	global_load_lds_dwordx4 v192, s[44:45] offset:2048 sc1
	v_rcp_f32_e32 v207, v207
	v_mul_f32_e32 v206, v206, v130
	s_waitcnt vmcnt(9)
	s_barrier
	s_waitcnt lgkmcnt(4)
	v_mfma_f32_32x32x16_f16 v[32:47], a[48:51], v[160:163], v[32:47]
	ds_read_b128 v[160:163], v192 offset:32768
	v_rcp_f32_e32 v208, v208
	v_mul_f32_e32 v207, v207, v131
	ds_read_b128 v[236:239], v248 offset:0
	ds_read_b64 v[240:241], v248 offset:32
	ds_read_b128 v[242:245], v248 offset:16
	ds_read_b64 v[246:247], v248 offset:40
	v_mfma_f32_32x32x16_f16 v[48:63], a[48:51], v[164:167], v[48:63]
	ds_read_b128 v[164:167], v192 offset:33792
	v_rcp_f32_e32 v209, v209
	v_fmamk_f32 v208, v208, 0xc0b8aa3b, v198
	s_waitcnt lgkmcnt(3)
	s_waitcnt vmcnt(6)
	v_fma_f32 v96, v229, v237, v240
	v_mfma_f32_32x32x16_f16 v[32:47], a[52:55], v[168:171], v[32:47]
	ds_read_b128 v[168:171], v192 offset:34816
	v_rcp_f32_e32 v210, v210
	v_fmamk_f32 v209, v209, 0xc0b8aa3b, v198
	v_fma_f32 v128, v200, v208, v204
	v_fma_f32 v97, v229, v239, v241
	v_fmac_f32_e32 v96, v228, v236
	v_mfma_f32_32x32x16_f16 v[48:63], a[52:55], v[172:175], v[48:63]
	ds_read_b128 v[172:175], v192 offset:35840
	global_load_lds_dwordx4 v192, s[44:45] offset:3072 sc1
	v_rcp_f32_e32 v211, v211
	v_fmamk_f32 v210, v210, 0xc0b8aa3b, v198
	v_fma_f32 v129, v201, v209, v205
	v_fmac_f32_e32 v97, v228, v238
	v_fma_f32 v112, v231, v237, v240
	v_mfma_f32_32x32x16_f16 v[32:47], a[56:59], v[176:179], v[32:47]
	ds_read_b128 v[176:179], v192 offset:36864
	v_rcp_f32_e32 v212, v212
	v_fmamk_f32 v211, v211, 0xc0b8aa3b, v198
	v_fma_f32 v130, v202, v210, v206
	v_fma_f32 v113, v231, v239, v241
	v_fmac_f32_e32 v112, v230, v236
	v_mfma_f32_32x32x16_f16 v[48:63], a[56:59], v[180:183], v[48:63]
	ds_read_b128 v[180:183], v192 offset:37888
	v_rcp_f32_e32 v213, v213
	v_fma_f32 v131, v203, v211, v207
	v_fmac_f32_e32 v113, v230, v238
	ds_read_b128 v[236:239], v248 offset:48
	ds_read_b64 v[240:241], v248 offset:80
	v_mfma_f32_32x32x16_f16 v[32:47], a[60:63], v[184:187], v[32:47]
	ds_read_b128 v[184:187], v192 offset:38912
	v_rcp_f32_e32 v214, v214
	s_waitcnt lgkmcnt(8)
	v_fma_f32 v98, v229, v243, v246
	v_mfma_f32_32x32x16_f16 v[48:63], a[60:63], v[188:191], v[48:63]
	ds_read_b128 v[188:191], v192 offset:39936
	s_add_u32 s44, s34, 0x18000
	s_addc_u32 s45, s35, 0
	s_mov_b32 m0, s58
	s_nop 0
	global_load_lds_dwordx4 v192, s[44:45] sc1
	v_rcp_f32_e32 v215, v215
	v_fma_f32 v99, v229, v245, v247
	v_fmac_f32_e32 v98, v228, v242
	s_waitcnt lgkmcnt(6)
	v_mfma_f32_32x32x16_f16 v[32:47], a[64:67], v[160:163], v[32:47]
	ds_read_b128 v[160:163], v192 offset:40960
	v_exp_f32_e32 v200, v128
	v_fmac_f32_e32 v99, v228, v244
	v_fma_f32 v114, v231, v243, v246
	v_mfma_f32_32x32x16_f16 v[48:63], a[64:67], v[164:167], v[48:63]
	ds_read_b128 v[164:167], v192 offset:41984
	v_exp_f32_e32 v201, v129
	v_add_f32_e32 v200, 1.0, v200
	v_fma_f32 v115, v231, v245, v247
	v_fmac_f32_e32 v114, v230, v242
	v_mfma_f32_32x32x16_f16 v[32:47], a[68:71], v[168:171], v[32:47]
	ds_read_b128 v[168:171], v192 offset:43008
	v_exp_f32_e32 v202, v130
	v_add_f32_e32 v201, 1.0, v201
	v_fmac_f32_e32 v115, v230, v244
	ds_read_b128 v[242:245], v248 offset:64
	ds_read_b64 v[246:247], v248 offset:88
	v_mfma_f32_32x32x16_f16 v[48:63], a[68:71], v[172:175], v[48:63]
	ds_read_b128 v[172:175], v192 offset:44032
	global_load_lds_dwordx4 v192, s[44:45] offset:1024 sc1
	v_exp_f32_e32 v203, v131
	v_add_f32_e32 v202, 1.0, v202
	s_waitcnt lgkmcnt(8)
	v_fma_f32 v100, v229, v237, v240
	s_waitcnt lgkmcnt(6)
	v_mfma_f32_32x32x16_f16 v[32:47], a[72:75], v[176:179], v[32:47]
	ds_read_b128 v[176:179], v192 offset:45056
	v_add_f32_e32 v203, 1.0, v203
	v_rcp_f32_e32 v200, v200
	v_fma_f32 v101, v229, v239, v241
	v_fmac_f32_e32 v100, v228, v236
	v_mfma_f32_32x32x16_f16 v[48:63], a[72:75], v[180:183], v[48:63]
	ds_read_b128 v[180:183], v192 offset:46080
	v_rcp_f32_e32 v201, v201
	v_fma_f32 v200, v200, 2.0, -1.0
	v_fmac_f32_e32 v101, v228, v238
	v_fma_f32 v116, v231, v237, v240
	v_mfma_f32_32x32x16_f16 v[32:47], a[76:79], v[184:187], v[32:47]
	ds_read_b128 v[184:187], v192 offset:47104
	v_rcp_f32_e32 v202, v202
	v_fma_f32 v201, v201, 2.0, -1.0
	v_mul_f32_e32 v216, v212, v200
	v_fma_f32 v117, v231, v239, v241
	v_fmac_f32_e32 v116, v230, v236
	v_mfma_f32_32x32x16_f16 v[48:63], a[76:79], v[188:191], v[48:63]
	ds_read_b128 v[188:191], v192 offset:48128
	global_load_lds_dwordx4 v192, s[44:45] offset:2048 sc1
	v_rcp_f32_e32 v203, v203
	v_fma_f32 v202, v202, 2.0, -1.0
	v_mul_f32_e32 v217, v213, v201
	v_fmac_f32_e32 v117, v230, v238
	ds_read_b128 v[236:239], v248 offset:96
	ds_read_b64 v[240:241], v248 offset:128
	s_waitcnt lgkmcnt(6)
	v_mfma_f32_32x32x16_f16 v[32:47], a[80:83], v[160:163], v[32:47]
	ds_read_b128 v[160:163], v192 offset:49152
	v_fma_f32 v203, v203, 2.0, -1.0
	v_mul_f32_e32 v218, v214, v202
	v_exp_f32_e32 v200, v16
	v_fma_f32 v102, v229, v243, v246
	v_mfma_f32_32x32x16_f16 v[48:63], a[80:83], v[164:167], v[48:63]
	ds_read_b128 v[164:167], v192 offset:50176
	v_mul_f32_e32 v219, v215, v203
	v_cvt_pk_f16_f32 v220, v216, v217
	v_exp_f32_e32 v201, v17
	v_fma_f32 v103, v229, v245, v247
	v_fmac_f32_e32 v102, v228, v242
	v_mfma_f32_32x32x16_f16 v[32:47], a[84:87], v[168:171], v[32:47]
	ds_read_b128 v[168:171], v192 offset:51200
	v_cvt_pk_f16_f32 v221, v218, v219
	v_exp_f32_e32 v202, v18
	v_add_f32_e32 v200, 1.0, v200
	v_fmac_f32_e32 v103, v228, v244
	v_fma_f32 v118, v231, v243, v246
	v_mfma_f32_32x32x16_f16 v[48:63], a[84:87], v[172:175], v[48:63]
	ds_read_b128 v[172:175], v192 offset:52224
	global_load_lds_dwordx4 v192, s[44:45] offset:3072 sc1
	s_cmp_lg_u32 s33, s60
	s_cbranch_scc1 .LE_nht26
	s_add_u32 s46, s62, 0x0
	s_addc_u32 s47, s63, 0
	global_store_dwordx4 v250, v[216:219], s[46:47]
	s_waitcnt vmcnt(0)
.LE_nht26:
	v_exp_f32_e32 v203, v19
	v_fma_f32 v119, v231, v245, v247
	v_fmac_f32_e32 v118, v230, v242
	s_waitcnt lgkmcnt(6)
	v_mfma_f32_32x32x16_f16 v[32:47], a[88:91], v[176:179], v[32:47]
	ds_read_b128 v[176:179], v192 offset:53248
	v_exp_f32_e32 v204, v20
	v_add_f32_e32 v201, 1.0, v201
	v_add_f32_e32 v202, 1.0, v202
	v_fmac_f32_e32 v119, v230, v244
	ds_read_b128 v[242:245], v248 offset:112
	ds_read_b64 v[246:247], v248 offset:136
	v_mfma_f32_32x32x16_f16 v[48:63], a[88:91], v[180:183], v[48:63]
	ds_read_b128 v[180:183], v192 offset:54272
	v_exp_f32_e32 v205, v21
	v_add_f32_e32 v203, 1.0, v203
	v_add_f32_e32 v204, 1.0, v204
	s_waitcnt lgkmcnt(8)
	v_fma_f32 v104, v229, v237, v240
	v_mfma_f32_32x32x16_f16 v[32:47], a[92:95], v[184:187], v[32:47]
	ds_read_b128 v[184:187], v192 offset:55296
	v_exp_f32_e32 v206, v22
	v_add_f32_e32 v205, 1.0, v205
	v_fma_f32 v105, v229, v239, v241
	v_fmac_f32_e32 v104, v228, v236
	v_mfma_f32_32x32x16_f16 v[48:63], a[92:95], v[188:191], v[48:63]
	ds_read_b128 v[188:191], v192 offset:56320
	s_add_u32 s44, s34, 0x19000
	s_addc_u32 s45, s35, 0
	s_mov_b32 m0, s59
	s_nop 0
	global_load_lds_dwordx4 v192, s[44:45] sc1
	s_lshl_b32 s64, s71, 3
	s_add_u32 s64, s64, s29
	s_lshl_b32 s64, s64, 7
	s_add_u32 s38, s8, s64
	s_addc_u32 s39, s9, 0
	global_load_dword v251, v196, s[38:39] sc1
	v_exp_f32_e32 v207, v23
	v_add_f32_e32 v206, 1.0, v206
	v_fmac_f32_e32 v105, v228, v238
	v_fma_f32 v120, v231, v237, v240
	s_waitcnt lgkmcnt(6)
	v_mfma_f32_32x32x16_f16 v[32:47], a[96:99], v[160:163], v[32:47]
	ds_read_b128 v[160:163], v192 offset:57344
	v_exp_f32_e32 v208, v24
	v_add_f32_e32 v207, 1.0, v207
	v_fma_f32 v121, v231, v239, v241
	v_fmac_f32_e32 v120, v230, v236
	v_mfma_f32_32x32x16_f16 v[48:63], a[96:99], v[164:167], v[48:63]
	ds_read_b128 v[164:167], v192 offset:58368
	v_exp_f32_e32 v209, v25
	v_add_f32_e32 v208, 1.0, v208
	v_fmac_f32_e32 v121, v230, v238
	ds_read_b128 v[236:239], v248 offset:144
	ds_read_b64 v[240:241], v248 offset:176
	v_mfma_f32_32x32x16_f16 v[32:47], a[100:103], v[168:171], v[32:47]
	ds_read_b128 v[168:171], v192 offset:59392
	v_exp_f32_e32 v210, v26
	v_add_f32_e32 v209, 1.0, v209
	s_waitcnt lgkmcnt(8)
	v_fma_f32 v106, v229, v243, v246
	v_mfma_f32_32x32x16_f16 v[48:63], a[100:103], v[172:175], v[48:63]
	ds_read_b128 v[172:175], v192 offset:60416
	global_load_lds_dwordx4 v192, s[44:45] offset:1024 sc1
	v_exp_f32_e32 v211, v27
	v_add_f32_e32 v210, 1.0, v210
	v_fma_f32 v107, v229, v245, v247
	v_fmac_f32_e32 v106, v228, v242
	s_waitcnt lgkmcnt(6)
	v_mfma_f32_32x32x16_f16 v[32:47], a[104:107], v[176:179], v[32:47]
	ds_read_b128 v[176:179], v192 offset:61440
	v_exp_f32_e32 v212, v28
	v_add_f32_e32 v211, 1.0, v211
	v_fmac_f32_e32 v107, v228, v244
	v_fma_f32 v122, v231, v243, v246
	v_mfma_f32_32x32x16_f16 v[48:63], a[104:107], v[180:183], v[48:63]
	ds_read_b128 v[180:183], v192 offset:62464
	v_exp_f32_e32 v213, v29
	v_add_f32_e32 v212, 1.0, v212
	v_fma_f32 v123, v231, v245, v247
	v_fmac_f32_e32 v122, v230, v242
	v_mfma_f32_32x32x16_f16 v[32:47], a[108:111], v[184:187], v[32:47]
	ds_read_b128 v[184:187], v192 offset:63488
	v_exp_f32_e32 v214, v30
	v_add_f32_e32 v213, 1.0, v213
	v_fmac_f32_e32 v123, v230, v244
	ds_read_b128 v[242:245], v248 offset:160
	ds_read_b64 v[246:247], v248 offset:184
	v_mfma_f32_32x32x16_f16 v[48:63], a[108:111], v[188:191], v[48:63]
	ds_read_b128 v[188:191], v192 offset:64512
	global_load_lds_dwordx4 v192, s[44:45] offset:2048 sc1
	v_exp_f32_e32 v215, v31
	v_add_f32_e32 v214, 1.0, v214
	s_waitcnt lgkmcnt(8)
	v_fma_f32 v108, v229, v237, v240
	s_waitcnt vmcnt(8)
	s_barrier
	s_waitcnt lgkmcnt(6)
	v_mfma_f32_32x32x16_f16 v[32:47], a[112:115], v[160:163], v[32:47]
	ds_read_b128 v[160:163], v193 offset:0
	v_add_f32_e32 v215, 1.0, v215
	v_rcp_f32_e32 v200, v200
	v_fma_f32 v109, v229, v239, v241
	v_fmac_f32_e32 v108, v228, v236
	v_mfma_f32_32x32x16_f16 v[48:63], a[112:115], v[164:167], v[48:63]
	ds_read_b128 v[164:167], v193 offset:1024
	v_rcp_f32_e32 v201, v201
	v_fmac_f32_e32 v109, v228, v238
	v_fma_f32 v124, v231, v237, v240
	v_mfma_f32_32x32x16_f16 v[32:47], a[116:119], v[168:171], v[32:47]
	ds_read_b128 v[168:171], v193 offset:2048
	v_rcp_f32_e32 v202, v202
	v_fma_f32 v125, v231, v239, v241
	v_fmac_f32_e32 v124, v230, v236
	v_mfma_f32_32x32x16_f16 v[48:63], a[116:119], v[172:175], v[48:63]
	ds_read_b128 v[172:175], v193 offset:3072
	global_load_lds_dwordx4 v192, s[44:45] offset:3072 sc1
	v_rcp_f32_e32 v203, v203
	v_fmac_f32_e32 v125, v230, v238
	s_waitcnt lgkmcnt(5)
	s_waitcnt lgkmcnt(4)
	v_mfma_f32_32x32x16_f16 v[32:47], a[120:123], v[176:179], v[32:47]
	ds_read_b128 v[176:179], v193 offset:4096
	v_rcp_f32_e32 v204, v204
	v_fma_f32 v110, v229, v243, v246
	v_fma_f32 v111, v229, v245, v247
	v_mfma_f32_32x32x16_f16 v[48:63], a[120:123], v[180:183], v[48:63]
	ds_read_b128 v[180:183], v193 offset:5120
	v_rcp_f32_e32 v205, v205
	v_mul_f32_e32 v204, v204, v132
	v_fmac_f32_e32 v110, v228, v242
	v_fmac_f32_e32 v111, v228, v244
	v_mfma_f32_32x32x16_f16 v[32:47], a[124:127], v[184:187], v[32:47]
	ds_read_b128 v[184:187], v193 offset:6144
	v_rcp_f32_e32 v206, v206
	v_mul_f32_e32 v205, v205, v133
	v_fma_f32 v126, v231, v243, v246
	v_fma_f32 v127, v231, v245, v247
	v_mfma_f32_32x32x16_f16 v[48:63], a[124:127], v[188:191], v[48:63]
	ds_read_b128 v[188:191], v193 offset:7168
	s_waitcnt vmcnt(3)
	v_cmp_gt_u32_e32 vcc, 3, v251
	s_cbranch_vccz .LE_tok27

.LE_tok27:
	s_and_b32 s64, s71, 1
	s_lshl_b32 s64, s64, 22
	s_add_u32 s64, s64, s49
	s_add_u32 s64, s64, 0x40000
	s_add_u32 s34, s6, s64
	s_addc_u32 s35, s7, 0
	s_add_u32 s44, s34, 0x0
	s_addc_u32 s45, s35, 0
	s_mov_b32 m0, s52
	s_nop 0
	global_load_lds_dwordx4 v192, s[44:45] sc1
	v_rcp_f32_e32 v207, v207
	v_mul_f32_e32 v206, v206, v134
	v_fmac_f32_e32 v126, v230, v242
	v_fmac_f32_e32 v127, v230, v244
	s_waitcnt lgkmcnt(4)
	v_mfma_f32_32x32x16_f16 v[32:47], a[128:131], v[160:163], v[32:47]
	ds_read_b128 v[160:163], v193 offset:8192
	v_rcp_f32_e32 v208, v208
	v_mul_f32_e32 v207, v207, v135
	v_mfma_f32_32x32x16_f16 v[48:63], a[128:131], v[164:167], v[48:63]
	ds_read_b128 v[164:167], v193 offset:9216
	v_rcp_f32_e32 v209, v209
	v_fmamk_f32 v208, v208, 0xc0b8aa3b, v198
	v_mfma_f32_32x32x16_f16 v[32:47], a[132:135], v[168:171], v[32:47]
	ds_read_b128 v[168:171], v193 offset:10240
	v_rcp_f32_e32 v210, v210
	v_fmamk_f32 v209, v209, 0xc0b8aa3b, v198
	v_fma_f32 v132, v200, v208, v204
	v_mfma_f32_32x32x16_f16 v[48:63], a[132:135], v[172:175], v[48:63]
	ds_read_b128 v[172:175], v193 offset:11264
	global_load_lds_dwordx4 v192, s[44:45] offset:1024 sc1
	v_rcp_f32_e32 v211, v211
	v_fmamk_f32 v210, v210, 0xc0b8aa3b, v198
	v_fma_f32 v133, v201, v209, v205
	s_waitcnt lgkmcnt(4)
	v_mfma_f32_32x32x16_f16 v[32:47], a[136:139], v[176:179], v[32:47]
	ds_read_b128 v[176:179], v193 offset:12288
	v_rcp_f32_e32 v212, v212
	v_fmamk_f32 v211, v211, 0xc0b8aa3b, v198
	v_fma_f32 v134, v202, v210, v206
	v_mfma_f32_32x32x16_f16 v[48:63], a[136:139], v[180:183], v[48:63]
	ds_read_b128 v[180:183], v193 offset:13312
	v_rcp_f32_e32 v213, v213
	v_fma_f32 v135, v203, v211, v207
	v_mfma_f32_32x32x16_f16 v[32:47], a[140:143], v[184:187], v[32:47]
	ds_read_b128 v[184:187], v193 offset:14336
	v_rcp_f32_e32 v214, v214
	v_mfma_f32_32x32x16_f16 v[48:63], a[140:143], v[188:191], v[48:63]
	ds_read_b128 v[188:191], v193 offset:15360
	global_load_lds_dwordx4 v192, s[44:45] offset:2048 sc1
	v_rcp_f32_e32 v215, v215
	s_waitcnt lgkmcnt(4)
	v_mfma_f32_32x32x16_f16 v[32:47], a[144:147], v[160:163], v[32:47]
	ds_read_b128 v[160:163], v193 offset:16384
	v_exp_f32_e32 v200, v132
	v_mfma_f32_32x32x16_f16 v[48:63], a[144:147], v[164:167], v[48:63]
	ds_read_b128 v[164:167], v193 offset:17408
	v_exp_f32_e32 v201, v133
	v_add_f32_e32 v200, 1.0, v200
	v_mfma_f32_32x32x16_f16 v[32:47], a[148:151], v[168:171], v[32:47]
	ds_read_b128 v[168:171], v193 offset:18432
	v_exp_f32_e32 v202, v134
	v_add_f32_e32 v201, 1.0, v201
	v_mfma_f32_32x32x16_f16 v[48:63], a[148:151], v[172:175], v[48:63]
	ds_read_b128 v[172:175], v193 offset:19456
	global_load_lds_dwordx4 v192, s[44:45] offset:3072 sc1
	v_exp_f32_e32 v203, v135
	v_add_f32_e32 v202, 1.0, v202
	s_waitcnt lgkmcnt(4)
	v_mfma_f32_32x32x16_f16 v[32:47], a[152:155], v[176:179], v[32:47]
	ds_read_b128 v[176:179], v193 offset:20480
	v_add_f32_e32 v203, 1.0, v203
	v_rcp_f32_e32 v200, v200
	v_mfma_f32_32x32x16_f16 v[48:63], a[152:155], v[180:183], v[48:63]
	ds_read_b128 v[180:183], v193 offset:21504
	v_rcp_f32_e32 v201, v201
	v_fma_f32 v200, v200, 2.0, -1.0
	v_mfma_f32_32x32x16_f16 v[32:47], a[156:159], v[184:187], v[32:47]
	ds_read_b128 v[184:187], v193 offset:22528
	v_rcp_f32_e32 v202, v202
	v_fma_f32 v201, v201, 2.0, -1.0
	v_mul_f32_e32 v216, v212, v200
	v_mfma_f32_32x32x16_f16 v[48:63], a[156:159], v[188:191], v[48:63]
	ds_read_b128 v[188:191], v193 offset:23552
	s_add_u32 s44, s34, 0x1000
	s_addc_u32 s45, s35, 0
	s_mov_b32 m0, s53
	s_nop 0
	global_load_lds_dwordx4 v192, s[44:45] sc1
	v_rcp_f32_e32 v203, v203
	v_fma_f32 v202, v202, 2.0, -1.0
	v_mul_f32_e32 v217, v213, v201
	s_waitcnt lgkmcnt(4)
	v_mfma_f32_32x32x16_f16 v[32:47], a[160:163], v[160:163], v[32:47]
	ds_read_b128 v[160:163], v193 offset:24576
	v_fma_f32 v203, v203, 2.0, -1.0
	v_mul_f32_e32 v218, v214, v202
	v_mfma_f32_32x32x16_f16 v[48:63], a[160:163], v[164:167], v[48:63]
	ds_read_b128 v[164:167], v193 offset:25600
	v_mul_f32_e32 v219, v215, v203
	v_cvt_pk_f16_f32 v222, v216, v217
	v_mfma_f32_32x32x16_f16 v[32:47], a[164:167], v[168:171], v[32:47]
	ds_read_b128 v[168:171], v193 offset:26624
	v_cvt_pk_f16_f32 v223, v218, v219
	v_mfma_f32_32x32x16_f16 v[48:63], a[164:167], v[172:175], v[48:63]
	ds_read_b128 v[172:175], v193 offset:27648
	global_load_lds_dwordx4 v192, s[44:45] offset:1024 sc1
	s_cmp_lg_u32 s33, s60
	s_cbranch_scc1 .LE_nht29
	s_add_u32 s46, s62, 0x20000
	s_addc_u32 s47, s63, 0
	global_store_dwordx4 v250, v[216:219], s[46:47]
	s_waitcnt vmcnt(0)
.LE_nht29:
	s_waitcnt lgkmcnt(4)
	v_mfma_f32_32x32x16_f16 v[32:47], a[168:171], v[176:179], v[32:47]
	ds_read_b128 v[176:179], v193 offset:28672
	s_nop 1
	v_permlane32_swap_b32_e32 v220, v222
	v_permlane32_swap_b32_e32 v221, v223
	s_cmp_eq_u32 s31, 0
	s_cbranch_scc1 .LE_slow30
	global_store_dwordx4 v195, v[220:223], s[36:37] offset:0
	s_branch .LE_join31

.LE_join31:
	v_mfma_f32_32x32x16_f16 v[48:63], a[168:171], v[180:183], v[48:63]
	ds_read_b128 v[180:183], v193 offset:29696
	v_mfma_f32_32x32x16_f16 v[32:47], a[172:175], v[184:187], v[32:47]
	ds_read_b128 v[184:187], v193 offset:30720
	v_mfma_f32_32x32x16_f16 v[48:63], a[172:175], v[188:191], v[48:63]
	ds_read_b128 v[188:191], v193 offset:31744
	global_load_lds_dwordx4 v192, s[44:45] offset:2048 sc1
	s_waitcnt vmcnt(8)
	s_barrier
	s_waitcnt lgkmcnt(4)
	v_mfma_f32_32x32x16_f16 v[32:47], a[176:179], v[160:163], v[32:47]
	ds_read_b128 v[160:163], v193 offset:32768
	v_mfma_f32_32x32x16_f16 v[48:63], a[176:179], v[164:167], v[48:63]
	ds_read_b128 v[164:167], v193 offset:33792
	v_mfma_f32_32x32x16_f16 v[32:47], a[180:183], v[168:171], v[32:47]
	ds_read_b128 v[168:171], v193 offset:34816
	v_mfma_f32_32x32x16_f16 v[48:63], a[180:183], v[172:175], v[48:63]
	ds_read_b128 v[172:175], v193 offset:35840
	global_load_lds_dwordx4 v192, s[44:45] offset:3072 sc1
	s_waitcnt lgkmcnt(4)
	v_mfma_f32_32x32x16_f16 v[32:47], a[184:187], v[176:179], v[32:47]
	ds_read_b128 v[176:179], v193 offset:36864
	v_mfma_f32_32x32x16_f16 v[48:63], a[184:187], v[180:183], v[48:63]
	ds_read_b128 v[180:183], v193 offset:37888
	v_mfma_f32_32x32x16_f16 v[32:47], a[188:191], v[184:187], v[32:47]
	ds_read_b128 v[184:187], v193 offset:38912
	v_mfma_f32_32x32x16_f16 v[48:63], a[188:191], v[188:191], v[48:63]
	ds_read_b128 v[188:191], v193 offset:39936
	s_add_u32 s44, s34, 0x8000
	s_addc_u32 s45, s35, 0
	s_mov_b32 m0, s54
	s_nop 0
	global_load_lds_dwordx4 v192, s[44:45] sc1
	s_waitcnt lgkmcnt(4)
	v_mfma_f32_32x32x16_f16 v[32:47], a[192:195], v[160:163], v[32:47]
	ds_read_b128 v[160:163], v193 offset:40960
	v_mfma_f32_32x32x16_f16 v[48:63], a[192:195], v[164:167], v[48:63]
	ds_read_b128 v[164:167], v193 offset:41984
	s_waitcnt vmcnt(3)
	s_barrier
	v_mov_b32_e32 v199, 1
	s_cmp_eq_u32 s31, 0
	s_cbranch_scc1 .LE_slow32
	global_store_dword v197, v199, s[40:41]
	s_branch .LE_join33

.LE_join33:
	v_mfma_f32_32x32x16_f16 v[32:47], a[196:199], v[168:171], v[32:47]
	ds_read_b128 v[168:171], v193 offset:43008
	v_mfma_f32_32x32x16_f16 v[48:63], a[196:199], v[172:175], v[48:63]
	ds_read_b128 v[172:175], v193 offset:44032
	global_load_lds_dwordx4 v192, s[44:45] offset:1024 sc1
	s_waitcnt lgkmcnt(4)
	v_mfma_f32_32x32x16_f16 v[32:47], a[200:203], v[176:179], v[32:47]
	ds_read_b128 v[176:179], v193 offset:45056
	v_mfma_f32_32x32x16_f16 v[48:63], a[200:203], v[180:183], v[48:63]
	ds_read_b128 v[180:183], v193 offset:46080
	v_mfma_f32_32x32x16_f16 v[32:47], a[204:207], v[184:187], v[32:47]
	ds_read_b128 v[184:187], v193 offset:47104
	v_mfma_f32_32x32x16_f16 v[48:63], a[204:207], v[188:191], v[48:63]
	ds_read_b128 v[188:191], v193 offset:48128
	global_load_lds_dwordx4 v192, s[44:45] offset:2048 sc1
	s_waitcnt lgkmcnt(4)
	v_mfma_f32_32x32x16_f16 v[32:47], a[208:211], v[160:163], v[32:47]
	ds_read_b128 v[160:163], v193 offset:49152
	v_mfma_f32_32x32x16_f16 v[48:63], a[208:211], v[164:167], v[48:63]
	ds_read_b128 v[164:167], v193 offset:50176
	v_mfma_f32_32x32x16_f16 v[32:47], a[212:215], v[168:171], v[32:47]
	ds_read_b128 v[168:171], v193 offset:51200
	v_mfma_f32_32x32x16_f16 v[48:63], a[212:215], v[172:175], v[48:63]
	ds_read_b128 v[172:175], v193 offset:52224
	global_load_lds_dwordx4 v192, s[44:45] offset:3072 sc1
	s_waitcnt lgkmcnt(4)
	v_mfma_f32_32x32x16_f16 v[32:47], a[216:219], v[176:179], v[32:47]
	ds_read_b128 v[176:179], v193 offset:53248
	v_mfma_f32_32x32x16_f16 v[48:63], a[216:219], v[180:183], v[48:63]
	ds_read_b128 v[180:183], v193 offset:54272
	v_mfma_f32_32x32x16_f16 v[32:47], a[220:223], v[184:187], v[32:47]
	ds_read_b128 v[184:187], v193 offset:55296
	v_mfma_f32_32x32x16_f16 v[48:63], a[220:223], v[188:191], v[48:63]
	ds_read_b128 v[188:191], v193 offset:56320
	s_add_u32 s44, s34, 0x9000
	s_addc_u32 s45, s35, 0
	s_mov_b32 m0, s55
	s_nop 0
	global_load_lds_dwordx4 v192, s[44:45] sc1
	s_waitcnt lgkmcnt(4)
	v_mfma_f32_32x32x16_f16 v[32:47], a[224:227], v[160:163], v[32:47]
	ds_read_b128 v[160:163], v193 offset:57344
	v_mfma_f32_32x32x16_f16 v[48:63], a[224:227], v[164:167], v[48:63]
	ds_read_b128 v[164:167], v193 offset:58368
	v_mfma_f32_32x32x16_f16 v[32:47], a[228:231], v[168:171], v[32:47]
	ds_read_b128 v[168:171], v193 offset:59392
	v_mfma_f32_32x32x16_f16 v[48:63], a[228:231], v[172:175], v[48:63]
	ds_read_b128 v[172:175], v193 offset:60416
	global_load_lds_dwordx4 v192, s[44:45] offset:1024 sc1
	s_waitcnt lgkmcnt(4)
	v_mfma_f32_32x32x16_f16 v[32:47], a[232:235], v[176:179], v[32:47]
	ds_read_b128 v[176:179], v193 offset:61440
	v_mfma_f32_32x32x16_f16 v[48:63], a[232:235], v[180:183], v[48:63]
	ds_read_b128 v[180:183], v193 offset:62464
	v_mfma_f32_32x32x16_f16 v[32:47], a[236:239], v[184:187], v[32:47]
	ds_read_b128 v[184:187], v193 offset:63488
	v_mfma_f32_32x32x16_f16 v[48:63], a[236:239], v[188:191], v[48:63]
	ds_read_b128 v[188:191], v193 offset:64512
	global_load_lds_dwordx4 v192, s[44:45] offset:2048 sc1
	s_waitcnt vmcnt(8)
	s_barrier
	s_waitcnt lgkmcnt(4)
	v_mfma_f32_32x32x16_f16 v[32:47], a[240:243], v[160:163], v[32:47]
	ds_read_b128 v[160:163], v192 offset:0
	v_mfma_f32_32x32x16_f16 v[48:63], a[240:243], v[164:167], v[48:63]
	ds_read_b128 v[164:167], v192 offset:1024
	v_mfma_f32_32x32x16_f16 v[32:47], a[244:247], v[168:171], v[32:47]
	ds_read_b128 v[168:171], v192 offset:2048
	v_mfma_f32_32x32x16_f16 v[48:63], a[244:247], v[172:175], v[48:63]
	ds_read_b128 v[172:175], v192 offset:3072
	global_load_lds_dwordx4 v192, s[44:45] offset:3072 sc1
	s_waitcnt lgkmcnt(4)
	v_mfma_f32_32x32x16_f16 v[32:47], a[248:251], v[176:179], v[32:47]
	ds_read_b128 v[176:179], v192 offset:4096
	v_mfma_f32_32x32x16_f16 v[48:63], a[248:251], v[180:183], v[48:63]
	ds_read_b128 v[180:183], v192 offset:5120
	v_mfma_f32_32x32x16_f16 v[32:47], a[252:255], v[184:187], v[32:47]
	ds_read_b128 v[184:187], v192 offset:6144
	v_mfma_f32_32x32x16_f16 v[48:63], a[252:255], v[188:191], v[48:63]
	ds_read_b128 v[188:191], v192 offset:7168
	s_add_u32 s44, s34, 0x10000
	s_addc_u32 s45, s35, 0
	s_mov_b32 m0, s56
	s_nop 0
	global_load_lds_dwordx4 v192, s[44:45] sc1
	s_and_b32 s64, s33, 1
	s_lshl_b32 s64, s64, 22
	s_add_u32 s64, s64, s50
	s_add_u32 s64, s64, 0x20000
	s_add_u32 s36, s6, s64
	s_addc_u32 s37, s7, 0
	s_lshl_b32 s64, s33, 3
	s_add_u32 s64, s64, s29
	s_lshl_b32 s64, s64, 5
	s_add_u32 s64, s64, s30
	s_lshl_b32 s64, s64, 2
	s_add_u32 s40, s8, s64
	s_addc_u32 s41, s9, 0
	s_lshl_b32 s64, s61, 11
	s_lshl_b32 s65, s29, 8
	s_add_u32 s64, s64, s65
	s_lshl_b32 s64, s64, 3
	s_add_u32 s42, s12, s64
	s_addc_u32 s43, s13, 0
	s_nop 3
	global_load_dwordx2 v[228:229], v249, s[42:43] offset:0
	global_load_dwordx2 v[230:231], v249, s[42:43] offset:256
	s_waitcnt lgkmcnt(4)
	v_mfma_f32_32x32x16_f16 v[64:79], a[0:3], v[160:163], v[64:79]
	ds_read_b128 v[160:163], v192 offset:8192
	v_exp_f32_e32 v200, v32
	v_mfma_f32_32x32x16_f16 v[80:95], a[0:3], v[164:167], v[80:95]
	ds_read_b128 v[164:167], v192 offset:9216
	v_exp_f32_e32 v201, v33
	v_add_f32_e32 v200, 1.0, v200
	v_mfma_f32_32x32x16_f16 v[64:79], a[4:7], v[168:171], v[64:79]
	ds_read_b128 v[168:171], v192 offset:10240
	v_exp_f32_e32 v202, v34
	v_add_f32_e32 v201, 1.0, v201
	v_mfma_f32_32x32x16_f16 v[80:95], a[4:7], v[172:175], v[80:95]
	ds_read_b128 v[172:175], v192 offset:11264
	global_load_lds_dwordx4 v192, s[44:45] offset:1024 sc1
	v_exp_f32_e32 v203, v35
	v_add_f32_e32 v202, 1.0, v202
	s_waitcnt lgkmcnt(4)
	v_mfma_f32_32x32x16_f16 v[64:79], a[8:11], v[176:179], v[64:79]
	ds_read_b128 v[176:179], v192 offset:12288
	v_exp_f32_e32 v204, v36
	v_add_f32_e32 v203, 1.0, v203
	v_mfma_f32_32x32x16_f16 v[80:95], a[8:11], v[180:183], v[80:95]
	ds_read_b128 v[180:183], v192 offset:13312
	v_exp_f32_e32 v205, v37
	v_add_f32_e32 v204, 1.0, v204
	v_mfma_f32_32x32x16_f16 v[64:79], a[12:15], v[184:187], v[64:79]
	ds_read_b128 v[184:187], v192 offset:14336
	v_exp_f32_e32 v206, v38
	v_add_f32_e32 v205, 1.0, v205
	v_mfma_f32_32x32x16_f16 v[80:95], a[12:15], v[188:191], v[80:95]
	ds_read_b128 v[188:191], v192 offset:15360
	global_load_lds_dwordx4 v192, s[44:45] offset:2048 sc1
	v_exp_f32_e32 v207, v39
	v_add_f32_e32 v206, 1.0, v206
	s_waitcnt lgkmcnt(4)
	v_mfma_f32_32x32x16_f16 v[64:79], a[16:19], v[160:163], v[64:79]
	ds_read_b128 v[160:163], v192 offset:16384
	v_exp_f32_e32 v208, v40
	v_add_f32_e32 v207, 1.0, v207
	v_mfma_f32_32x32x16_f16 v[80:95], a[16:19], v[164:167], v[80:95]
	ds_read_b128 v[164:167], v192 offset:17408
	v_exp_f32_e32 v209, v41
	v_add_f32_e32 v208, 1.0, v208
	v_mfma_f32_32x32x16_f16 v[64:79], a[20:23], v[168:171], v[64:79]
	ds_read_b128 v[168:171], v192 offset:18432
	v_exp_f32_e32 v210, v42
	v_add_f32_e32 v209, 1.0, v209
	v_mfma_f32_32x32x16_f16 v[80:95], a[20:23], v[172:175], v[80:95]
	ds_read_b128 v[172:175], v192 offset:19456
	global_load_lds_dwordx4 v192, s[44:45] offset:3072 sc1
	v_exp_f32_e32 v211, v43
	v_add_f32_e32 v210, 1.0, v210
	s_waitcnt lgkmcnt(4)
	v_mfma_f32_32x32x16_f16 v[64:79], a[24:27], v[176:179], v[64:79]
	ds_read_b128 v[176:179], v192 offset:20480
	v_exp_f32_e32 v212, v44
	v_add_f32_e32 v211, 1.0, v211
	v_mfma_f32_32x32x16_f16 v[80:95], a[24:27], v[180:183], v[80:95]
	ds_read_b128 v[180:183], v192 offset:21504
	v_exp_f32_e32 v213, v45
	v_add_f32_e32 v212, 1.0, v212
	v_mfma_f32_32x32x16_f16 v[64:79], a[28:31], v[184:187], v[64:79]
	ds_read_b128 v[184:187], v192 offset:22528
	v_exp_f32_e32 v214, v46
	v_add_f32_e32 v213, 1.0, v213
	v_mfma_f32_32x32x16_f16 v[80:95], a[28:31], v[188:191], v[80:95]
	ds_read_b128 v[188:191], v192 offset:23552
	s_add_u32 s44, s34, 0x11000
	s_addc_u32 s45, s35, 0
	s_mov_b32 m0, s57
	s_nop 0
	global_load_lds_dwordx4 v192, s[44:45] sc1
	v_exp_f32_e32 v215, v47
	v_add_f32_e32 v214, 1.0, v214
	s_waitcnt lgkmcnt(4)
	v_mfma_f32_32x32x16_f16 v[64:79], a[32:35], v[160:163], v[64:79]
	ds_read_b128 v[160:163], v192 offset:24576
	v_add_f32_e32 v215, 1.0, v215
	v_rcp_f32_e32 v200, v200
	v_mfma_f32_32x32x16_f16 v[80:95], a[32:35], v[164:167], v[80:95]
	ds_read_b128 v[164:167], v192 offset:25600
	v_rcp_f32_e32 v201, v201
	v_mfma_f32_32x32x16_f16 v[64:79], a[36:39], v[168:171], v[64:79]
	ds_read_b128 v[168:171], v192 offset:26624
	v_rcp_f32_e32 v202, v202
	v_mfma_f32_32x32x16_f16 v[80:95], a[36:39], v[172:175], v[80:95]
	ds_read_b128 v[172:175], v192 offset:27648
	global_load_lds_dwordx4 v192, s[44:45] offset:1024 sc1
	v_rcp_f32_e32 v203, v203
	s_waitcnt lgkmcnt(4)
	v_mfma_f32_32x32x16_f16 v[64:79], a[40:43], v[176:179], v[64:79]
	ds_read_b128 v[176:179], v192 offset:28672
	v_rcp_f32_e32 v204, v204
	v_mfma_f32_32x32x16_f16 v[80:95], a[40:43], v[180:183], v[80:95]
	ds_read_b128 v[180:183], v192 offset:29696
	v_rcp_f32_e32 v205, v205
	v_mul_f32_e32 v204, v204, v136
	v_mfma_f32_32x32x16_f16 v[64:79], a[44:47], v[184:187], v[64:79]
	ds_read_b128 v[184:187], v192 offset:30720
	v_rcp_f32_e32 v206, v206
	v_mul_f32_e32 v205, v205, v137
	v_mfma_f32_32x32x16_f16 v[80:95], a[44:47], v[188:191], v[80:95]
	ds_read_b128 v[188:191], v192 offset:31744
	global_load_lds_dwordx4 v192, s[44:45] offset:2048 sc1
	v_rcp_f32_e32 v207, v207
	v_mul_f32_e32 v206, v206, v138
	s_waitcnt vmcnt(9)
	s_barrier
	s_waitcnt lgkmcnt(4)
	v_mfma_f32_32x32x16_f16 v[64:79], a[48:51], v[160:163], v[64:79]
	ds_read_b128 v[160:163], v192 offset:32768
	v_rcp_f32_e32 v208, v208
	v_mul_f32_e32 v207, v207, v139
	ds_read_b128 v[236:239], v248 offset:0
	ds_read_b64 v[240:241], v248 offset:32
	ds_read_b128 v[242:245], v248 offset:16
	ds_read_b64 v[246:247], v248 offset:40
	v_mfma_f32_32x32x16_f16 v[80:95], a[48:51], v[164:167], v[80:95]
	ds_read_b128 v[164:167], v192 offset:33792
	v_rcp_f32_e32 v209, v209
	v_fmamk_f32 v208, v208, 0xc0b8aa3b, v198
	s_waitcnt lgkmcnt(3)
	s_waitcnt vmcnt(6)
	v_fma_f32 v0, v229, v237, v240
	v_mfma_f32_32x32x16_f16 v[64:79], a[52:55], v[168:171], v[64:79]
	ds_read_b128 v[168:171], v192 offset:34816
	v_rcp_f32_e32 v210, v210
	v_fmamk_f32 v209, v209, 0xc0b8aa3b, v198
	v_fma_f32 v136, v200, v208, v204
	v_fma_f32 v1, v229, v239, v241
	v_fmac_f32_e32 v0, v228, v236
	v_mfma_f32_32x32x16_f16 v[80:95], a[52:55], v[172:175], v[80:95]
	ds_read_b128 v[172:175], v192 offset:35840
	global_load_lds_dwordx4 v192, s[44:45] offset:3072 sc1
	v_rcp_f32_e32 v211, v211
	v_fmamk_f32 v210, v210, 0xc0b8aa3b, v198
	v_fma_f32 v137, v201, v209, v205
	v_fmac_f32_e32 v1, v228, v238
	v_fma_f32 v16, v231, v237, v240
	v_mfma_f32_32x32x16_f16 v[64:79], a[56:59], v[176:179], v[64:79]
	ds_read_b128 v[176:179], v192 offset:36864
	v_rcp_f32_e32 v212, v212
	v_fmamk_f32 v211, v211, 0xc0b8aa3b, v198
	v_fma_f32 v138, v202, v210, v206
	v_fma_f32 v17, v231, v239, v241
	v_fmac_f32_e32 v16, v230, v236
	v_mfma_f32_32x32x16_f16 v[80:95], a[56:59], v[180:183], v[80:95]
	ds_read_b128 v[180:183], v192 offset:37888
	v_rcp_f32_e32 v213, v213
	v_fma_f32 v139, v203, v211, v207
	v_fmac_f32_e32 v17, v230, v238
	ds_read_b128 v[236:239], v248 offset:48
	ds_read_b64 v[240:241], v248 offset:80
	v_mfma_f32_32x32x16_f16 v[64:79], a[60:63], v[184:187], v[64:79]
	ds_read_b128 v[184:187], v192 offset:38912
	v_rcp_f32_e32 v214, v214
	s_waitcnt lgkmcnt(8)
	v_fma_f32 v2, v229, v243, v246
	v_mfma_f32_32x32x16_f16 v[80:95], a[60:63], v[188:191], v[80:95]
	ds_read_b128 v[188:191], v192 offset:39936
	s_add_u32 s44, s34, 0x18000
	s_addc_u32 s45, s35, 0
	s_mov_b32 m0, s58
	s_nop 0
	global_load_lds_dwordx4 v192, s[44:45] sc1
	v_rcp_f32_e32 v215, v215
	v_fma_f32 v3, v229, v245, v247
	v_fmac_f32_e32 v2, v228, v242
	s_waitcnt lgkmcnt(6)
	v_mfma_f32_32x32x16_f16 v[64:79], a[64:67], v[160:163], v[64:79]
	ds_read_b128 v[160:163], v192 offset:40960
	v_exp_f32_e32 v200, v136
	v_fmac_f32_e32 v3, v228, v244
	v_fma_f32 v18, v231, v243, v246
	v_mfma_f32_32x32x16_f16 v[80:95], a[64:67], v[164:167], v[80:95]
	ds_read_b128 v[164:167], v192 offset:41984
	v_exp_f32_e32 v201, v137
	v_add_f32_e32 v200, 1.0, v200
	v_fma_f32 v19, v231, v245, v247
	v_fmac_f32_e32 v18, v230, v242
	v_mfma_f32_32x32x16_f16 v[64:79], a[68:71], v[168:171], v[64:79]
	ds_read_b128 v[168:171], v192 offset:43008
	v_exp_f32_e32 v202, v138
	v_add_f32_e32 v201, 1.0, v201
	v_fmac_f32_e32 v19, v230, v244
	ds_read_b128 v[242:245], v248 offset:64
	ds_read_b64 v[246:247], v248 offset:88
	v_mfma_f32_32x32x16_f16 v[80:95], a[68:71], v[172:175], v[80:95]
	ds_read_b128 v[172:175], v192 offset:44032
	global_load_lds_dwordx4 v192, s[44:45] offset:1024 sc1
	v_exp_f32_e32 v203, v139
	v_add_f32_e32 v202, 1.0, v202
	s_waitcnt lgkmcnt(8)
	v_fma_f32 v4, v229, v237, v240
	s_waitcnt lgkmcnt(6)
	v_mfma_f32_32x32x16_f16 v[64:79], a[72:75], v[176:179], v[64:79]
	ds_read_b128 v[176:179], v192 offset:45056
	v_add_f32_e32 v203, 1.0, v203
	v_rcp_f32_e32 v200, v200
	v_fma_f32 v5, v229, v239, v241
	v_fmac_f32_e32 v4, v228, v236
	v_mfma_f32_32x32x16_f16 v[80:95], a[72:75], v[180:183], v[80:95]
	ds_read_b128 v[180:183], v192 offset:46080
	v_rcp_f32_e32 v201, v201
	v_fma_f32 v200, v200, 2.0, -1.0
	v_fmac_f32_e32 v5, v228, v238
	v_fma_f32 v20, v231, v237, v240
	v_mfma_f32_32x32x16_f16 v[64:79], a[76:79], v[184:187], v[64:79]
	ds_read_b128 v[184:187], v192 offset:47104
	v_rcp_f32_e32 v202, v202
	v_fma_f32 v201, v201, 2.0, -1.0
	v_mul_f32_e32 v216, v212, v200
	v_fma_f32 v21, v231, v239, v241
	v_fmac_f32_e32 v20, v230, v236
	v_mfma_f32_32x32x16_f16 v[80:95], a[76:79], v[188:191], v[80:95]
	ds_read_b128 v[188:191], v192 offset:48128
	global_load_lds_dwordx4 v192, s[44:45] offset:2048 sc1
	v_rcp_f32_e32 v203, v203
	v_fma_f32 v202, v202, 2.0, -1.0
	v_mul_f32_e32 v217, v213, v201
	v_fmac_f32_e32 v21, v230, v238
	ds_read_b128 v[236:239], v248 offset:96
	ds_read_b64 v[240:241], v248 offset:128
	s_waitcnt lgkmcnt(6)
	v_mfma_f32_32x32x16_f16 v[64:79], a[80:83], v[160:163], v[64:79]
	ds_read_b128 v[160:163], v192 offset:49152
	v_fma_f32 v203, v203, 2.0, -1.0
	v_mul_f32_e32 v218, v214, v202
	v_exp_f32_e32 v200, v48
	v_fma_f32 v6, v229, v243, v246
	v_mfma_f32_32x32x16_f16 v[80:95], a[80:83], v[164:167], v[80:95]
	ds_read_b128 v[164:167], v192 offset:50176
	v_mul_f32_e32 v219, v215, v203
	v_cvt_pk_f16_f32 v220, v216, v217
	v_exp_f32_e32 v201, v49
	v_fma_f32 v7, v229, v245, v247
	v_fmac_f32_e32 v6, v228, v242
	v_mfma_f32_32x32x16_f16 v[64:79], a[84:87], v[168:171], v[64:79]
	ds_read_b128 v[168:171], v192 offset:51200
	v_cvt_pk_f16_f32 v221, v218, v219
	v_exp_f32_e32 v202, v50
	v_add_f32_e32 v200, 1.0, v200
	v_fmac_f32_e32 v7, v228, v244
	v_fma_f32 v22, v231, v243, v246
	v_mfma_f32_32x32x16_f16 v[80:95], a[84:87], v[172:175], v[80:95]
	ds_read_b128 v[172:175], v192 offset:52224
	global_load_lds_dwordx4 v192, s[44:45] offset:3072 sc1
	s_cmp_lg_u32 s33, s60
	s_cbranch_scc1 .LE_nht34
	s_add_u32 s46, s62, 0x40000
	s_addc_u32 s47, s63, 0
	global_store_dwordx4 v250, v[216:219], s[46:47]
	s_waitcnt vmcnt(0)
.LE_nht34:
	v_exp_f32_e32 v203, v51
	v_fma_f32 v23, v231, v245, v247
	v_fmac_f32_e32 v22, v230, v242
	s_waitcnt lgkmcnt(6)
	v_mfma_f32_32x32x16_f16 v[64:79], a[88:91], v[176:179], v[64:79]
	ds_read_b128 v[176:179], v192 offset:53248
	v_exp_f32_e32 v204, v52
	v_add_f32_e32 v201, 1.0, v201
	v_add_f32_e32 v202, 1.0, v202
	v_fmac_f32_e32 v23, v230, v244
	ds_read_b128 v[242:245], v248 offset:112
	ds_read_b64 v[246:247], v248 offset:136
	v_mfma_f32_32x32x16_f16 v[80:95], a[88:91], v[180:183], v[80:95]
	ds_read_b128 v[180:183], v192 offset:54272
	v_exp_f32_e32 v205, v53
	v_add_f32_e32 v203, 1.0, v203
	v_add_f32_e32 v204, 1.0, v204
	s_waitcnt lgkmcnt(8)
	v_fma_f32 v8, v229, v237, v240
	v_mfma_f32_32x32x16_f16 v[64:79], a[92:95], v[184:187], v[64:79]
	ds_read_b128 v[184:187], v192 offset:55296
	v_exp_f32_e32 v206, v54
	v_add_f32_e32 v205, 1.0, v205
	v_fma_f32 v9, v229, v239, v241
	v_fmac_f32_e32 v8, v228, v236
	v_mfma_f32_32x32x16_f16 v[80:95], a[92:95], v[188:191], v[80:95]
	ds_read_b128 v[188:191], v192 offset:56320
	s_add_u32 s44, s34, 0x19000
	s_addc_u32 s45, s35, 0
	s_mov_b32 m0, s59
	s_nop 0
	global_load_lds_dwordx4 v192, s[44:45] sc1
	s_lshl_b32 s64, s71, 3
	s_add_u32 s64, s64, s29
	s_lshl_b32 s64, s64, 7
	s_add_u32 s38, s8, s64
	s_addc_u32 s39, s9, 0
	global_load_dword v251, v196, s[38:39] sc1
	v_exp_f32_e32 v207, v55
	v_add_f32_e32 v206, 1.0, v206
	v_fmac_f32_e32 v9, v228, v238
	v_fma_f32 v24, v231, v237, v240
	s_waitcnt lgkmcnt(6)
	v_mfma_f32_32x32x16_f16 v[64:79], a[96:99], v[160:163], v[64:79]
	ds_read_b128 v[160:163], v192 offset:57344
	v_exp_f32_e32 v208, v56
	v_add_f32_e32 v207, 1.0, v207
	v_fma_f32 v25, v231, v239, v241
	v_fmac_f32_e32 v24, v230, v236
	v_mfma_f32_32x32x16_f16 v[80:95], a[96:99], v[164:167], v[80:95]
	ds_read_b128 v[164:167], v192 offset:58368
	v_exp_f32_e32 v209, v57
	v_add_f32_e32 v208, 1.0, v208
	v_fmac_f32_e32 v25, v230, v238
	ds_read_b128 v[236:239], v248 offset:144
	ds_read_b64 v[240:241], v248 offset:176
	v_mfma_f32_32x32x16_f16 v[64:79], a[100:103], v[168:171], v[64:79]
	ds_read_b128 v[168:171], v192 offset:59392
	v_exp_f32_e32 v210, v58
	v_add_f32_e32 v209, 1.0, v209
	s_waitcnt lgkmcnt(8)
	v_fma_f32 v10, v229, v243, v246
	v_mfma_f32_32x32x16_f16 v[80:95], a[100:103], v[172:175], v[80:95]
	ds_read_b128 v[172:175], v192 offset:60416
	global_load_lds_dwordx4 v192, s[44:45] offset:1024 sc1
	v_exp_f32_e32 v211, v59
	v_add_f32_e32 v210, 1.0, v210
	v_fma_f32 v11, v229, v245, v247
	v_fmac_f32_e32 v10, v228, v242
	s_waitcnt lgkmcnt(6)
	v_mfma_f32_32x32x16_f16 v[64:79], a[104:107], v[176:179], v[64:79]
	ds_read_b128 v[176:179], v192 offset:61440
	v_exp_f32_e32 v212, v60
	v_add_f32_e32 v211, 1.0, v211
	v_fmac_f32_e32 v11, v228, v244
	v_fma_f32 v26, v231, v243, v246
	v_mfma_f32_32x32x16_f16 v[80:95], a[104:107], v[180:183], v[80:95]
	ds_read_b128 v[180:183], v192 offset:62464
	v_exp_f32_e32 v213, v61
	v_add_f32_e32 v212, 1.0, v212
	v_fma_f32 v27, v231, v245, v247
	v_fmac_f32_e32 v26, v230, v242
	v_mfma_f32_32x32x16_f16 v[64:79], a[108:111], v[184:187], v[64:79]
	ds_read_b128 v[184:187], v192 offset:63488
	v_exp_f32_e32 v214, v62
	v_add_f32_e32 v213, 1.0, v213
	v_fmac_f32_e32 v27, v230, v244
	ds_read_b128 v[242:245], v248 offset:160
	ds_read_b64 v[246:247], v248 offset:184
	v_mfma_f32_32x32x16_f16 v[80:95], a[108:111], v[188:191], v[80:95]
	ds_read_b128 v[188:191], v192 offset:64512
	global_load_lds_dwordx4 v192, s[44:45] offset:2048 sc1
	v_exp_f32_e32 v215, v63
	v_add_f32_e32 v214, 1.0, v214
	s_waitcnt lgkmcnt(8)
	v_fma_f32 v12, v229, v237, v240
	s_waitcnt vmcnt(8)
	s_barrier
	s_waitcnt lgkmcnt(6)
	v_mfma_f32_32x32x16_f16 v[64:79], a[112:115], v[160:163], v[64:79]
	ds_read_b128 v[160:163], v193 offset:0
	v_add_f32_e32 v215, 1.0, v215
	v_rcp_f32_e32 v200, v200
	v_fma_f32 v13, v229, v239, v241
	v_fmac_f32_e32 v12, v228, v236
	v_mfma_f32_32x32x16_f16 v[80:95], a[112:115], v[164:167], v[80:95]
	ds_read_b128 v[164:167], v193 offset:1024
	v_rcp_f32_e32 v201, v201
	v_fmac_f32_e32 v13, v228, v238
	v_fma_f32 v28, v231, v237, v240
	v_mfma_f32_32x32x16_f16 v[64:79], a[116:119], v[168:171], v[64:79]
	ds_read_b128 v[168:171], v193 offset:2048
	v_rcp_f32_e32 v202, v202
	v_fma_f32 v29, v231, v239, v241
	v_fmac_f32_e32 v28, v230, v236
	v_mfma_f32_32x32x16_f16 v[80:95], a[116:119], v[172:175], v[80:95]
	ds_read_b128 v[172:175], v193 offset:3072
	global_load_lds_dwordx4 v192, s[44:45] offset:3072 sc1
	v_rcp_f32_e32 v203, v203
	v_fmac_f32_e32 v29, v230, v238
	s_waitcnt lgkmcnt(5)
	s_waitcnt lgkmcnt(4)
	v_mfma_f32_32x32x16_f16 v[64:79], a[120:123], v[176:179], v[64:79]
	ds_read_b128 v[176:179], v193 offset:4096
	v_rcp_f32_e32 v204, v204
	v_fma_f32 v14, v229, v243, v246
	v_fma_f32 v15, v229, v245, v247
	v_mfma_f32_32x32x16_f16 v[80:95], a[120:123], v[180:183], v[80:95]
	ds_read_b128 v[180:183], v193 offset:5120
	v_rcp_f32_e32 v205, v205
	v_mul_f32_e32 v204, v204, v140
	v_fmac_f32_e32 v14, v228, v242
	v_fmac_f32_e32 v15, v228, v244
	v_mfma_f32_32x32x16_f16 v[64:79], a[124:127], v[184:187], v[64:79]
	ds_read_b128 v[184:187], v193 offset:6144
	v_rcp_f32_e32 v206, v206
	v_mul_f32_e32 v205, v205, v141
	v_fma_f32 v30, v231, v243, v246
	v_fma_f32 v31, v231, v245, v247
	v_mfma_f32_32x32x16_f16 v[80:95], a[124:127], v[188:191], v[80:95]
	ds_read_b128 v[188:191], v193 offset:7168
	s_waitcnt vmcnt(3)
	v_cmp_gt_u32_e32 vcc, 4, v251
	s_cbranch_vccz .LE_tok35

.LE_tok35:
	s_and_b32 s64, s71, 1
	s_lshl_b32 s64, s64, 22
	s_add_u32 s64, s64, s49
	s_add_u32 s64, s64, 0x60000
	s_add_u32 s34, s6, s64
	s_addc_u32 s35, s7, 0
	s_add_u32 s44, s34, 0x0
	s_addc_u32 s45, s35, 0
	s_mov_b32 m0, s52
	s_nop 0
	global_load_lds_dwordx4 v192, s[44:45] sc1
	v_rcp_f32_e32 v207, v207
	v_mul_f32_e32 v206, v206, v142
	v_fmac_f32_e32 v30, v230, v242
	v_fmac_f32_e32 v31, v230, v244
	s_waitcnt lgkmcnt(4)
	v_mfma_f32_32x32x16_f16 v[64:79], a[128:131], v[160:163], v[64:79]
	ds_read_b128 v[160:163], v193 offset:8192
	v_rcp_f32_e32 v208, v208
	v_mul_f32_e32 v207, v207, v143
	v_mfma_f32_32x32x16_f16 v[80:95], a[128:131], v[164:167], v[80:95]
	ds_read_b128 v[164:167], v193 offset:9216
	v_rcp_f32_e32 v209, v209
	v_fmamk_f32 v208, v208, 0xc0b8aa3b, v198
	v_mfma_f32_32x32x16_f16 v[64:79], a[132:135], v[168:171], v[64:79]
	ds_read_b128 v[168:171], v193 offset:10240
	v_rcp_f32_e32 v210, v210
	v_fmamk_f32 v209, v209, 0xc0b8aa3b, v198
	v_fma_f32 v140, v200, v208, v204
	v_mfma_f32_32x32x16_f16 v[80:95], a[132:135], v[172:175], v[80:95]
	ds_read_b128 v[172:175], v193 offset:11264
	global_load_lds_dwordx4 v192, s[44:45] offset:1024 sc1
	v_rcp_f32_e32 v211, v211
	v_fmamk_f32 v210, v210, 0xc0b8aa3b, v198
	v_fma_f32 v141, v201, v209, v205
	s_waitcnt lgkmcnt(4)
	v_mfma_f32_32x32x16_f16 v[64:79], a[136:139], v[176:179], v[64:79]
	ds_read_b128 v[176:179], v193 offset:12288
	v_rcp_f32_e32 v212, v212
	v_fmamk_f32 v211, v211, 0xc0b8aa3b, v198
	v_fma_f32 v142, v202, v210, v206
	v_mfma_f32_32x32x16_f16 v[80:95], a[136:139], v[180:183], v[80:95]
	ds_read_b128 v[180:183], v193 offset:13312
	v_rcp_f32_e32 v213, v213
	v_fma_f32 v143, v203, v211, v207
	v_mfma_f32_32x32x16_f16 v[64:79], a[140:143], v[184:187], v[64:79]
	ds_read_b128 v[184:187], v193 offset:14336
	v_rcp_f32_e32 v214, v214
	v_mfma_f32_32x32x16_f16 v[80:95], a[140:143], v[188:191], v[80:95]
	ds_read_b128 v[188:191], v193 offset:15360
	global_load_lds_dwordx4 v192, s[44:45] offset:2048 sc1
	v_rcp_f32_e32 v215, v215
	s_waitcnt lgkmcnt(4)
	v_mfma_f32_32x32x16_f16 v[64:79], a[144:147], v[160:163], v[64:79]
	ds_read_b128 v[160:163], v193 offset:16384
	v_exp_f32_e32 v200, v140
	v_mfma_f32_32x32x16_f16 v[80:95], a[144:147], v[164:167], v[80:95]
	ds_read_b128 v[164:167], v193 offset:17408
	v_exp_f32_e32 v201, v141
	v_add_f32_e32 v200, 1.0, v200
	v_mfma_f32_32x32x16_f16 v[64:79], a[148:151], v[168:171], v[64:79]
	ds_read_b128 v[168:171], v193 offset:18432
	v_exp_f32_e32 v202, v142
	v_add_f32_e32 v201, 1.0, v201
	v_mfma_f32_32x32x16_f16 v[80:95], a[148:151], v[172:175], v[80:95]
	ds_read_b128 v[172:175], v193 offset:19456
	global_load_lds_dwordx4 v192, s[44:45] offset:3072 sc1
	v_exp_f32_e32 v203, v143
	v_add_f32_e32 v202, 1.0, v202
	s_waitcnt lgkmcnt(4)
	v_mfma_f32_32x32x16_f16 v[64:79], a[152:155], v[176:179], v[64:79]
	ds_read_b128 v[176:179], v193 offset:20480
	v_add_f32_e32 v203, 1.0, v203
	v_rcp_f32_e32 v200, v200
	v_mfma_f32_32x32x16_f16 v[80:95], a[152:155], v[180:183], v[80:95]
	ds_read_b128 v[180:183], v193 offset:21504
	v_rcp_f32_e32 v201, v201
	v_fma_f32 v200, v200, 2.0, -1.0
	v_mfma_f32_32x32x16_f16 v[64:79], a[156:159], v[184:187], v[64:79]
	ds_read_b128 v[184:187], v193 offset:22528
	v_rcp_f32_e32 v202, v202
	v_fma_f32 v201, v201, 2.0, -1.0
	v_mul_f32_e32 v216, v212, v200
	v_mfma_f32_32x32x16_f16 v[80:95], a[156:159], v[188:191], v[80:95]
	ds_read_b128 v[188:191], v193 offset:23552
	s_add_u32 s44, s34, 0x1000
	s_addc_u32 s45, s35, 0
	s_mov_b32 m0, s53
	s_nop 0
	global_load_lds_dwordx4 v192, s[44:45] sc1
	v_rcp_f32_e32 v203, v203
	v_fma_f32 v202, v202, 2.0, -1.0
	v_mul_f32_e32 v217, v213, v201
	s_waitcnt lgkmcnt(4)
	v_mfma_f32_32x32x16_f16 v[64:79], a[160:163], v[160:163], v[64:79]
	ds_read_b128 v[160:163], v193 offset:24576
	v_fma_f32 v203, v203, 2.0, -1.0
	v_mul_f32_e32 v218, v214, v202
	v_mfma_f32_32x32x16_f16 v[80:95], a[160:163], v[164:167], v[80:95]
	ds_read_b128 v[164:167], v193 offset:25600
	v_mul_f32_e32 v219, v215, v203
	v_cvt_pk_f16_f32 v222, v216, v217
	v_mfma_f32_32x32x16_f16 v[64:79], a[164:167], v[168:171], v[64:79]
	ds_read_b128 v[168:171], v193 offset:26624
	v_cvt_pk_f16_f32 v223, v218, v219
	v_mfma_f32_32x32x16_f16 v[80:95], a[164:167], v[172:175], v[80:95]
	ds_read_b128 v[172:175], v193 offset:27648
	global_load_lds_dwordx4 v192, s[44:45] offset:1024 sc1
	s_cmp_lg_u32 s33, s60
	s_cbranch_scc1 .LE_nht37
	s_add_u32 s46, s62, 0x60000
	s_addc_u32 s47, s63, 0
	global_store_dwordx4 v250, v[216:219], s[46:47]
	s_waitcnt vmcnt(0)
.LE_nht37:
	s_waitcnt lgkmcnt(4)
	v_mfma_f32_32x32x16_f16 v[64:79], a[168:171], v[176:179], v[64:79]
	ds_read_b128 v[176:179], v193 offset:28672
	s_nop 1
	v_permlane32_swap_b32_e32 v220, v222
	v_permlane32_swap_b32_e32 v221, v223
	s_cmp_eq_u32 s31, 0
	s_cbranch_scc1 .LE_slow38
	global_store_dwordx4 v195, v[220:223], s[36:37] offset:0
	s_branch .LE_join39

.LE_join39:
	v_mfma_f32_32x32x16_f16 v[80:95], a[168:171], v[180:183], v[80:95]
	ds_read_b128 v[180:183], v193 offset:29696
	v_mfma_f32_32x32x16_f16 v[64:79], a[172:175], v[184:187], v[64:79]
	ds_read_b128 v[184:187], v193 offset:30720
	v_mfma_f32_32x32x16_f16 v[80:95], a[172:175], v[188:191], v[80:95]
	ds_read_b128 v[188:191], v193 offset:31744
	global_load_lds_dwordx4 v192, s[44:45] offset:2048 sc1
	s_waitcnt vmcnt(8)
	s_barrier
	s_waitcnt lgkmcnt(4)
	v_mfma_f32_32x32x16_f16 v[64:79], a[176:179], v[160:163], v[64:79]
	ds_read_b128 v[160:163], v193 offset:32768
	v_mfma_f32_32x32x16_f16 v[80:95], a[176:179], v[164:167], v[80:95]
	ds_read_b128 v[164:167], v193 offset:33792
	v_mfma_f32_32x32x16_f16 v[64:79], a[180:183], v[168:171], v[64:79]
	ds_read_b128 v[168:171], v193 offset:34816
	v_mfma_f32_32x32x16_f16 v[80:95], a[180:183], v[172:175], v[80:95]
	ds_read_b128 v[172:175], v193 offset:35840
	global_load_lds_dwordx4 v192, s[44:45] offset:3072 sc1
	s_waitcnt lgkmcnt(4)
	v_mfma_f32_32x32x16_f16 v[64:79], a[184:187], v[176:179], v[64:79]
	ds_read_b128 v[176:179], v193 offset:36864
	v_mfma_f32_32x32x16_f16 v[80:95], a[184:187], v[180:183], v[80:95]
	ds_read_b128 v[180:183], v193 offset:37888
	v_mfma_f32_32x32x16_f16 v[64:79], a[188:191], v[184:187], v[64:79]
	ds_read_b128 v[184:187], v193 offset:38912
	v_mfma_f32_32x32x16_f16 v[80:95], a[188:191], v[188:191], v[80:95]
	ds_read_b128 v[188:191], v193 offset:39936
	s_add_u32 s44, s34, 0x8000
	s_addc_u32 s45, s35, 0
	s_mov_b32 m0, s54
	s_nop 0
	global_load_lds_dwordx4 v192, s[44:45] sc1
	s_waitcnt lgkmcnt(4)
	v_mfma_f32_32x32x16_f16 v[64:79], a[192:195], v[160:163], v[64:79]
	ds_read_b128 v[160:163], v193 offset:40960
	v_mfma_f32_32x32x16_f16 v[80:95], a[192:195], v[164:167], v[80:95]
	ds_read_b128 v[164:167], v193 offset:41984
	s_waitcnt vmcnt(3)
	s_barrier
	v_mov_b32_e32 v199, 2
	s_cmp_eq_u32 s31, 0
	s_cbranch_scc1 .LE_slow40
	global_store_dword v197, v199, s[40:41]
	s_branch .LE_join41

.LE_join41:
	v_mfma_f32_32x32x16_f16 v[64:79], a[196:199], v[168:171], v[64:79]
	ds_read_b128 v[168:171], v193 offset:43008
	v_mfma_f32_32x32x16_f16 v[80:95], a[196:199], v[172:175], v[80:95]
	ds_read_b128 v[172:175], v193 offset:44032
	global_load_lds_dwordx4 v192, s[44:45] offset:1024 sc1
	s_waitcnt lgkmcnt(4)
	v_mfma_f32_32x32x16_f16 v[64:79], a[200:203], v[176:179], v[64:79]
	ds_read_b128 v[176:179], v193 offset:45056
	v_mfma_f32_32x32x16_f16 v[80:95], a[200:203], v[180:183], v[80:95]
	ds_read_b128 v[180:183], v193 offset:46080
	v_mfma_f32_32x32x16_f16 v[64:79], a[204:207], v[184:187], v[64:79]
	ds_read_b128 v[184:187], v193 offset:47104
	v_mfma_f32_32x32x16_f16 v[80:95], a[204:207], v[188:191], v[80:95]
	ds_read_b128 v[188:191], v193 offset:48128
	global_load_lds_dwordx4 v192, s[44:45] offset:2048 sc1
	s_waitcnt lgkmcnt(4)
	v_mfma_f32_32x32x16_f16 v[64:79], a[208:211], v[160:163], v[64:79]
	ds_read_b128 v[160:163], v193 offset:49152
	v_mfma_f32_32x32x16_f16 v[80:95], a[208:211], v[164:167], v[80:95]
	ds_read_b128 v[164:167], v193 offset:50176
	v_mfma_f32_32x32x16_f16 v[64:79], a[212:215], v[168:171], v[64:79]
	ds_read_b128 v[168:171], v193 offset:51200
	v_mfma_f32_32x32x16_f16 v[80:95], a[212:215], v[172:175], v[80:95]
	ds_read_b128 v[172:175], v193 offset:52224
	global_load_lds_dwordx4 v192, s[44:45] offset:3072 sc1
	s_waitcnt lgkmcnt(4)
	v_mfma_f32_32x32x16_f16 v[64:79], a[216:219], v[176:179], v[64:79]
	ds_read_b128 v[176:179], v193 offset:53248
	v_mfma_f32_32x32x16_f16 v[80:95], a[216:219], v[180:183], v[80:95]
	ds_read_b128 v[180:183], v193 offset:54272
	v_mfma_f32_32x32x16_f16 v[64:79], a[220:223], v[184:187], v[64:79]
	ds_read_b128 v[184:187], v193 offset:55296
	v_mfma_f32_32x32x16_f16 v[80:95], a[220:223], v[188:191], v[80:95]
	ds_read_b128 v[188:191], v193 offset:56320
	s_add_u32 s44, s34, 0x9000
	s_addc_u32 s45, s35, 0
	s_mov_b32 m0, s55
	s_nop 0
	global_load_lds_dwordx4 v192, s[44:45] sc1
	s_waitcnt lgkmcnt(4)
	v_mfma_f32_32x32x16_f16 v[64:79], a[224:227], v[160:163], v[64:79]
	ds_read_b128 v[160:163], v193 offset:57344
	v_mfma_f32_32x32x16_f16 v[80:95], a[224:227], v[164:167], v[80:95]
	ds_read_b128 v[164:167], v193 offset:58368
	v_mfma_f32_32x32x16_f16 v[64:79], a[228:231], v[168:171], v[64:79]
	ds_read_b128 v[168:171], v193 offset:59392
	v_mfma_f32_32x32x16_f16 v[80:95], a[228:231], v[172:175], v[80:95]
	ds_read_b128 v[172:175], v193 offset:60416
	global_load_lds_dwordx4 v192, s[44:45] offset:1024 sc1
	s_waitcnt lgkmcnt(4)
	v_mfma_f32_32x32x16_f16 v[64:79], a[232:235], v[176:179], v[64:79]
	ds_read_b128 v[176:179], v193 offset:61440
	v_mfma_f32_32x32x16_f16 v[80:95], a[232:235], v[180:183], v[80:95]
	ds_read_b128 v[180:183], v193 offset:62464
	v_mfma_f32_32x32x16_f16 v[64:79], a[236:239], v[184:187], v[64:79]
	ds_read_b128 v[184:187], v193 offset:63488
	v_mfma_f32_32x32x16_f16 v[80:95], a[236:239], v[188:191], v[80:95]
	ds_read_b128 v[188:191], v193 offset:64512
	global_load_lds_dwordx4 v192, s[44:45] offset:2048 sc1
	s_waitcnt vmcnt(8)
	s_barrier
	s_waitcnt lgkmcnt(4)
	v_mfma_f32_32x32x16_f16 v[64:79], a[240:243], v[160:163], v[64:79]
	ds_read_b128 v[160:163], v192 offset:0
	v_mfma_f32_32x32x16_f16 v[80:95], a[240:243], v[164:167], v[80:95]
	ds_read_b128 v[164:167], v192 offset:1024
	v_mfma_f32_32x32x16_f16 v[64:79], a[244:247], v[168:171], v[64:79]
	ds_read_b128 v[168:171], v192 offset:2048
	v_mfma_f32_32x32x16_f16 v[80:95], a[244:247], v[172:175], v[80:95]
	ds_read_b128 v[172:175], v192 offset:3072
	global_load_lds_dwordx4 v192, s[44:45] offset:3072 sc1
	s_waitcnt lgkmcnt(4)
	v_mfma_f32_32x32x16_f16 v[64:79], a[248:251], v[176:179], v[64:79]
	ds_read_b128 v[176:179], v192 offset:4096
	v_mfma_f32_32x32x16_f16 v[80:95], a[248:251], v[180:183], v[80:95]
	ds_read_b128 v[180:183], v192 offset:5120
	v_mfma_f32_32x32x16_f16 v[64:79], a[252:255], v[184:187], v[64:79]
	ds_read_b128 v[184:187], v192 offset:6144
	v_mfma_f32_32x32x16_f16 v[80:95], a[252:255], v[188:191], v[80:95]
	ds_read_b128 v[188:191], v192 offset:7168
	s_add_u32 s44, s34, 0x10000
	s_addc_u32 s45, s35, 0
	s_mov_b32 m0, s56
	s_nop 0
	global_load_lds_dwordx4 v192, s[44:45] sc1
	s_and_b32 s64, s33, 1
	s_lshl_b32 s64, s64, 22
	s_add_u32 s64, s64, s50
	s_add_u32 s64, s64, 0x40000
	s_add_u32 s36, s6, s64
	s_addc_u32 s37, s7, 0
	s_lshl_b32 s64, s33, 3
	s_add_u32 s64, s64, s29
	s_lshl_b32 s64, s64, 5
	s_add_u32 s64, s64, s30
	s_lshl_b32 s64, s64, 2
	s_add_u32 s40, s8, s64
	s_addc_u32 s41, s9, 0
	s_lshl_b32 s64, s61, 11
	s_lshl_b32 s65, s29, 8
	s_add_u32 s64, s64, s65
	s_add_u32 s64, s64, 64
	s_lshl_b32 s64, s64, 3
	s_add_u32 s42, s12, s64
	s_addc_u32 s43, s13, 0
	s_nop 3
	global_load_dwordx2 v[228:229], v249, s[42:43] offset:0
	global_load_dwordx2 v[230:231], v249, s[42:43] offset:256
	s_waitcnt lgkmcnt(4)
	v_mfma_f32_32x32x16_f16 v[96:111], a[0:3], v[160:163], v[96:111]
	ds_read_b128 v[160:163], v192 offset:8192
	v_exp_f32_e32 v200, v64
	v_mfma_f32_32x32x16_f16 v[112:127], a[0:3], v[164:167], v[112:127]
	ds_read_b128 v[164:167], v192 offset:9216
	v_exp_f32_e32 v201, v65
	v_add_f32_e32 v200, 1.0, v200
	v_mfma_f32_32x32x16_f16 v[96:111], a[4:7], v[168:171], v[96:111]
	ds_read_b128 v[168:171], v192 offset:10240
	v_exp_f32_e32 v202, v66
	v_add_f32_e32 v201, 1.0, v201
	v_mfma_f32_32x32x16_f16 v[112:127], a[4:7], v[172:175], v[112:127]
	ds_read_b128 v[172:175], v192 offset:11264
	global_load_lds_dwordx4 v192, s[44:45] offset:1024 sc1
	v_exp_f32_e32 v203, v67
	v_add_f32_e32 v202, 1.0, v202
	s_waitcnt lgkmcnt(4)
	v_mfma_f32_32x32x16_f16 v[96:111], a[8:11], v[176:179], v[96:111]
	ds_read_b128 v[176:179], v192 offset:12288
	v_exp_f32_e32 v204, v68
	v_add_f32_e32 v203, 1.0, v203
	v_mfma_f32_32x32x16_f16 v[112:127], a[8:11], v[180:183], v[112:127]
	ds_read_b128 v[180:183], v192 offset:13312
	v_exp_f32_e32 v205, v69
	v_add_f32_e32 v204, 1.0, v204
	v_mfma_f32_32x32x16_f16 v[96:111], a[12:15], v[184:187], v[96:111]
	ds_read_b128 v[184:187], v192 offset:14336
	v_exp_f32_e32 v206, v70
	v_add_f32_e32 v205, 1.0, v205
	v_mfma_f32_32x32x16_f16 v[112:127], a[12:15], v[188:191], v[112:127]
	ds_read_b128 v[188:191], v192 offset:15360
	global_load_lds_dwordx4 v192, s[44:45] offset:2048 sc1
	v_exp_f32_e32 v207, v71
	v_add_f32_e32 v206, 1.0, v206
	s_waitcnt lgkmcnt(4)
	v_mfma_f32_32x32x16_f16 v[96:111], a[16:19], v[160:163], v[96:111]
	ds_read_b128 v[160:163], v192 offset:16384
	v_exp_f32_e32 v208, v72
	v_add_f32_e32 v207, 1.0, v207
	v_mfma_f32_32x32x16_f16 v[112:127], a[16:19], v[164:167], v[112:127]
	ds_read_b128 v[164:167], v192 offset:17408
	v_exp_f32_e32 v209, v73
	v_add_f32_e32 v208, 1.0, v208
	v_mfma_f32_32x32x16_f16 v[96:111], a[20:23], v[168:171], v[96:111]
	ds_read_b128 v[168:171], v192 offset:18432
	v_exp_f32_e32 v210, v74
	v_add_f32_e32 v209, 1.0, v209
	v_mfma_f32_32x32x16_f16 v[112:127], a[20:23], v[172:175], v[112:127]
	ds_read_b128 v[172:175], v192 offset:19456
	global_load_lds_dwordx4 v192, s[44:45] offset:3072 sc1
	v_exp_f32_e32 v211, v75
	v_add_f32_e32 v210, 1.0, v210
	s_waitcnt lgkmcnt(4)
	v_mfma_f32_32x32x16_f16 v[96:111], a[24:27], v[176:179], v[96:111]
	ds_read_b128 v[176:179], v192 offset:20480
	v_exp_f32_e32 v212, v76
	v_add_f32_e32 v211, 1.0, v211
	v_mfma_f32_32x32x16_f16 v[112:127], a[24:27], v[180:183], v[112:127]
	ds_read_b128 v[180:183], v192 offset:21504
	v_exp_f32_e32 v213, v77
	v_add_f32_e32 v212, 1.0, v212
	v_mfma_f32_32x32x16_f16 v[96:111], a[28:31], v[184:187], v[96:111]
	ds_read_b128 v[184:187], v192 offset:22528
	v_exp_f32_e32 v214, v78
	v_add_f32_e32 v213, 1.0, v213
	v_mfma_f32_32x32x16_f16 v[112:127], a[28:31], v[188:191], v[112:127]
	ds_read_b128 v[188:191], v192 offset:23552
	s_add_u32 s44, s34, 0x11000
	s_addc_u32 s45, s35, 0
	s_mov_b32 m0, s57
	s_nop 0
	global_load_lds_dwordx4 v192, s[44:45] sc1
	v_exp_f32_e32 v215, v79
	v_add_f32_e32 v214, 1.0, v214
	s_waitcnt lgkmcnt(4)
	v_mfma_f32_32x32x16_f16 v[96:111], a[32:35], v[160:163], v[96:111]
	ds_read_b128 v[160:163], v192 offset:24576
	v_add_f32_e32 v215, 1.0, v215
	v_rcp_f32_e32 v200, v200
	v_mfma_f32_32x32x16_f16 v[112:127], a[32:35], v[164:167], v[112:127]
	ds_read_b128 v[164:167], v192 offset:25600
	v_rcp_f32_e32 v201, v201
	v_mfma_f32_32x32x16_f16 v[96:111], a[36:39], v[168:171], v[96:111]
	ds_read_b128 v[168:171], v192 offset:26624
	v_rcp_f32_e32 v202, v202
	v_mfma_f32_32x32x16_f16 v[112:127], a[36:39], v[172:175], v[112:127]
	ds_read_b128 v[172:175], v192 offset:27648
	global_load_lds_dwordx4 v192, s[44:45] offset:1024 sc1
	v_rcp_f32_e32 v203, v203
	s_waitcnt lgkmcnt(4)
	v_mfma_f32_32x32x16_f16 v[96:111], a[40:43], v[176:179], v[96:111]
	ds_read_b128 v[176:179], v192 offset:28672
	v_rcp_f32_e32 v204, v204
	v_mfma_f32_32x32x16_f16 v[112:127], a[40:43], v[180:183], v[112:127]
	ds_read_b128 v[180:183], v192 offset:29696
	v_rcp_f32_e32 v205, v205
	v_mul_f32_e32 v204, v204, v144
	v_mfma_f32_32x32x16_f16 v[96:111], a[44:47], v[184:187], v[96:111]
	ds_read_b128 v[184:187], v192 offset:30720
	v_rcp_f32_e32 v206, v206
	v_mul_f32_e32 v205, v205, v145
	v_mfma_f32_32x32x16_f16 v[112:127], a[44:47], v[188:191], v[112:127]
	ds_read_b128 v[188:191], v192 offset:31744
	global_load_lds_dwordx4 v192, s[44:45] offset:2048 sc1
	v_rcp_f32_e32 v207, v207
	v_mul_f32_e32 v206, v206, v146
	s_waitcnt vmcnt(9)
	s_barrier
	s_waitcnt lgkmcnt(4)
	v_mfma_f32_32x32x16_f16 v[96:111], a[48:51], v[160:163], v[96:111]
	ds_read_b128 v[160:163], v192 offset:32768
	v_rcp_f32_e32 v208, v208
	v_mul_f32_e32 v207, v207, v147
	ds_read_b128 v[236:239], v248 offset:0
	ds_read_b64 v[240:241], v248 offset:32
	ds_read_b128 v[242:245], v248 offset:16
	ds_read_b64 v[246:247], v248 offset:40
	v_mfma_f32_32x32x16_f16 v[112:127], a[48:51], v[164:167], v[112:127]
	ds_read_b128 v[164:167], v192 offset:33792
	v_rcp_f32_e32 v209, v209
	v_fmamk_f32 v208, v208, 0xc0b8aa3b, v198
	s_waitcnt lgkmcnt(3)
	s_waitcnt vmcnt(6)
	v_fma_f32 v32, v229, v237, v240
	v_mfma_f32_32x32x16_f16 v[96:111], a[52:55], v[168:171], v[96:111]
	ds_read_b128 v[168:171], v192 offset:34816
	v_rcp_f32_e32 v210, v210
	v_fmamk_f32 v209, v209, 0xc0b8aa3b, v198
	v_fma_f32 v144, v200, v208, v204
	v_fma_f32 v33, v229, v239, v241
	v_fmac_f32_e32 v32, v228, v236
	v_mfma_f32_32x32x16_f16 v[112:127], a[52:55], v[172:175], v[112:127]
	ds_read_b128 v[172:175], v192 offset:35840
	global_load_lds_dwordx4 v192, s[44:45] offset:3072 sc1
	v_rcp_f32_e32 v211, v211
	v_fmamk_f32 v210, v210, 0xc0b8aa3b, v198
	v_fma_f32 v145, v201, v209, v205
	v_fmac_f32_e32 v33, v228, v238
	v_fma_f32 v48, v231, v237, v240
	v_mfma_f32_32x32x16_f16 v[96:111], a[56:59], v[176:179], v[96:111]
	ds_read_b128 v[176:179], v192 offset:36864
	v_rcp_f32_e32 v212, v212
	v_fmamk_f32 v211, v211, 0xc0b8aa3b, v198
	v_fma_f32 v146, v202, v210, v206
	v_fma_f32 v49, v231, v239, v241
	v_fmac_f32_e32 v48, v230, v236
	v_mfma_f32_32x32x16_f16 v[112:127], a[56:59], v[180:183], v[112:127]
	ds_read_b128 v[180:183], v192 offset:37888
	v_rcp_f32_e32 v213, v213
	v_fma_f32 v147, v203, v211, v207
	v_fmac_f32_e32 v49, v230, v238
	ds_read_b128 v[236:239], v248 offset:48
	ds_read_b64 v[240:241], v248 offset:80
	v_mfma_f32_32x32x16_f16 v[96:111], a[60:63], v[184:187], v[96:111]
	ds_read_b128 v[184:187], v192 offset:38912
	v_rcp_f32_e32 v214, v214
	s_waitcnt lgkmcnt(8)
	v_fma_f32 v34, v229, v243, v246
	v_mfma_f32_32x32x16_f16 v[112:127], a[60:63], v[188:191], v[112:127]
	ds_read_b128 v[188:191], v192 offset:39936
	s_add_u32 s44, s34, 0x18000
	s_addc_u32 s45, s35, 0
	s_mov_b32 m0, s58
	s_nop 0
	global_load_lds_dwordx4 v192, s[44:45] sc1
	v_rcp_f32_e32 v215, v215
	v_fma_f32 v35, v229, v245, v247
	v_fmac_f32_e32 v34, v228, v242
	s_waitcnt lgkmcnt(6)
	v_mfma_f32_32x32x16_f16 v[96:111], a[64:67], v[160:163], v[96:111]
	ds_read_b128 v[160:163], v192 offset:40960
	v_exp_f32_e32 v200, v144
	v_fmac_f32_e32 v35, v228, v244
	v_fma_f32 v50, v231, v243, v246
	v_mfma_f32_32x32x16_f16 v[112:127], a[64:67], v[164:167], v[112:127]
	ds_read_b128 v[164:167], v192 offset:41984
	v_exp_f32_e32 v201, v145
	v_add_f32_e32 v200, 1.0, v200
	v_fma_f32 v51, v231, v245, v247
	v_fmac_f32_e32 v50, v230, v242
	v_mfma_f32_32x32x16_f16 v[96:111], a[68:71], v[168:171], v[96:111]
	ds_read_b128 v[168:171], v192 offset:43008
	v_exp_f32_e32 v202, v146
	v_add_f32_e32 v201, 1.0, v201
	v_fmac_f32_e32 v51, v230, v244
	ds_read_b128 v[242:245], v248 offset:64
	ds_read_b64 v[246:247], v248 offset:88
	v_mfma_f32_32x32x16_f16 v[112:127], a[68:71], v[172:175], v[112:127]
	ds_read_b128 v[172:175], v192 offset:44032
	global_load_lds_dwordx4 v192, s[44:45] offset:1024 sc1
	v_exp_f32_e32 v203, v147
	v_add_f32_e32 v202, 1.0, v202
	s_waitcnt lgkmcnt(8)
	v_fma_f32 v36, v229, v237, v240
	s_waitcnt lgkmcnt(6)
	v_mfma_f32_32x32x16_f16 v[96:111], a[72:75], v[176:179], v[96:111]
	ds_read_b128 v[176:179], v192 offset:45056
	v_add_f32_e32 v203, 1.0, v203
	v_rcp_f32_e32 v200, v200
	v_fma_f32 v37, v229, v239, v241
	v_fmac_f32_e32 v36, v228, v236
	v_mfma_f32_32x32x16_f16 v[112:127], a[72:75], v[180:183], v[112:127]
	ds_read_b128 v[180:183], v192 offset:46080
	v_rcp_f32_e32 v201, v201
	v_fma_f32 v200, v200, 2.0, -1.0
	v_fmac_f32_e32 v37, v228, v238
	v_fma_f32 v52, v231, v237, v240
	v_mfma_f32_32x32x16_f16 v[96:111], a[76:79], v[184:187], v[96:111]
	ds_read_b128 v[184:187], v192 offset:47104
	v_rcp_f32_e32 v202, v202
	v_fma_f32 v201, v201, 2.0, -1.0
	v_mul_f32_e32 v216, v212, v200
	v_fma_f32 v53, v231, v239, v241
	v_fmac_f32_e32 v52, v230, v236
	v_mfma_f32_32x32x16_f16 v[112:127], a[76:79], v[188:191], v[112:127]
	ds_read_b128 v[188:191], v192 offset:48128
	global_load_lds_dwordx4 v192, s[44:45] offset:2048 sc1
	v_rcp_f32_e32 v203, v203
	v_fma_f32 v202, v202, 2.0, -1.0
	v_mul_f32_e32 v217, v213, v201
	v_fmac_f32_e32 v53, v230, v238
	ds_read_b128 v[236:239], v248 offset:96
	ds_read_b64 v[240:241], v248 offset:128
	s_waitcnt lgkmcnt(6)
	v_mfma_f32_32x32x16_f16 v[96:111], a[80:83], v[160:163], v[96:111]
	ds_read_b128 v[160:163], v192 offset:49152
	v_fma_f32 v203, v203, 2.0, -1.0
	v_mul_f32_e32 v218, v214, v202
	v_exp_f32_e32 v200, v80
	v_fma_f32 v38, v229, v243, v246
	v_mfma_f32_32x32x16_f16 v[112:127], a[80:83], v[164:167], v[112:127]
	ds_read_b128 v[164:167], v192 offset:50176
	v_mul_f32_e32 v219, v215, v203
	v_cvt_pk_f16_f32 v220, v216, v217
	v_exp_f32_e32 v201, v81
	v_fma_f32 v39, v229, v245, v247
	v_fmac_f32_e32 v38, v228, v242
	v_mfma_f32_32x32x16_f16 v[96:111], a[84:87], v[168:171], v[96:111]
	ds_read_b128 v[168:171], v192 offset:51200
	v_cvt_pk_f16_f32 v221, v218, v219
	v_exp_f32_e32 v202, v82
	v_add_f32_e32 v200, 1.0, v200
	v_fmac_f32_e32 v39, v228, v244
	v_fma_f32 v54, v231, v243, v246
	v_mfma_f32_32x32x16_f16 v[112:127], a[84:87], v[172:175], v[112:127]
	ds_read_b128 v[172:175], v192 offset:52224
	global_load_lds_dwordx4 v192, s[44:45] offset:3072 sc1
	s_cmp_lg_u32 s33, s60
	s_cbranch_scc1 .LE_nht42
	s_add_u32 s46, s62, 0x80000
	s_addc_u32 s47, s63, 0
	global_store_dwordx4 v250, v[216:219], s[46:47]
	s_waitcnt vmcnt(0)
.LE_nht42:
	v_exp_f32_e32 v203, v83
	v_fma_f32 v55, v231, v245, v247
	v_fmac_f32_e32 v54, v230, v242
	s_waitcnt lgkmcnt(6)
	v_mfma_f32_32x32x16_f16 v[96:111], a[88:91], v[176:179], v[96:111]
	ds_read_b128 v[176:179], v192 offset:53248
	v_exp_f32_e32 v204, v84
	v_add_f32_e32 v201, 1.0, v201
	v_add_f32_e32 v202, 1.0, v202
	v_fmac_f32_e32 v55, v230, v244
	ds_read_b128 v[242:245], v248 offset:112
	ds_read_b64 v[246:247], v248 offset:136
	v_mfma_f32_32x32x16_f16 v[112:127], a[88:91], v[180:183], v[112:127]
	ds_read_b128 v[180:183], v192 offset:54272
	v_exp_f32_e32 v205, v85
	v_add_f32_e32 v203, 1.0, v203
	v_add_f32_e32 v204, 1.0, v204
	s_waitcnt lgkmcnt(8)
	v_fma_f32 v40, v229, v237, v240
	v_mfma_f32_32x32x16_f16 v[96:111], a[92:95], v[184:187], v[96:111]
	ds_read_b128 v[184:187], v192 offset:55296
	v_exp_f32_e32 v206, v86
	v_add_f32_e32 v205, 1.0, v205
	v_fma_f32 v41, v229, v239, v241
	v_fmac_f32_e32 v40, v228, v236
	v_mfma_f32_32x32x16_f16 v[112:127], a[92:95], v[188:191], v[112:127]
	ds_read_b128 v[188:191], v192 offset:56320
	s_add_u32 s44, s34, 0x19000
	s_addc_u32 s45, s35, 0
	s_mov_b32 m0, s59
	s_nop 0
	global_load_lds_dwordx4 v192, s[44:45] sc1
	s_lshl_b32 s64, s33, 3
	s_add_u32 s64, s64, s29
	s_lshl_b32 s64, s64, 7
	s_add_u32 s38, s8, s64
	s_addc_u32 s39, s9, 0
	global_load_dword v251, v196, s[38:39] sc1
	v_exp_f32_e32 v207, v87
	v_add_f32_e32 v206, 1.0, v206
	v_fmac_f32_e32 v41, v228, v238
	v_fma_f32 v56, v231, v237, v240
	s_waitcnt lgkmcnt(6)
	v_mfma_f32_32x32x16_f16 v[96:111], a[96:99], v[160:163], v[96:111]
	ds_read_b128 v[160:163], v192 offset:57344
	v_exp_f32_e32 v208, v88
	v_add_f32_e32 v207, 1.0, v207
	v_fma_f32 v57, v231, v239, v241
	v_fmac_f32_e32 v56, v230, v236
	v_mfma_f32_32x32x16_f16 v[112:127], a[96:99], v[164:167], v[112:127]
	ds_read_b128 v[164:167], v192 offset:58368
	v_exp_f32_e32 v209, v89
	v_add_f32_e32 v208, 1.0, v208
	v_fmac_f32_e32 v57, v230, v238
	ds_read_b128 v[236:239], v248 offset:144
	ds_read_b64 v[240:241], v248 offset:176
	v_mfma_f32_32x32x16_f16 v[96:111], a[100:103], v[168:171], v[96:111]
	ds_read_b128 v[168:171], v192 offset:59392
	v_exp_f32_e32 v210, v90
	v_add_f32_e32 v209, 1.0, v209
	s_waitcnt lgkmcnt(8)
	v_fma_f32 v42, v229, v243, v246
	v_mfma_f32_32x32x16_f16 v[112:127], a[100:103], v[172:175], v[112:127]
	ds_read_b128 v[172:175], v192 offset:60416
	global_load_lds_dwordx4 v192, s[44:45] offset:1024 sc1
	v_exp_f32_e32 v211, v91
	v_add_f32_e32 v210, 1.0, v210
	v_fma_f32 v43, v229, v245, v247
	v_fmac_f32_e32 v42, v228, v242
	s_waitcnt lgkmcnt(6)
	v_mfma_f32_32x32x16_f16 v[96:111], a[104:107], v[176:179], v[96:111]
	ds_read_b128 v[176:179], v192 offset:61440
	v_exp_f32_e32 v212, v92
	v_add_f32_e32 v211, 1.0, v211
	v_fmac_f32_e32 v43, v228, v244
	v_fma_f32 v58, v231, v243, v246
	v_mfma_f32_32x32x16_f16 v[112:127], a[104:107], v[180:183], v[112:127]
	ds_read_b128 v[180:183], v192 offset:62464
	v_exp_f32_e32 v213, v93
	v_add_f32_e32 v212, 1.0, v212
	v_fma_f32 v59, v231, v245, v247
	v_fmac_f32_e32 v58, v230, v242
	v_mfma_f32_32x32x16_f16 v[96:111], a[108:111], v[184:187], v[96:111]
	ds_read_b128 v[184:187], v192 offset:63488
	v_exp_f32_e32 v214, v94
	v_add_f32_e32 v213, 1.0, v213
	v_fmac_f32_e32 v59, v230, v244
	ds_read_b128 v[242:245], v248 offset:160
	ds_read_b64 v[246:247], v248 offset:184
	v_mfma_f32_32x32x16_f16 v[112:127], a[108:111], v[188:191], v[112:127]
	ds_read_b128 v[188:191], v192 offset:64512
	global_load_lds_dwordx4 v192, s[44:45] offset:2048 sc1
	v_exp_f32_e32 v215, v95
	v_add_f32_e32 v214, 1.0, v214
	s_waitcnt lgkmcnt(8)
	v_fma_f32 v44, v229, v237, v240
	s_waitcnt vmcnt(8)
	s_barrier
	s_waitcnt lgkmcnt(6)
	v_mfma_f32_32x32x16_f16 v[96:111], a[112:115], v[160:163], v[96:111]
	ds_read_b128 v[160:163], v193 offset:0
	v_add_f32_e32 v215, 1.0, v215
	v_rcp_f32_e32 v200, v200
	v_fma_f32 v45, v229, v239, v241
	v_fmac_f32_e32 v44, v228, v236
	v_mfma_f32_32x32x16_f16 v[112:127], a[112:115], v[164:167], v[112:127]
	ds_read_b128 v[164:167], v193 offset:1024
	v_rcp_f32_e32 v201, v201
	v_fmac_f32_e32 v45, v228, v238
	v_fma_f32 v60, v231, v237, v240
	v_mfma_f32_32x32x16_f16 v[96:111], a[116:119], v[168:171], v[96:111]
	ds_read_b128 v[168:171], v193 offset:2048
	v_rcp_f32_e32 v202, v202
	v_fma_f32 v61, v231, v239, v241
	v_fmac_f32_e32 v60, v230, v236
	v_mfma_f32_32x32x16_f16 v[112:127], a[116:119], v[172:175], v[112:127]
	ds_read_b128 v[172:175], v193 offset:3072
	global_load_lds_dwordx4 v192, s[44:45] offset:3072 sc1
	v_rcp_f32_e32 v203, v203
	v_fmac_f32_e32 v61, v230, v238
	s_waitcnt lgkmcnt(5)
	s_waitcnt lgkmcnt(4)
	v_mfma_f32_32x32x16_f16 v[96:111], a[120:123], v[176:179], v[96:111]
	ds_read_b128 v[176:179], v193 offset:4096
	v_rcp_f32_e32 v204, v204
	v_fma_f32 v46, v229, v243, v246
	v_fma_f32 v47, v229, v245, v247
	v_mfma_f32_32x32x16_f16 v[112:127], a[120:123], v[180:183], v[112:127]
	ds_read_b128 v[180:183], v193 offset:5120
	v_rcp_f32_e32 v205, v205
	v_mul_f32_e32 v204, v204, v148
	v_fmac_f32_e32 v46, v228, v242
	v_fmac_f32_e32 v47, v228, v244
	v_mfma_f32_32x32x16_f16 v[96:111], a[124:127], v[184:187], v[96:111]
	ds_read_b128 v[184:187], v193 offset:6144
	v_rcp_f32_e32 v206, v206
	v_mul_f32_e32 v205, v205, v149
	v_fma_f32 v62, v231, v243, v246
	v_fma_f32 v63, v231, v245, v247
	v_mfma_f32_32x32x16_f16 v[112:127], a[124:127], v[188:191], v[112:127]
	ds_read_b128 v[188:191], v193 offset:7168
	s_waitcnt vmcnt(3)
	v_cmp_gt_u32_e32 vcc, 1, v251
	s_cbranch_vccz .LE_tok43

.LE_tok43:
	s_and_b32 s64, s33, 1
	s_lshl_b32 s64, s64, 22
	s_add_u32 s64, s64, s49
	s_add_u32 s34, s6, s64
	s_addc_u32 s35, s7, 0
	s_add_u32 s44, s34, 0x0
	s_addc_u32 s45, s35, 0
	s_mov_b32 m0, s52
	s_nop 0
	global_load_lds_dwordx4 v192, s[44:45] sc1
	v_rcp_f32_e32 v207, v207
	v_mul_f32_e32 v206, v206, v150
	v_fmac_f32_e32 v62, v230, v242
	v_fmac_f32_e32 v63, v230, v244
	s_waitcnt lgkmcnt(4)
	v_mfma_f32_32x32x16_f16 v[96:111], a[128:131], v[160:163], v[96:111]
	ds_read_b128 v[160:163], v193 offset:8192
	v_rcp_f32_e32 v208, v208
	v_mul_f32_e32 v207, v207, v151
	v_mfma_f32_32x32x16_f16 v[112:127], a[128:131], v[164:167], v[112:127]
	ds_read_b128 v[164:167], v193 offset:9216
	v_rcp_f32_e32 v209, v209
	v_fmamk_f32 v208, v208, 0xc0b8aa3b, v198
	v_mfma_f32_32x32x16_f16 v[96:111], a[132:135], v[168:171], v[96:111]
	ds_read_b128 v[168:171], v193 offset:10240
	v_rcp_f32_e32 v210, v210
	v_fmamk_f32 v209, v209, 0xc0b8aa3b, v198
	v_fma_f32 v148, v200, v208, v204
	v_mfma_f32_32x32x16_f16 v[112:127], a[132:135], v[172:175], v[112:127]
	ds_read_b128 v[172:175], v193 offset:11264
	global_load_lds_dwordx4 v192, s[44:45] offset:1024 sc1
	v_rcp_f32_e32 v211, v211
	v_fmamk_f32 v210, v210, 0xc0b8aa3b, v198
	v_fma_f32 v149, v201, v209, v205
	s_waitcnt lgkmcnt(4)
	v_mfma_f32_32x32x16_f16 v[96:111], a[136:139], v[176:179], v[96:111]
	ds_read_b128 v[176:179], v193 offset:12288
	v_rcp_f32_e32 v212, v212
	v_fmamk_f32 v211, v211, 0xc0b8aa3b, v198
	v_fma_f32 v150, v202, v210, v206
	v_mfma_f32_32x32x16_f16 v[112:127], a[136:139], v[180:183], v[112:127]
	ds_read_b128 v[180:183], v193 offset:13312
	v_rcp_f32_e32 v213, v213
	v_fma_f32 v151, v203, v211, v207
	v_mfma_f32_32x32x16_f16 v[96:111], a[140:143], v[184:187], v[96:111]
	ds_read_b128 v[184:187], v193 offset:14336
	v_rcp_f32_e32 v214, v214
	v_mfma_f32_32x32x16_f16 v[112:127], a[140:143], v[188:191], v[112:127]
	ds_read_b128 v[188:191], v193 offset:15360
	global_load_lds_dwordx4 v192, s[44:45] offset:2048 sc1
	v_rcp_f32_e32 v215, v215
	s_waitcnt lgkmcnt(4)
	v_mfma_f32_32x32x16_f16 v[96:111], a[144:147], v[160:163], v[96:111]
	ds_read_b128 v[160:163], v193 offset:16384
	v_exp_f32_e32 v200, v148
	v_mfma_f32_32x32x16_f16 v[112:127], a[144:147], v[164:167], v[112:127]
	ds_read_b128 v[164:167], v193 offset:17408
	v_exp_f32_e32 v201, v149
	v_add_f32_e32 v200, 1.0, v200
	v_mfma_f32_32x32x16_f16 v[96:111], a[148:151], v[168:171], v[96:111]
	ds_read_b128 v[168:171], v193 offset:18432
	v_exp_f32_e32 v202, v150
	v_add_f32_e32 v201, 1.0, v201
	v_mfma_f32_32x32x16_f16 v[112:127], a[148:151], v[172:175], v[112:127]
	ds_read_b128 v[172:175], v193 offset:19456
	global_load_lds_dwordx4 v192, s[44:45] offset:3072 sc1
	v_exp_f32_e32 v203, v151
	v_add_f32_e32 v202, 1.0, v202
	s_waitcnt lgkmcnt(4)
	v_mfma_f32_32x32x16_f16 v[96:111], a[152:155], v[176:179], v[96:111]
	ds_read_b128 v[176:179], v193 offset:20480
	v_add_f32_e32 v203, 1.0, v203
	v_rcp_f32_e32 v200, v200
	v_mfma_f32_32x32x16_f16 v[112:127], a[152:155], v[180:183], v[112:127]
	ds_read_b128 v[180:183], v193 offset:21504
	v_rcp_f32_e32 v201, v201
	v_fma_f32 v200, v200, 2.0, -1.0
	v_mfma_f32_32x32x16_f16 v[96:111], a[156:159], v[184:187], v[96:111]
	ds_read_b128 v[184:187], v193 offset:22528
	v_rcp_f32_e32 v202, v202
	v_fma_f32 v201, v201, 2.0, -1.0
	v_mul_f32_e32 v216, v212, v200
	v_mfma_f32_32x32x16_f16 v[112:127], a[156:159], v[188:191], v[112:127]
	ds_read_b128 v[188:191], v193 offset:23552
	s_add_u32 s44, s34, 0x1000
	s_addc_u32 s45, s35, 0
	s_mov_b32 m0, s53
	s_nop 0
	global_load_lds_dwordx4 v192, s[44:45] sc1
	v_rcp_f32_e32 v203, v203
	v_fma_f32 v202, v202, 2.0, -1.0
	v_mul_f32_e32 v217, v213, v201
	s_waitcnt lgkmcnt(4)
	v_mfma_f32_32x32x16_f16 v[96:111], a[160:163], v[160:163], v[96:111]
	ds_read_b128 v[160:163], v193 offset:24576
	v_fma_f32 v203, v203, 2.0, -1.0
	v_mul_f32_e32 v218, v214, v202
	v_mfma_f32_32x32x16_f16 v[112:127], a[160:163], v[164:167], v[112:127]
	ds_read_b128 v[164:167], v193 offset:25600
	v_mul_f32_e32 v219, v215, v203
	v_cvt_pk_f16_f32 v222, v216, v217
	v_mfma_f32_32x32x16_f16 v[96:111], a[164:167], v[168:171], v[96:111]
	ds_read_b128 v[168:171], v193 offset:26624
	v_cvt_pk_f16_f32 v223, v218, v219
	v_mfma_f32_32x32x16_f16 v[112:127], a[164:167], v[172:175], v[112:127]
	ds_read_b128 v[172:175], v193 offset:27648
	global_load_lds_dwordx4 v192, s[44:45] offset:1024 sc1
	s_cmp_lg_u32 s33, s60
	s_cbranch_scc1 .LE_nht45
	s_add_u32 s46, s62, 0xa0000
	s_addc_u32 s47, s63, 0
	global_store_dwordx4 v250, v[216:219], s[46:47]
	s_waitcnt vmcnt(0)
.LE_nht45:
	s_waitcnt lgkmcnt(4)
	v_mfma_f32_32x32x16_f16 v[96:111], a[168:171], v[176:179], v[96:111]
	ds_read_b128 v[176:179], v193 offset:28672
	s_nop 1
	v_permlane32_swap_b32_e32 v220, v222
	v_permlane32_swap_b32_e32 v221, v223
	s_cmp_eq_u32 s31, 0
	s_cbranch_scc1 .LE_slow46
	global_store_dwordx4 v195, v[220:223], s[36:37] offset:0
	s_branch .LE_join47

.LE_join47:
	v_mfma_f32_32x32x16_f16 v[112:127], a[168:171], v[180:183], v[112:127]
	ds_read_b128 v[180:183], v193 offset:29696
	v_mfma_f32_32x32x16_f16 v[96:111], a[172:175], v[184:187], v[96:111]
	ds_read_b128 v[184:187], v193 offset:30720
	v_mfma_f32_32x32x16_f16 v[112:127], a[172:175], v[188:191], v[112:127]
	ds_read_b128 v[188:191], v193 offset:31744
	global_load_lds_dwordx4 v192, s[44:45] offset:2048 sc1
	s_waitcnt vmcnt(8)
	s_barrier
	s_waitcnt lgkmcnt(4)
	v_mfma_f32_32x32x16_f16 v[96:111], a[176:179], v[160:163], v[96:111]
	ds_read_b128 v[160:163], v193 offset:32768
	v_mfma_f32_32x32x16_f16 v[112:127], a[176:179], v[164:167], v[112:127]
	ds_read_b128 v[164:167], v193 offset:33792
	v_mfma_f32_32x32x16_f16 v[96:111], a[180:183], v[168:171], v[96:111]
	ds_read_b128 v[168:171], v193 offset:34816
	v_mfma_f32_32x32x16_f16 v[112:127], a[180:183], v[172:175], v[112:127]
	ds_read_b128 v[172:175], v193 offset:35840
	global_load_lds_dwordx4 v192, s[44:45] offset:3072 sc1
	s_waitcnt lgkmcnt(4)
	v_mfma_f32_32x32x16_f16 v[96:111], a[184:187], v[176:179], v[96:111]
	ds_read_b128 v[176:179], v193 offset:36864
	v_mfma_f32_32x32x16_f16 v[112:127], a[184:187], v[180:183], v[112:127]
	ds_read_b128 v[180:183], v193 offset:37888
	v_mfma_f32_32x32x16_f16 v[96:111], a[188:191], v[184:187], v[96:111]
	ds_read_b128 v[184:187], v193 offset:38912
	v_mfma_f32_32x32x16_f16 v[112:127], a[188:191], v[188:191], v[112:127]
	ds_read_b128 v[188:191], v193 offset:39936
	s_add_u32 s44, s34, 0x8000
	s_addc_u32 s45, s35, 0
	s_mov_b32 m0, s54
	s_nop 0
	global_load_lds_dwordx4 v192, s[44:45] sc1
	s_waitcnt lgkmcnt(4)
	v_mfma_f32_32x32x16_f16 v[96:111], a[192:195], v[160:163], v[96:111]
	ds_read_b128 v[160:163], v193 offset:40960
	v_mfma_f32_32x32x16_f16 v[112:127], a[192:195], v[164:167], v[112:127]
	ds_read_b128 v[164:167], v193 offset:41984
	s_waitcnt vmcnt(3)
	s_barrier
	v_mov_b32_e32 v199, 3
	s_cmp_eq_u32 s31, 0
	s_cbranch_scc1 .LE_slow48
	global_store_dword v197, v199, s[40:41]
	s_branch .LE_join49

.LE_join49:
	v_mfma_f32_32x32x16_f16 v[96:111], a[196:199], v[168:171], v[96:111]
	ds_read_b128 v[168:171], v193 offset:43008
	v_mfma_f32_32x32x16_f16 v[112:127], a[196:199], v[172:175], v[112:127]
	ds_read_b128 v[172:175], v193 offset:44032
	global_load_lds_dwordx4 v192, s[44:45] offset:1024 sc1
	s_waitcnt lgkmcnt(4)
	v_mfma_f32_32x32x16_f16 v[96:111], a[200:203], v[176:179], v[96:111]
	ds_read_b128 v[176:179], v193 offset:45056
	v_mfma_f32_32x32x16_f16 v[112:127], a[200:203], v[180:183], v[112:127]
	ds_read_b128 v[180:183], v193 offset:46080
	v_mfma_f32_32x32x16_f16 v[96:111], a[204:207], v[184:187], v[96:111]
	ds_read_b128 v[184:187], v193 offset:47104
	v_mfma_f32_32x32x16_f16 v[112:127], a[204:207], v[188:191], v[112:127]
	ds_read_b128 v[188:191], v193 offset:48128
	global_load_lds_dwordx4 v192, s[44:45] offset:2048 sc1
	s_waitcnt lgkmcnt(4)
	v_mfma_f32_32x32x16_f16 v[96:111], a[208:211], v[160:163], v[96:111]
	ds_read_b128 v[160:163], v193 offset:49152
	v_mfma_f32_32x32x16_f16 v[112:127], a[208:211], v[164:167], v[112:127]
	ds_read_b128 v[164:167], v193 offset:50176
	v_mfma_f32_32x32x16_f16 v[96:111], a[212:215], v[168:171], v[96:111]
	ds_read_b128 v[168:171], v193 offset:51200
	v_mfma_f32_32x32x16_f16 v[112:127], a[212:215], v[172:175], v[112:127]
	ds_read_b128 v[172:175], v193 offset:52224
	global_load_lds_dwordx4 v192, s[44:45] offset:3072 sc1
	s_waitcnt lgkmcnt(4)
	v_mfma_f32_32x32x16_f16 v[96:111], a[216:219], v[176:179], v[96:111]
	ds_read_b128 v[176:179], v193 offset:53248
	v_mfma_f32_32x32x16_f16 v[112:127], a[216:219], v[180:183], v[112:127]
	ds_read_b128 v[180:183], v193 offset:54272
	v_mfma_f32_32x32x16_f16 v[96:111], a[220:223], v[184:187], v[96:111]
	ds_read_b128 v[184:187], v193 offset:55296
	v_mfma_f32_32x32x16_f16 v[112:127], a[220:223], v[188:191], v[112:127]
	ds_read_b128 v[188:191], v193 offset:56320
	s_add_u32 s44, s34, 0x9000
	s_addc_u32 s45, s35, 0
	s_mov_b32 m0, s55
	s_nop 0
	global_load_lds_dwordx4 v192, s[44:45] sc1
	s_waitcnt lgkmcnt(4)
	v_mfma_f32_32x32x16_f16 v[96:111], a[224:227], v[160:163], v[96:111]
	ds_read_b128 v[160:163], v193 offset:57344
	v_mfma_f32_32x32x16_f16 v[112:127], a[224:227], v[164:167], v[112:127]
	ds_read_b128 v[164:167], v193 offset:58368
	v_mfma_f32_32x32x16_f16 v[96:111], a[228:231], v[168:171], v[96:111]
	ds_read_b128 v[168:171], v193 offset:59392
	v_mfma_f32_32x32x16_f16 v[112:127], a[228:231], v[172:175], v[112:127]
	ds_read_b128 v[172:175], v193 offset:60416
	global_load_lds_dwordx4 v192, s[44:45] offset:1024 sc1
	s_waitcnt lgkmcnt(4)
	v_mfma_f32_32x32x16_f16 v[96:111], a[232:235], v[176:179], v[96:111]
	ds_read_b128 v[176:179], v193 offset:61440
	v_mfma_f32_32x32x16_f16 v[112:127], a[232:235], v[180:183], v[112:127]
	ds_read_b128 v[180:183], v193 offset:62464
	v_mfma_f32_32x32x16_f16 v[96:111], a[236:239], v[184:187], v[96:111]
	ds_read_b128 v[184:187], v193 offset:63488
	v_mfma_f32_32x32x16_f16 v[112:127], a[236:239], v[188:191], v[112:127]
	ds_read_b128 v[188:191], v193 offset:64512
	global_load_lds_dwordx4 v192, s[44:45] offset:2048 sc1
	s_waitcnt vmcnt(8)
	s_barrier
	s_waitcnt lgkmcnt(4)
	v_mfma_f32_32x32x16_f16 v[96:111], a[240:243], v[160:163], v[96:111]
	ds_read_b128 v[160:163], v192 offset:0
	v_mfma_f32_32x32x16_f16 v[112:127], a[240:243], v[164:167], v[112:127]
	ds_read_b128 v[164:167], v192 offset:1024
	v_mfma_f32_32x32x16_f16 v[96:111], a[244:247], v[168:171], v[96:111]
	ds_read_b128 v[168:171], v192 offset:2048
	v_mfma_f32_32x32x16_f16 v[112:127], a[244:247], v[172:175], v[112:127]
	ds_read_b128 v[172:175], v192 offset:3072
	global_load_lds_dwordx4 v192, s[44:45] offset:3072 sc1
	s_waitcnt lgkmcnt(4)
	v_mfma_f32_32x32x16_f16 v[96:111], a[248:251], v[176:179], v[96:111]
	ds_read_b128 v[176:179], v192 offset:4096
	v_mfma_f32_32x32x16_f16 v[112:127], a[248:251], v[180:183], v[112:127]
	ds_read_b128 v[180:183], v192 offset:5120
	v_mfma_f32_32x32x16_f16 v[96:111], a[252:255], v[184:187], v[96:111]
	ds_read_b128 v[184:187], v192 offset:6144
	v_mfma_f32_32x32x16_f16 v[112:127], a[252:255], v[188:191], v[112:127]
	ds_read_b128 v[188:191], v192 offset:7168
	s_add_u32 s44, s34, 0x10000
	s_addc_u32 s45, s35, 0
	s_mov_b32 m0, s56
	s_nop 0
	global_load_lds_dwordx4 v192, s[44:45] sc1
	s_add_u32 s33, s33, 1
	s_cmp_lt_u32 s33, s28
	s_cbranch_scc1 .LE_loop16

.LD_loop16:
	s_sub_u32 s71, s33, 1
	s_add_u32 s61, s33, 1
	s_min_u32 s61, s61, s60
	s_and_b32 s64, s71, 1
	s_lshl_b32 s64, s64, 22
	s_add_u32 s64, s64, s50
	s_add_u32 s64, s64, 0x60000
	s_add_u32 s36, s6, s64
	s_addc_u32 s37, s7, 0
	s_lshl_b32 s64, s71, 3
	s_add_u32 s64, s64, s29
	s_lshl_b32 s64, s64, 5
	s_add_u32 s64, s64, s30
	s_lshl_b32 s64, s64, 2
	s_add_u32 s40, s8, s64
	s_addc_u32 s41, s9, 0
	s_lshl_b32 s64, s71, 19
	s_add_u32 s64, s64, 0x600
	s_add_u32 s72, s62, s64
	s_addc_u32 s73, s63, 0
	s_nop 3
	s_waitcnt lgkmcnt(4)
	v_mfma_f32_32x32x16_f16 v[0:15], a[0:3], v[160:163], v[0:15]
	ds_read_b128 v[160:163], v192 offset:8192
	v_exp_f32_e32 v200, v96
	v_mfma_f32_32x32x16_f16 v[16:31], a[0:3], v[164:167], v[16:31]
	ds_read_b128 v[164:167], v192 offset:9216
	v_exp_f32_e32 v201, v97
	v_add_f32_e32 v200, 1.0, v200
	v_mfma_f32_32x32x16_f16 v[0:15], a[4:7], v[168:171], v[0:15]
	ds_read_b128 v[168:171], v192 offset:10240
	v_exp_f32_e32 v202, v98
	v_add_f32_e32 v201, 1.0, v201
	v_mfma_f32_32x32x16_f16 v[16:31], a[4:7], v[172:175], v[16:31]
	ds_read_b128 v[172:175], v192 offset:11264
	global_load_lds_dwordx4 v192, s[44:45] offset:1024 sc1
	v_exp_f32_e32 v203, v99
	v_add_f32_e32 v202, 1.0, v202
	s_waitcnt lgkmcnt(4)
	v_mfma_f32_32x32x16_f16 v[0:15], a[8:11], v[176:179], v[0:15]
	ds_read_b128 v[176:179], v192 offset:12288
	v_exp_f32_e32 v204, v100
	v_add_f32_e32 v203, 1.0, v203
	v_mfma_f32_32x32x16_f16 v[16:31], a[8:11], v[180:183], v[16:31]
	ds_read_b128 v[180:183], v192 offset:13312
	v_exp_f32_e32 v205, v101
	v_add_f32_e32 v204, 1.0, v204
	v_mfma_f32_32x32x16_f16 v[0:15], a[12:15], v[184:187], v[0:15]
	ds_read_b128 v[184:187], v192 offset:14336
	v_exp_f32_e32 v206, v102
	v_add_f32_e32 v205, 1.0, v205
	v_mfma_f32_32x32x16_f16 v[16:31], a[12:15], v[188:191], v[16:31]
	ds_read_b128 v[188:191], v192 offset:15360
	global_load_lds_dwordx4 v192, s[44:45] offset:2048 sc1
	v_exp_f32_e32 v207, v103
	v_add_f32_e32 v206, 1.0, v206
	s_waitcnt lgkmcnt(4)
	v_mfma_f32_32x32x16_f16 v[0:15], a[16:19], v[160:163], v[0:15]
	ds_read_b128 v[160:163], v192 offset:16384
	v_exp_f32_e32 v208, v104
	v_add_f32_e32 v207, 1.0, v207
	v_mfma_f32_32x32x16_f16 v[16:31], a[16:19], v[164:167], v[16:31]
	ds_read_b128 v[164:167], v192 offset:17408
	v_exp_f32_e32 v209, v105
	v_add_f32_e32 v208, 1.0, v208
	v_mfma_f32_32x32x16_f16 v[0:15], a[20:23], v[168:171], v[0:15]
	ds_read_b128 v[168:171], v192 offset:18432
	v_exp_f32_e32 v210, v106
	v_add_f32_e32 v209, 1.0, v209
	v_mfma_f32_32x32x16_f16 v[16:31], a[20:23], v[172:175], v[16:31]
	ds_read_b128 v[172:175], v192 offset:19456
	global_load_lds_dwordx4 v192, s[44:45] offset:3072 sc1
	v_exp_f32_e32 v211, v107
	v_add_f32_e32 v210, 1.0, v210
	s_waitcnt lgkmcnt(4)
	v_mfma_f32_32x32x16_f16 v[0:15], a[24:27], v[176:179], v[0:15]
	ds_read_b128 v[176:179], v192 offset:20480
	v_exp_f32_e32 v212, v108
	v_add_f32_e32 v211, 1.0, v211
	v_mfma_f32_32x32x16_f16 v[16:31], a[24:27], v[180:183], v[16:31]
	ds_read_b128 v[180:183], v192 offset:21504
	v_exp_f32_e32 v213, v109
	v_add_f32_e32 v212, 1.0, v212
	v_mfma_f32_32x32x16_f16 v[0:15], a[28:31], v[184:187], v[0:15]
	ds_read_b128 v[184:187], v192 offset:22528
	v_exp_f32_e32 v214, v110
	v_add_f32_e32 v213, 1.0, v213
	v_mfma_f32_32x32x16_f16 v[16:31], a[28:31], v[188:191], v[16:31]
	ds_read_b128 v[188:191], v192 offset:23552
	s_add_u32 s44, s34, 0x11000
	s_addc_u32 s45, s35, 0
	s_mov_b32 m0, s57
	s_nop 0
	global_load_lds_dwordx4 v192, s[44:45] sc1
	v_exp_f32_e32 v215, v111
	v_add_f32_e32 v214, 1.0, v214
	s_waitcnt lgkmcnt(4)
	v_mfma_f32_32x32x16_f16 v[0:15], a[32:35], v[160:163], v[0:15]
	ds_read_b128 v[160:163], v192 offset:24576
	v_add_f32_e32 v215, 1.0, v215
	v_rcp_f32_e32 v200, v200
	v_mfma_f32_32x32x16_f16 v[16:31], a[32:35], v[164:167], v[16:31]
	ds_read_b128 v[164:167], v192 offset:25600
	v_rcp_f32_e32 v201, v201
	v_mfma_f32_32x32x16_f16 v[0:15], a[36:39], v[168:171], v[0:15]
	ds_read_b128 v[168:171], v192 offset:26624
	v_rcp_f32_e32 v202, v202
	v_mfma_f32_32x32x16_f16 v[16:31], a[36:39], v[172:175], v[16:31]
	ds_read_b128 v[172:175], v192 offset:27648
	global_load_lds_dwordx4 v192, s[44:45] offset:1024 sc1
	v_rcp_f32_e32 v203, v203
	s_waitcnt lgkmcnt(4)
	v_mfma_f32_32x32x16_f16 v[0:15], a[40:43], v[176:179], v[0:15]
	ds_read_b128 v[176:179], v192 offset:28672
	v_rcp_f32_e32 v204, v204
	v_mfma_f32_32x32x16_f16 v[16:31], a[40:43], v[180:183], v[16:31]
	ds_read_b128 v[180:183], v192 offset:29696
	v_rcp_f32_e32 v205, v205
	v_mul_f32_e32 v204, v204, v152
	v_mfma_f32_32x32x16_f16 v[0:15], a[44:47], v[184:187], v[0:15]
	ds_read_b128 v[184:187], v192 offset:30720
	v_rcp_f32_e32 v206, v206
	v_mul_f32_e32 v205, v205, v153
	v_mfma_f32_32x32x16_f16 v[16:31], a[44:47], v[188:191], v[16:31]
	ds_read_b128 v[188:191], v192 offset:31744
	global_load_lds_dwordx4 v192, s[44:45] offset:2048 sc1
	v_rcp_f32_e32 v207, v207
	v_mul_f32_e32 v206, v206, v154
	s_waitcnt vmcnt(7)
	s_barrier
	s_waitcnt lgkmcnt(4)
	v_mfma_f32_32x32x16_f16 v[0:15], a[48:51], v[160:163], v[0:15]
	ds_read_b128 v[160:163], v192 offset:32768
	v_rcp_f32_e32 v208, v208
	v_mul_f32_e32 v207, v207, v155
	s_add_u32 s46, s42, 0x4000
	s_addc_u32 s47, s43, 0
	global_load_dwordx4 v[64:67], v192, s[46:47] offset:0
	v_mfma_f32_32x32x16_f16 v[16:31], a[48:51], v[164:167], v[16:31]
	ds_read_b128 v[164:167], v192 offset:33792
	v_rcp_f32_e32 v209, v209
	v_fmamk_f32 v208, v208, 0xc0b8aa3b, v198
	global_load_dwordx4 v[68:71], v192, s[46:47] offset:1024
	global_load_dwordx4 v[72:75], v192, s[46:47] offset:2048
	v_mfma_f32_32x32x16_f16 v[0:15], a[52:55], v[168:171], v[0:15]
	ds_read_b128 v[168:171], v192 offset:34816
	v_rcp_f32_e32 v210, v210
	v_fmamk_f32 v209, v209, 0xc0b8aa3b, v198
	v_fma_f32 v152, v200, v208, v204
	global_load_dwordx4 v[76:79], v192, s[46:47] offset:3072
	s_add_u32 s46, s42, 0x5000
	s_addc_u32 s47, s43, 0
	v_mfma_f32_32x32x16_f16 v[16:31], a[52:55], v[172:175], v[16:31]
	ds_read_b128 v[172:175], v192 offset:35840
	global_load_lds_dwordx4 v192, s[44:45] offset:3072 sc1
	v_rcp_f32_e32 v211, v211
	v_fmamk_f32 v210, v210, 0xc0b8aa3b, v198
	v_fma_f32 v153, v201, v209, v205
	global_load_dwordx4 v[80:83], v192, s[46:47] offset:0
	global_load_dwordx4 v[84:87], v192, s[46:47] offset:1024
	s_waitcnt lgkmcnt(4)
	v_mfma_f32_32x32x16_f16 v[0:15], a[56:59], v[176:179], v[0:15]
	ds_read_b128 v[176:179], v192 offset:36864
	v_rcp_f32_e32 v212, v212
	v_fmamk_f32 v211, v211, 0xc0b8aa3b, v198
	v_fma_f32 v154, v202, v210, v206
	global_load_dwordx4 v[88:91], v192, s[46:47] offset:2048
	global_load_dwordx4 v[92:95], v192, s[46:47] offset:3072
	v_mfma_f32_32x32x16_f16 v[16:31], a[56:59], v[180:183], v[16:31]
	ds_read_b128 v[180:183], v192 offset:37888
	v_rcp_f32_e32 v213, v213
	v_fma_f32 v155, v203, v211, v207
	v_mfma_f32_32x32x16_f16 v[0:15], a[60:63], v[184:187], v[0:15]
	ds_read_b128 v[184:187], v192 offset:38912
	v_rcp_f32_e32 v214, v214
	v_mfma_f32_32x32x16_f16 v[16:31], a[60:63], v[188:191], v[16:31]
	ds_read_b128 v[188:191], v192 offset:39936
	s_add_u32 s44, s34, 0x18000
	s_addc_u32 s45, s35, 0
	s_mov_b32 m0, s58
	s_nop 0
	global_load_lds_dwordx4 v192, s[44:45] sc1
	v_rcp_f32_e32 v215, v215
	s_waitcnt lgkmcnt(4)
	v_mfma_f32_32x32x16_f16 v[0:15], a[64:67], v[160:163], v[0:15]
	ds_read_b128 v[160:163], v192 offset:40960
	v_exp_f32_e32 v200, v152
	v_mfma_f32_32x32x16_f16 v[16:31], a[64:67], v[164:167], v[16:31]
	ds_read_b128 v[164:167], v192 offset:41984
	v_exp_f32_e32 v201, v153
	v_add_f32_e32 v200, 1.0, v200
	v_mfma_f32_32x32x16_f16 v[0:15], a[68:71], v[168:171], v[0:15]
	ds_read_b128 v[168:171], v192 offset:43008
	v_exp_f32_e32 v202, v154
	v_add_f32_e32 v201, 1.0, v201
	v_mfma_f32_32x32x16_f16 v[16:31], a[68:71], v[172:175], v[16:31]
	ds_read_b128 v[172:175], v192 offset:44032
	global_load_lds_dwordx4 v192, s[44:45] offset:1024 sc1
	v_exp_f32_e32 v203, v155
	v_add_f32_e32 v202, 1.0, v202
	s_waitcnt lgkmcnt(4)
	v_mfma_f32_32x32x16_f16 v[0:15], a[72:75], v[176:179], v[0:15]
	ds_read_b128 v[176:179], v192 offset:45056
	v_add_f32_e32 v203, 1.0, v203
	v_rcp_f32_e32 v200, v200
	v_mfma_f32_32x32x16_f16 v[16:31], a[72:75], v[180:183], v[16:31]
	ds_read_b128 v[180:183], v192 offset:46080
	v_rcp_f32_e32 v201, v201
	v_fma_f32 v200, v200, 2.0, -1.0
	v_mfma_f32_32x32x16_f16 v[0:15], a[76:79], v[184:187], v[0:15]
	ds_read_b128 v[184:187], v192 offset:47104
	v_rcp_f32_e32 v202, v202
	v_fma_f32 v201, v201, 2.0, -1.0
	v_mul_f32_e32 v216, v212, v200
	v_mfma_f32_32x32x16_f16 v[16:31], a[76:79], v[188:191], v[16:31]
	ds_read_b128 v[188:191], v192 offset:48128
	global_load_lds_dwordx4 v192, s[44:45] offset:2048 sc1
	v_rcp_f32_e32 v203, v203
	v_fma_f32 v202, v202, 2.0, -1.0
	v_mul_f32_e32 v217, v213, v201
	s_waitcnt lgkmcnt(4)
	v_mfma_f32_32x32x16_f16 v[0:15], a[80:83], v[160:163], v[0:15]
	ds_read_b128 v[160:163], v192 offset:49152
	v_fma_f32 v203, v203, 2.0, -1.0
	v_mul_f32_e32 v218, v214, v202
	v_exp_f32_e32 v200, v112
	v_mfma_f32_32x32x16_f16 v[16:31], a[80:83], v[164:167], v[16:31]
	ds_read_b128 v[164:167], v192 offset:50176
	v_mul_f32_e32 v219, v215, v203
	v_mul_f32_e32 v236, v216, v228
	v_exp_f32_e32 v201, v113
	v_mfma_f32_32x32x16_f16 v[0:15], a[84:87], v[168:171], v[0:15]
	ds_read_b128 v[168:171], v192 offset:51200
	v_mul_f32_e32 v237, v216, v232
	v_fmac_f32_e32 v236, v217, v229
	v_exp_f32_e32 v202, v114
	v_mfma_f32_32x32x16_f16 v[16:31], a[84:87], v[172:175], v[16:31]
	ds_read_b128 v[172:175], v192 offset:52224
	global_load_lds_dwordx4 v192, s[44:45] offset:3072 sc1
	v_fmac_f32_e32 v237, v217, v233
	v_fmac_f32_e32 v236, v218, v230
	v_exp_f32_e32 v203, v115
	s_waitcnt lgkmcnt(4)
	v_mfma_f32_32x32x16_f16 v[0:15], a[88:91], v[176:179], v[0:15]
	ds_read_b128 v[176:179], v192 offset:53248
	v_fmac_f32_e32 v237, v218, v234
	v_fmac_f32_e32 v236, v219, v231
	v_exp_f32_e32 v204, v116
	v_mfma_f32_32x32x16_f16 v[16:31], a[88:91], v[180:183], v[16:31]
	ds_read_b128 v[180:183], v192 offset:54272
	v_fmac_f32_e32 v237, v219, v235
	v_mov_b32_e32 v238, v236
	v_exp_f32_e32 v205, v117
	v_mfma_f32_32x32x16_f16 v[0:15], a[92:95], v[184:187], v[0:15]
	ds_read_b128 v[184:187], v192 offset:55296
	v_mov_b32_e32 v239, v236
	v_mov_b32_e32 v240, v237
	v_exp_f32_e32 v206, v118
	v_mfma_f32_32x32x16_f16 v[16:31], a[92:95], v[188:191], v[16:31]
	ds_read_b128 v[188:191], v192 offset:56320
	s_add_u32 s44, s34, 0x19000
	s_addc_u32 s45, s35, 0
	s_mov_b32 m0, s59
	s_nop 0
	global_load_lds_dwordx4 v192, s[44:45] sc1
	s_lshl_b32 s64, s71, 3
	s_add_u32 s64, s64, s29
	s_lshl_b32 s64, s64, 7
	s_add_u32 s38, s8, s64
	s_addc_u32 s39, s9, 0
	global_load_dword v251, v196, s[38:39] sc1
	v_mov_b32_e32 v241, v237
	v_cvt_pk_f16_f32 v220, v216, v217
	v_exp_f32_e32 v207, v119
	s_waitcnt lgkmcnt(4)
	v_mfma_f32_32x32x16_f16 v[0:15], a[96:99], v[160:163], v[0:15]
	ds_read_b128 v[160:163], v192 offset:57344
	s_nop 1
	v_permlane32_swap_b32_e32 v238, v239
	v_permlane32_swap_b32_e32 v240, v241
	v_add_f32_e32 v238, v238, v239
	v_add_f32_e32 v239, v240, v241
	ds_write_b64 v248, v[238:239] offset:1536
	v_exp_f32_e32 v208, v120
	v_mfma_f32_32x32x16_f16 v[16:31], a[96:99], v[164:167], v[16:31]
	ds_read_b128 v[164:167], v192 offset:58368
	v_cvt_pk_f16_f32 v221, v218, v219
	v_exp_f32_e32 v209, v121
	v_add_f32_e32 v200, 1.0, v200
	v_mfma_f32_32x32x16_f16 v[0:15], a[100:103], v[168:171], v[0:15]
	ds_read_b128 v[168:171], v192 offset:59392
	v_exp_f32_e32 v210, v122
	v_add_f32_e32 v201, 1.0, v201
	v_add_f32_e32 v202, 1.0, v202
	v_mfma_f32_32x32x16_f16 v[16:31], a[100:103], v[172:175], v[16:31]
	ds_read_b128 v[172:175], v192 offset:60416
	global_load_lds_dwordx4 v192, s[44:45] offset:1024 sc1
	v_exp_f32_e32 v211, v123
	v_add_f32_e32 v203, 1.0, v203
	v_add_f32_e32 v204, 1.0, v204
	s_waitcnt lgkmcnt(5)
	v_mfma_f32_32x32x16_f16 v[0:15], a[104:107], v[176:179], v[0:15]
	ds_read_b128 v[176:179], v192 offset:61440
	v_exp_f32_e32 v212, v124
	v_add_f32_e32 v205, 1.0, v205
	v_add_f32_e32 v206, 1.0, v206
	v_mfma_f32_32x32x16_f16 v[16:31], a[104:107], v[180:183], v[16:31]
	ds_read_b128 v[180:183], v192 offset:62464
	v_exp_f32_e32 v213, v125
	v_add_f32_e32 v207, 1.0, v207
	v_add_f32_e32 v208, 1.0, v208
	v_mfma_f32_32x32x16_f16 v[0:15], a[108:111], v[184:187], v[0:15]
	ds_read_b128 v[184:187], v192 offset:63488
	v_exp_f32_e32 v214, v126
	v_add_f32_e32 v209, 1.0, v209
	v_add_f32_e32 v210, 1.0, v210
	v_mfma_f32_32x32x16_f16 v[16:31], a[108:111], v[188:191], v[16:31]
	ds_read_b128 v[188:191], v192 offset:64512
	global_load_lds_dwordx4 v192, s[44:45] offset:2048 sc1
	v_exp_f32_e32 v215, v127
	v_add_f32_e32 v211, 1.0, v211
	v_add_f32_e32 v212, 1.0, v212
	s_waitcnt vmcnt(12)
	s_barrier
	s_waitcnt lgkmcnt(4)
	v_mfma_f32_32x32x16_f16 v[0:15], a[112:115], v[160:163], v[0:15]
	ds_read_b128 v[160:163], v193 offset:0
	v_add_f32_e32 v213, 1.0, v213
	v_add_f32_e32 v214, 1.0, v214
	v_rcp_f32_e32 v200, v200
	v_mfma_f32_32x32x16_f16 v[16:31], a[112:115], v[164:167], v[16:31]
	ds_read_b128 v[164:167], v193 offset:1024
	v_add_f32_e32 v215, 1.0, v215
	v_rcp_f32_e32 v201, v201
	v_mfma_f32_32x32x16_f16 v[0:15], a[116:119], v[168:171], v[0:15]
	ds_read_b128 v[168:171], v193 offset:2048
	v_rcp_f32_e32 v202, v202
	v_mfma_f32_32x32x16_f16 v[16:31], a[116:119], v[172:175], v[16:31]
	ds_read_b128 v[172:175], v193 offset:3072
	global_load_lds_dwordx4 v192, s[44:45] offset:3072 sc1
	v_rcp_f32_e32 v203, v203
	s_waitcnt lgkmcnt(4)
	v_mfma_f32_32x32x16_f16 v[0:15], a[120:123], v[176:179], v[0:15]
	ds_read_b128 v[176:179], v193 offset:4096
	v_rcp_f32_e32 v204, v204
	v_mfma_f32_32x32x16_f16 v[16:31], a[120:123], v[180:183], v[16:31]
	ds_read_b128 v[180:183], v193 offset:5120
	v_rcp_f32_e32 v205, v205
	v_mul_f32_e32 v204, v204, v156
	v_mfma_f32_32x32x16_f16 v[0:15], a[124:127], v[184:187], v[0:15]
	ds_read_b128 v[184:187], v193 offset:6144
	v_rcp_f32_e32 v206, v206
	v_mul_f32_e32 v205, v205, v157
	v_mfma_f32_32x32x16_f16 v[16:31], a[124:127], v[188:191], v[16:31]
	ds_read_b128 v[188:191], v193 offset:7168
	s_waitcnt vmcnt(3)
	v_cmp_gt_u32_e32 vcc, 2, v251
	s_cbranch_vccz .LD_tok20

.LD_tok20:
	s_and_b32 s64, s71, 1
	s_lshl_b32 s64, s64, 22
	s_add_u32 s64, s64, s49
	s_add_u32 s64, s64, 0x20000
	s_add_u32 s34, s6, s64
	s_addc_u32 s35, s7, 0
	s_add_u32 s44, s34, 0x0
	s_addc_u32 s45, s35, 0
	s_mov_b32 m0, s52
	s_nop 0
	global_load_lds_dwordx4 v192, s[44:45] sc1
	v_rcp_f32_e32 v207, v207
	v_mul_f32_e32 v206, v206, v158
	s_waitcnt lgkmcnt(4)
	v_mfma_f32_32x32x16_f16 v[0:15], a[128:131], v[160:163], v[0:15]
	ds_read_b128 v[160:163], v193 offset:8192
	v_rcp_f32_e32 v208, v208
	v_mul_f32_e32 v207, v207, v159
	v_mfma_f32_32x32x16_f16 v[16:31], a[128:131], v[164:167], v[16:31]
	ds_read_b128 v[164:167], v193 offset:9216
	v_rcp_f32_e32 v209, v209
	v_fmamk_f32 v208, v208, 0xc0b8aa3b, v198
	v_mfma_f32_32x32x16_f16 v[0:15], a[132:135], v[168:171], v[0:15]
	ds_read_b128 v[168:171], v193 offset:10240
	v_rcp_f32_e32 v210, v210
	v_fmamk_f32 v209, v209, 0xc0b8aa3b, v198
	v_fma_f32 v156, v200, v208, v204
	v_mfma_f32_32x32x16_f16 v[16:31], a[132:135], v[172:175], v[16:31]
	ds_read_b128 v[172:175], v193 offset:11264
	global_load_lds_dwordx4 v192, s[44:45] offset:1024 sc1
	v_rcp_f32_e32 v211, v211
	v_fmamk_f32 v210, v210, 0xc0b8aa3b, v198
	v_fma_f32 v157, v201, v209, v205
	s_waitcnt lgkmcnt(4)
	v_mfma_f32_32x32x16_f16 v[0:15], a[136:139], v[176:179], v[0:15]
	ds_read_b128 v[176:179], v193 offset:12288
	v_rcp_f32_e32 v212, v212
	v_fmamk_f32 v211, v211, 0xc0b8aa3b, v198
	v_fma_f32 v158, v202, v210, v206
	v_mfma_f32_32x32x16_f16 v[16:31], a[136:139], v[180:183], v[16:31]
	ds_read_b128 v[180:183], v193 offset:13312
	v_rcp_f32_e32 v213, v213
	v_fma_f32 v159, v203, v211, v207
	v_mfma_f32_32x32x16_f16 v[0:15], a[140:143], v[184:187], v[0:15]
	ds_read_b128 v[184:187], v193 offset:14336
	v_rcp_f32_e32 v214, v214
	v_mfma_f32_32x32x16_f16 v[16:31], a[140:143], v[188:191], v[16:31]
	ds_read_b128 v[188:191], v193 offset:15360
	global_load_lds_dwordx4 v192, s[44:45] offset:2048 sc1
	v_rcp_f32_e32 v215, v215
	s_waitcnt lgkmcnt(4)
	v_mfma_f32_32x32x16_f16 v[0:15], a[144:147], v[160:163], v[0:15]
	ds_read_b128 v[160:163], v193 offset:16384
	v_exp_f32_e32 v200, v156
	v_mfma_f32_32x32x16_f16 v[16:31], a[144:147], v[164:167], v[16:31]
	ds_read_b128 v[164:167], v193 offset:17408
	v_exp_f32_e32 v201, v157
	v_add_f32_e32 v200, 1.0, v200
	v_mfma_f32_32x32x16_f16 v[0:15], a[148:151], v[168:171], v[0:15]
	ds_read_b128 v[168:171], v193 offset:18432
	v_exp_f32_e32 v202, v158
	v_add_f32_e32 v201, 1.0, v201
	v_mfma_f32_32x32x16_f16 v[16:31], a[148:151], v[172:175], v[16:31]
	ds_read_b128 v[172:175], v193 offset:19456
	global_load_lds_dwordx4 v192, s[44:45] offset:3072 sc1
	v_exp_f32_e32 v203, v159
	v_add_f32_e32 v202, 1.0, v202
	s_waitcnt lgkmcnt(4)
	v_mfma_f32_32x32x16_f16 v[0:15], a[152:155], v[176:179], v[0:15]
	ds_read_b128 v[176:179], v193 offset:20480
	v_add_f32_e32 v203, 1.0, v203
	v_rcp_f32_e32 v200, v200
	v_mfma_f32_32x32x16_f16 v[16:31], a[152:155], v[180:183], v[16:31]
	ds_read_b128 v[180:183], v193 offset:21504
	v_rcp_f32_e32 v201, v201
	v_fma_f32 v200, v200, 2.0, -1.0
	v_mfma_f32_32x32x16_f16 v[0:15], a[156:159], v[184:187], v[0:15]
	ds_read_b128 v[184:187], v193 offset:22528
	v_rcp_f32_e32 v202, v202
	v_fma_f32 v201, v201, 2.0, -1.0
	v_mul_f32_e32 v216, v212, v200
	v_mfma_f32_32x32x16_f16 v[16:31], a[156:159], v[188:191], v[16:31]
	ds_read_b128 v[188:191], v193 offset:23552
	s_add_u32 s44, s34, 0x1000
	s_addc_u32 s45, s35, 0
	s_mov_b32 m0, s53
	s_nop 0
	global_load_lds_dwordx4 v192, s[44:45] sc1
	v_rcp_f32_e32 v203, v203
	v_fma_f32 v202, v202, 2.0, -1.0
	v_mul_f32_e32 v217, v213, v201
	s_waitcnt lgkmcnt(4)
	v_mfma_f32_32x32x16_f16 v[0:15], a[160:163], v[160:163], v[0:15]
	ds_read_b128 v[160:163], v193 offset:24576
	v_fma_f32 v203, v203, 2.0, -1.0
	v_mul_f32_e32 v218, v214, v202
	v_mfma_f32_32x32x16_f16 v[16:31], a[160:163], v[164:167], v[16:31]
	ds_read_b128 v[164:167], v193 offset:25600
	v_mul_f32_e32 v219, v215, v203
	v_mul_f32_e32 v236, v216, v228
	v_mfma_f32_32x32x16_f16 v[0:15], a[164:167], v[168:171], v[0:15]
	ds_read_b128 v[168:171], v193 offset:26624
	v_mul_f32_e32 v237, v216, v232
	v_fmac_f32_e32 v236, v217, v229
	v_mfma_f32_32x32x16_f16 v[16:31], a[164:167], v[172:175], v[16:31]
	ds_read_b128 v[172:175], v193 offset:27648
	global_load_lds_dwordx4 v192, s[44:45] offset:1024 sc1
	v_fmac_f32_e32 v237, v217, v233
	v_fmac_f32_e32 v236, v218, v230
	s_waitcnt lgkmcnt(4)
	v_mfma_f32_32x32x16_f16 v[0:15], a[168:171], v[176:179], v[0:15]
	ds_read_b128 v[176:179], v193 offset:28672
	v_fmac_f32_e32 v237, v218, v234
	v_fmac_f32_e32 v236, v219, v231
	v_mfma_f32_32x32x16_f16 v[16:31], a[168:171], v[180:183], v[16:31]
	ds_read_b128 v[180:183], v193 offset:29696
	v_fmac_f32_e32 v237, v219, v235
	v_mov_b32_e32 v238, v236
	v_mfma_f32_32x32x16_f16 v[0:15], a[172:175], v[184:187], v[0:15]
	ds_read_b128 v[184:187], v193 offset:30720
	v_mov_b32_e32 v239, v236
	v_mov_b32_e32 v240, v237
	v_mfma_f32_32x32x16_f16 v[16:31], a[172:175], v[188:191], v[16:31]
	ds_read_b128 v[188:191], v193 offset:31744
	global_load_lds_dwordx4 v192, s[44:45] offset:2048 sc1
	v_mov_b32_e32 v241, v237
	v_cvt_pk_f16_f32 v222, v216, v217
	s_waitcnt vmcnt(7)
	s_barrier
	s_waitcnt lgkmcnt(4)
	v_mfma_f32_32x32x16_f16 v[0:15], a[176:179], v[160:163], v[0:15]
	ds_read_b128 v[160:163], v193 offset:32768
	s_nop 1
	v_permlane32_swap_b32_e32 v238, v239
	v_permlane32_swap_b32_e32 v240, v241
	v_add_f32_e32 v238, v238, v239
	v_add_f32_e32 v239, v240, v241
	ds_write_b64 v248, v[238:239] offset:1792
	v_mfma_f32_32x32x16_f16 v[16:31], a[176:179], v[164:167], v[16:31]
	ds_read_b128 v[164:167], v193 offset:33792
	v_cvt_pk_f16_f32 v223, v218, v219
	v_mfma_f32_32x32x16_f16 v[0:15], a[180:183], v[168:171], v[0:15]
	ds_read_b128 v[168:171], v193 offset:34816
	s_nop 1
	v_permlane32_swap_b32_e32 v220, v222
	v_permlane32_swap_b32_e32 v221, v223
	s_cmp_eq_u32 s31, 0
	s_cbranch_scc1 .LD_slow22
	global_store_dwordx4 v195, v[220:223], s[36:37] offset:0
	s_branch .LD_join23

.LD_join23:
	v_mfma_f32_32x32x16_f16 v[16:31], a[180:183], v[172:175], v[16:31]
	ds_read_b128 v[172:175], v193 offset:35840
	global_load_lds_dwordx4 v192, s[44:45] offset:3072 sc1
	s_waitcnt lgkmcnt(5)
	v_mfma_f32_32x32x16_f16 v[0:15], a[184:187], v[176:179], v[0:15]
	ds_read_b128 v[176:179], v193 offset:36864
	v_mfma_f32_32x32x16_f16 v[16:31], a[184:187], v[180:183], v[16:31]
	ds_read_b128 v[180:183], v193 offset:37888
	v_mfma_f32_32x32x16_f16 v[0:15], a[188:191], v[184:187], v[0:15]
	ds_read_b128 v[184:187], v193 offset:38912
	v_mfma_f32_32x32x16_f16 v[16:31], a[188:191], v[188:191], v[16:31]
	ds_read_b128 v[188:191], v193 offset:39936
	s_add_u32 s44, s34, 0x8000
	s_addc_u32 s45, s35, 0
	s_mov_b32 m0, s54
	s_nop 0
	global_load_lds_dwordx4 v192, s[44:45] sc1
	s_waitcnt lgkmcnt(4)
	v_mfma_f32_32x32x16_f16 v[0:15], a[192:195], v[160:163], v[0:15]
	ds_read_b128 v[160:163], v193 offset:40960
	v_mfma_f32_32x32x16_f16 v[16:31], a[192:195], v[164:167], v[16:31]
	ds_read_b128 v[164:167], v193 offset:41984
	v_mfma_f32_32x32x16_f16 v[0:15], a[196:199], v[168:171], v[0:15]
	ds_read_b128 v[168:171], v193 offset:43008
	v_mfma_f32_32x32x16_f16 v[16:31], a[196:199], v[172:175], v[16:31]
	ds_read_b128 v[172:175], v193 offset:44032
	global_load_lds_dwordx4 v192, s[44:45] offset:1024 sc1
	s_waitcnt lgkmcnt(4)
	v_mfma_f32_32x32x16_f16 v[0:15], a[200:203], v[176:179], v[0:15]
	ds_read_b128 v[176:179], v193 offset:45056
	v_mfma_f32_32x32x16_f16 v[16:31], a[200:203], v[180:183], v[16:31]
	ds_read_b128 v[180:183], v193 offset:46080
	v_mfma_f32_32x32x16_f16 v[0:15], a[204:207], v[184:187], v[0:15]
	ds_read_b128 v[184:187], v193 offset:47104
	v_mfma_f32_32x32x16_f16 v[16:31], a[204:207], v[188:191], v[16:31]
	ds_read_b128 v[188:191], v193 offset:48128
	global_load_lds_dwordx4 v192, s[44:45] offset:2048 sc1
	s_waitcnt vmcnt(4)
	s_barrier
	v_mov_b32_e32 v199, 4
	s_cmp_eq_u32 s31, 0
	s_cbranch_scc1 .LD_slow24
	global_store_dword v197, v199, s[40:41]
	s_branch .LD_join25

.LD_join25:
	ds_read_b64 v[200:201], v249 offset:1536
	ds_read_b64 v[202:203], v249 offset:3584
	ds_read_b64 v[204:205], v249 offset:5632
	ds_read_b64 v[206:207], v249 offset:7680
	s_waitcnt lgkmcnt(8)
	v_mfma_f32_32x32x16_f16 v[0:15], a[208:211], v[160:163], v[0:15]
	ds_read_b128 v[160:163], v193 offset:49152
	v_mfma_f32_32x32x16_f16 v[16:31], a[208:211], v[164:167], v[16:31]
	ds_read_b128 v[164:167], v193 offset:50176
	v_mfma_f32_32x32x16_f16 v[0:15], a[212:215], v[168:171], v[0:15]
	ds_read_b128 v[168:171], v193 offset:51200
	v_mfma_f32_32x32x16_f16 v[16:31], a[212:215], v[172:175], v[16:31]
	ds_read_b128 v[172:175], v193 offset:52224
	global_load_lds_dwordx4 v192, s[44:45] offset:3072 sc1
	s_waitcnt lgkmcnt(8)
	v_mfma_f32_32x32x16_f16 v[0:15], a[216:219], v[176:179], v[0:15]
	ds_read_b128 v[176:179], v193 offset:53248
	v_mfma_f32_32x32x16_f16 v[16:31], a[216:219], v[180:183], v[16:31]
	ds_read_b128 v[180:183], v193 offset:54272
	v_mfma_f32_32x32x16_f16 v[0:15], a[220:223], v[184:187], v[0:15]
	ds_read_b128 v[184:187], v193 offset:55296
	v_mfma_f32_32x32x16_f16 v[16:31], a[220:223], v[188:191], v[16:31]
	ds_read_b128 v[188:191], v193 offset:56320
	s_add_u32 s44, s34, 0x9000
	s_addc_u32 s45, s35, 0
	s_mov_b32 m0, s55
	s_nop 0
	global_load_lds_dwordx4 v192, s[44:45] sc1
	s_waitcnt lgkmcnt(4)
	v_mfma_f32_32x32x16_f16 v[0:15], a[224:227], v[160:163], v[0:15]
	ds_read_b128 v[160:163], v193 offset:57344
	v_mfma_f32_32x32x16_f16 v[16:31], a[224:227], v[164:167], v[16:31]
	ds_read_b128 v[164:167], v193 offset:58368
	v_mfma_f32_32x32x16_f16 v[0:15], a[228:231], v[168:171], v[0:15]
	ds_read_b128 v[168:171], v193 offset:59392
	v_mfma_f32_32x32x16_f16 v[16:31], a[228:231], v[172:175], v[16:31]
	ds_read_b128 v[172:175], v193 offset:60416
	global_load_lds_dwordx4 v192, s[44:45] offset:1024 sc1
	v_add_f32_e32 v200, v200, v202
	v_add_f32_e32 v201, v201, v203
	v_add_f32_e32 v200, v200, v204
	v_add_f32_e32 v201, v201, v205
	v_add_f32_e32 v200, v200, v206
	v_add_f32_e32 v201, v201, v207
	global_store_dwordx2 v250, v[200:201], s[72:73]
	s_waitcnt lgkmcnt(4)
	v_mfma_f32_32x32x16_f16 v[0:15], a[232:235], v[176:179], v[0:15]
	ds_read_b128 v[176:179], v193 offset:61440
	v_mfma_f32_32x32x16_f16 v[16:31], a[232:235], v[180:183], v[16:31]
	ds_read_b128 v[180:183], v193 offset:62464
	v_mfma_f32_32x32x16_f16 v[0:15], a[236:239], v[184:187], v[0:15]
	ds_read_b128 v[184:187], v193 offset:63488
	v_mfma_f32_32x32x16_f16 v[16:31], a[236:239], v[188:191], v[16:31]
	ds_read_b128 v[188:191], v193 offset:64512
	global_load_lds_dwordx4 v192, s[44:45] offset:2048 sc1
	s_waitcnt vmcnt(9)
	s_barrier
	s_waitcnt lgkmcnt(4)
	v_mfma_f32_32x32x16_f16 v[0:15], a[240:243], v[160:163], v[0:15]
	ds_read_b128 v[160:163], v192 offset:0
	v_mfma_f32_32x32x16_f16 v[16:31], a[240:243], v[164:167], v[16:31]
	ds_read_b128 v[164:167], v192 offset:1024
	v_mfma_f32_32x32x16_f16 v[0:15], a[244:247], v[168:171], v[0:15]
	ds_read_b128 v[168:171], v192 offset:2048
	v_mfma_f32_32x32x16_f16 v[16:31], a[244:247], v[172:175], v[16:31]
	ds_read_b128 v[172:175], v192 offset:3072
	global_load_lds_dwordx4 v192, s[44:45] offset:3072 sc1
	s_waitcnt lgkmcnt(4)
	v_mfma_f32_32x32x16_f16 v[0:15], a[248:251], v[176:179], v[0:15]
	ds_read_b128 v[176:179], v192 offset:4096
	v_mfma_f32_32x32x16_f16 v[16:31], a[248:251], v[180:183], v[16:31]
	ds_read_b128 v[180:183], v192 offset:5120
	v_mfma_f32_32x32x16_f16 v[0:15], a[252:255], v[184:187], v[0:15]
	ds_read_b128 v[184:187], v192 offset:6144
	v_mfma_f32_32x32x16_f16 v[16:31], a[252:255], v[188:191], v[16:31]
	ds_read_b128 v[188:191], v192 offset:7168
	s_add_u32 s44, s34, 0x10000
	s_addc_u32 s45, s35, 0
	s_mov_b32 m0, s56
	s_nop 0
	global_load_lds_dwordx4 v192, s[44:45] sc1
	s_and_b32 s64, s33, 1
	s_lshl_b32 s64, s64, 22
	s_add_u32 s64, s64, s50
	s_add_u32 s36, s6, s64
	s_addc_u32 s37, s7, 0
	s_lshl_b32 s64, s33, 3
	s_add_u32 s64, s64, s29
	s_lshl_b32 s64, s64, 5
	s_add_u32 s64, s64, s30
	s_lshl_b32 s64, s64, 2
	s_add_u32 s40, s8, s64
	s_addc_u32 s41, s9, 0
	s_lshl_b32 s64, s33, 19
	s_add_u32 s72, s62, s64
	s_addc_u32 s73, s63, 0
	s_nop 3
	s_waitcnt lgkmcnt(4)
	v_mfma_f32_32x32x16_f16 v[32:47], a[0:3], v[160:163], v[32:47]
	ds_read_b128 v[160:163], v192 offset:8192
	v_exp_f32_e32 v200, v0
	v_mfma_f32_32x32x16_f16 v[48:63], a[0:3], v[164:167], v[48:63]
	ds_read_b128 v[164:167], v192 offset:9216
	v_exp_f32_e32 v201, v1
	v_add_f32_e32 v200, 1.0, v200
	v_mfma_f32_32x32x16_f16 v[32:47], a[4:7], v[168:171], v[32:47]
	ds_read_b128 v[168:171], v192 offset:10240
	v_exp_f32_e32 v202, v2
	v_add_f32_e32 v201, 1.0, v201
	v_mfma_f32_32x32x16_f16 v[48:63], a[4:7], v[172:175], v[48:63]
	ds_read_b128 v[172:175], v192 offset:11264
	global_load_lds_dwordx4 v192, s[44:45] offset:1024 sc1
	v_exp_f32_e32 v203, v3
	v_add_f32_e32 v202, 1.0, v202
	s_waitcnt lgkmcnt(4)
	v_mfma_f32_32x32x16_f16 v[32:47], a[8:11], v[176:179], v[32:47]
	ds_read_b128 v[176:179], v192 offset:12288
	v_exp_f32_e32 v204, v4
	v_add_f32_e32 v203, 1.0, v203
	v_mfma_f32_32x32x16_f16 v[48:63], a[8:11], v[180:183], v[48:63]
	ds_read_b128 v[180:183], v192 offset:13312
	v_exp_f32_e32 v205, v5
	v_add_f32_e32 v204, 1.0, v204
	v_mfma_f32_32x32x16_f16 v[32:47], a[12:15], v[184:187], v[32:47]
	ds_read_b128 v[184:187], v192 offset:14336
	v_exp_f32_e32 v206, v6
	v_add_f32_e32 v205, 1.0, v205
	v_mfma_f32_32x32x16_f16 v[48:63], a[12:15], v[188:191], v[48:63]
	ds_read_b128 v[188:191], v192 offset:15360
	global_load_lds_dwordx4 v192, s[44:45] offset:2048 sc1
	v_exp_f32_e32 v207, v7
	v_add_f32_e32 v206, 1.0, v206
	s_waitcnt lgkmcnt(4)
	v_mfma_f32_32x32x16_f16 v[32:47], a[16:19], v[160:163], v[32:47]
	ds_read_b128 v[160:163], v192 offset:16384
	v_exp_f32_e32 v208, v8
	v_add_f32_e32 v207, 1.0, v207
	v_mfma_f32_32x32x16_f16 v[48:63], a[16:19], v[164:167], v[48:63]
	ds_read_b128 v[164:167], v192 offset:17408
	v_exp_f32_e32 v209, v9
	v_add_f32_e32 v208, 1.0, v208
	v_mfma_f32_32x32x16_f16 v[32:47], a[20:23], v[168:171], v[32:47]
	ds_read_b128 v[168:171], v192 offset:18432
	v_exp_f32_e32 v210, v10
	v_add_f32_e32 v209, 1.0, v209
	v_mfma_f32_32x32x16_f16 v[48:63], a[20:23], v[172:175], v[48:63]
	ds_read_b128 v[172:175], v192 offset:19456
	global_load_lds_dwordx4 v192, s[44:45] offset:3072 sc1
	v_exp_f32_e32 v211, v11
	v_add_f32_e32 v210, 1.0, v210
	s_waitcnt lgkmcnt(4)
	v_mfma_f32_32x32x16_f16 v[32:47], a[24:27], v[176:179], v[32:47]
	ds_read_b128 v[176:179], v192 offset:20480
	v_exp_f32_e32 v212, v12
	v_add_f32_e32 v211, 1.0, v211
	v_mfma_f32_32x32x16_f16 v[48:63], a[24:27], v[180:183], v[48:63]
	ds_read_b128 v[180:183], v192 offset:21504
	v_exp_f32_e32 v213, v13
	v_add_f32_e32 v212, 1.0, v212
	v_mfma_f32_32x32x16_f16 v[32:47], a[28:31], v[184:187], v[32:47]
	ds_read_b128 v[184:187], v192 offset:22528
	v_exp_f32_e32 v214, v14
	v_add_f32_e32 v213, 1.0, v213
	v_mfma_f32_32x32x16_f16 v[48:63], a[28:31], v[188:191], v[48:63]
	ds_read_b128 v[188:191], v192 offset:23552
	s_add_u32 s44, s34, 0x11000
	s_addc_u32 s45, s35, 0
	s_mov_b32 m0, s57
	s_nop 0
	global_load_lds_dwordx4 v192, s[44:45] sc1
	v_exp_f32_e32 v215, v15
	v_add_f32_e32 v214, 1.0, v214
	s_waitcnt lgkmcnt(4)
	v_mfma_f32_32x32x16_f16 v[32:47], a[32:35], v[160:163], v[32:47]
	ds_read_b128 v[160:163], v192 offset:24576
	v_add_f32_e32 v215, 1.0, v215
	v_rcp_f32_e32 v200, v200
	v_mfma_f32_32x32x16_f16 v[48:63], a[32:35], v[164:167], v[48:63]
	ds_read_b128 v[164:167], v192 offset:25600
	v_rcp_f32_e32 v201, v201
	v_mfma_f32_32x32x16_f16 v[32:47], a[36:39], v[168:171], v[32:47]
	ds_read_b128 v[168:171], v192 offset:26624
	v_rcp_f32_e32 v202, v202
	v_mfma_f32_32x32x16_f16 v[48:63], a[36:39], v[172:175], v[48:63]
	ds_read_b128 v[172:175], v192 offset:27648
	global_load_lds_dwordx4 v192, s[44:45] offset:1024 sc1
	v_rcp_f32_e32 v203, v203
	s_waitcnt lgkmcnt(4)
	v_mfma_f32_32x32x16_f16 v[32:47], a[40:43], v[176:179], v[32:47]
	ds_read_b128 v[176:179], v192 offset:28672
	v_rcp_f32_e32 v204, v204
	v_mfma_f32_32x32x16_f16 v[48:63], a[40:43], v[180:183], v[48:63]
	ds_read_b128 v[180:183], v192 offset:29696
	v_rcp_f32_e32 v205, v205
	v_mul_f32_e32 v204, v204, v128
	v_mfma_f32_32x32x16_f16 v[32:47], a[44:47], v[184:187], v[32:47]
	ds_read_b128 v[184:187], v192 offset:30720
	v_rcp_f32_e32 v206, v206
	v_mul_f32_e32 v205, v205, v129
	v_mfma_f32_32x32x16_f16 v[48:63], a[44:47], v[188:191], v[48:63]
	ds_read_b128 v[188:191], v192 offset:31744
	global_load_lds_dwordx4 v192, s[44:45] offset:2048 sc1
	v_rcp_f32_e32 v207, v207
	v_mul_f32_e32 v206, v206, v130
	s_waitcnt vmcnt(7)
	s_barrier
	s_waitcnt lgkmcnt(4)
	v_mfma_f32_32x32x16_f16 v[32:47], a[48:51], v[160:163], v[32:47]
	ds_read_b128 v[160:163], v192 offset:32768
	v_rcp_f32_e32 v208, v208
	v_mul_f32_e32 v207, v207, v131
	s_add_u32 s46, s42, 0x6000
	s_addc_u32 s47, s43, 0
	global_load_dwordx4 v[96:99], v192, s[46:47] offset:0
	v_mfma_f32_32x32x16_f16 v[48:63], a[48:51], v[164:167], v[48:63]
	ds_read_b128 v[164:167], v192 offset:33792
	v_rcp_f32_e32 v209, v209
	v_fmamk_f32 v208, v208, 0xc0b8aa3b, v198
	global_load_dwordx4 v[100:103], v192, s[46:47] offset:1024
	global_load_dwordx4 v[104:107], v192, s[46:47] offset:2048
	v_mfma_f32_32x32x16_f16 v[32:47], a[52:55], v[168:171], v[32:47]
	ds_read_b128 v[168:171], v192 offset:34816
	v_rcp_f32_e32 v210, v210
	v_fmamk_f32 v209, v209, 0xc0b8aa3b, v198
	v_fma_f32 v128, v200, v208, v204
	global_load_dwordx4 v[108:111], v192, s[46:47] offset:3072
	s_add_u32 s46, s42, 0x7000
	s_addc_u32 s47, s43, 0
	v_mfma_f32_32x32x16_f16 v[48:63], a[52:55], v[172:175], v[48:63]
	ds_read_b128 v[172:175], v192 offset:35840
	global_load_lds_dwordx4 v192, s[44:45] offset:3072 sc1
	v_rcp_f32_e32 v211, v211
	v_fmamk_f32 v210, v210, 0xc0b8aa3b, v198
	v_fma_f32 v129, v201, v209, v205
	global_load_dwordx4 v[112:115], v192, s[46:47] offset:0
	global_load_dwordx4 v[116:119], v192, s[46:47] offset:1024
	s_waitcnt lgkmcnt(4)
	v_mfma_f32_32x32x16_f16 v[32:47], a[56:59], v[176:179], v[32:47]
	ds_read_b128 v[176:179], v192 offset:36864
	v_rcp_f32_e32 v212, v212
	v_fmamk_f32 v211, v211, 0xc0b8aa3b, v198
	v_fma_f32 v130, v202, v210, v206
	global_load_dwordx4 v[120:123], v192, s[46:47] offset:2048
	global_load_dwordx4 v[124:127], v192, s[46:47] offset:3072
	v_mfma_f32_32x32x16_f16 v[48:63], a[56:59], v[180:183], v[48:63]
	ds_read_b128 v[180:183], v192 offset:37888
	v_rcp_f32_e32 v213, v213
	v_fma_f32 v131, v203, v211, v207
	v_mfma_f32_32x32x16_f16 v[32:47], a[60:63], v[184:187], v[32:47]
	ds_read_b128 v[184:187], v192 offset:38912
	v_rcp_f32_e32 v214, v214
	v_mfma_f32_32x32x16_f16 v[48:63], a[60:63], v[188:191], v[48:63]
	ds_read_b128 v[188:191], v192 offset:39936
	s_add_u32 s44, s34, 0x18000
	s_addc_u32 s45, s35, 0
	s_mov_b32 m0, s58
	s_nop 0
	global_load_lds_dwordx4 v192, s[44:45] sc1
	v_rcp_f32_e32 v215, v215
	s_waitcnt lgkmcnt(4)
	v_mfma_f32_32x32x16_f16 v[32:47], a[64:67], v[160:163], v[32:47]
	ds_read_b128 v[160:163], v192 offset:40960
	v_exp_f32_e32 v200, v128
	v_mfma_f32_32x32x16_f16 v[48:63], a[64:67], v[164:167], v[48:63]
	ds_read_b128 v[164:167], v192 offset:41984
	v_exp_f32_e32 v201, v129
	v_add_f32_e32 v200, 1.0, v200
	v_mfma_f32_32x32x16_f16 v[32:47], a[68:71], v[168:171], v[32:47]
	ds_read_b128 v[168:171], v192 offset:43008
	v_exp_f32_e32 v202, v130
	v_add_f32_e32 v201, 1.0, v201
	v_mfma_f32_32x32x16_f16 v[48:63], a[68:71], v[172:175], v[48:63]
	ds_read_b128 v[172:175], v192 offset:44032
	global_load_lds_dwordx4 v192, s[44:45] offset:1024 sc1
	v_exp_f32_e32 v203, v131
	v_add_f32_e32 v202, 1.0, v202
	s_waitcnt lgkmcnt(4)
	v_mfma_f32_32x32x16_f16 v[32:47], a[72:75], v[176:179], v[32:47]
	ds_read_b128 v[176:179], v192 offset:45056
	v_add_f32_e32 v203, 1.0, v203
	v_rcp_f32_e32 v200, v200
	v_mfma_f32_32x32x16_f16 v[48:63], a[72:75], v[180:183], v[48:63]
	ds_read_b128 v[180:183], v192 offset:46080
	v_rcp_f32_e32 v201, v201
	v_fma_f32 v200, v200, 2.0, -1.0
	v_mfma_f32_32x32x16_f16 v[32:47], a[76:79], v[184:187], v[32:47]
	ds_read_b128 v[184:187], v192 offset:47104
	v_rcp_f32_e32 v202, v202
	v_fma_f32 v201, v201, 2.0, -1.0
	v_mul_f32_e32 v216, v212, v200
	v_mfma_f32_32x32x16_f16 v[48:63], a[76:79], v[188:191], v[48:63]
	ds_read_b128 v[188:191], v192 offset:48128
	global_load_lds_dwordx4 v192, s[44:45] offset:2048 sc1
	v_rcp_f32_e32 v203, v203
	v_fma_f32 v202, v202, 2.0, -1.0
	v_mul_f32_e32 v217, v213, v201
	s_waitcnt lgkmcnt(4)
	v_mfma_f32_32x32x16_f16 v[32:47], a[80:83], v[160:163], v[32:47]
	ds_read_b128 v[160:163], v192 offset:49152
	v_fma_f32 v203, v203, 2.0, -1.0
	v_mul_f32_e32 v218, v214, v202
	v_exp_f32_e32 v200, v16
	v_mfma_f32_32x32x16_f16 v[48:63], a[80:83], v[164:167], v[48:63]
	ds_read_b128 v[164:167], v192 offset:50176
	v_mul_f32_e32 v219, v215, v203
	v_mul_f32_e32 v236, v216, v228
	v_exp_f32_e32 v201, v17
	v_mfma_f32_32x32x16_f16 v[32:47], a[84:87], v[168:171], v[32:47]
	ds_read_b128 v[168:171], v192 offset:51200
	v_mul_f32_e32 v237, v216, v232
	v_fmac_f32_e32 v236, v217, v229
	v_exp_f32_e32 v202, v18
	v_mfma_f32_32x32x16_f16 v[48:63], a[84:87], v[172:175], v[48:63]
	ds_read_b128 v[172:175], v192 offset:52224
	global_load_lds_dwordx4 v192, s[44:45] offset:3072 sc1
	v_fmac_f32_e32 v237, v217, v233
	v_fmac_f32_e32 v236, v218, v230
	v_exp_f32_e32 v203, v19
	s_waitcnt lgkmcnt(4)
	v_mfma_f32_32x32x16_f16 v[32:47], a[88:91], v[176:179], v[32:47]
	ds_read_b128 v[176:179], v192 offset:53248
	v_fmac_f32_e32 v237, v218, v234
	v_fmac_f32_e32 v236, v219, v231
	v_exp_f32_e32 v204, v20
	v_mfma_f32_32x32x16_f16 v[48:63], a[88:91], v[180:183], v[48:63]
	ds_read_b128 v[180:183], v192 offset:54272
	v_fmac_f32_e32 v237, v219, v235
	v_mov_b32_e32 v238, v236
	v_exp_f32_e32 v205, v21
	v_mfma_f32_32x32x16_f16 v[32:47], a[92:95], v[184:187], v[32:47]
	ds_read_b128 v[184:187], v192 offset:55296
	v_mov_b32_e32 v239, v236
	v_mov_b32_e32 v240, v237
	v_exp_f32_e32 v206, v22
	v_mfma_f32_32x32x16_f16 v[48:63], a[92:95], v[188:191], v[48:63]
	ds_read_b128 v[188:191], v192 offset:56320
	s_add_u32 s44, s34, 0x19000
	s_addc_u32 s45, s35, 0
	s_mov_b32 m0, s59
	s_nop 0
	global_load_lds_dwordx4 v192, s[44:45] sc1
	s_lshl_b32 s64, s71, 3
	s_add_u32 s64, s64, s29
	s_lshl_b32 s64, s64, 7
	s_add_u32 s38, s8, s64
	s_addc_u32 s39, s9, 0
	global_load_dword v251, v196, s[38:39] sc1
	v_mov_b32_e32 v241, v237
	v_cvt_pk_f16_f32 v220, v216, v217
	v_exp_f32_e32 v207, v23
	s_waitcnt lgkmcnt(4)
	v_mfma_f32_32x32x16_f16 v[32:47], a[96:99], v[160:163], v[32:47]
	ds_read_b128 v[160:163], v192 offset:57344
	s_nop 1
	v_permlane32_swap_b32_e32 v238, v239
	v_permlane32_swap_b32_e32 v240, v241
	v_add_f32_e32 v238, v238, v239
	v_add_f32_e32 v239, v240, v241
	ds_write_b64 v248, v[238:239] offset:0
	v_exp_f32_e32 v208, v24
	v_mfma_f32_32x32x16_f16 v[48:63], a[96:99], v[164:167], v[48:63]
	ds_read_b128 v[164:167], v192 offset:58368
	v_cvt_pk_f16_f32 v221, v218, v219
	v_exp_f32_e32 v209, v25
	v_add_f32_e32 v200, 1.0, v200
	v_mfma_f32_32x32x16_f16 v[32:47], a[100:103], v[168:171], v[32:47]
	ds_read_b128 v[168:171], v192 offset:59392
	v_exp_f32_e32 v210, v26
	v_add_f32_e32 v201, 1.0, v201
	v_add_f32_e32 v202, 1.0, v202
	v_mfma_f32_32x32x16_f16 v[48:63], a[100:103], v[172:175], v[48:63]
	ds_read_b128 v[172:175], v192 offset:60416
	global_load_lds_dwordx4 v192, s[44:45] offset:1024 sc1
	v_exp_f32_e32 v211, v27
	v_add_f32_e32 v203, 1.0, v203
	v_add_f32_e32 v204, 1.0, v204
	s_waitcnt lgkmcnt(5)
	v_mfma_f32_32x32x16_f16 v[32:47], a[104:107], v[176:179], v[32:47]
	ds_read_b128 v[176:179], v192 offset:61440
	v_exp_f32_e32 v212, v28
	v_add_f32_e32 v205, 1.0, v205
	v_add_f32_e32 v206, 1.0, v206
	v_mfma_f32_32x32x16_f16 v[48:63], a[104:107], v[180:183], v[48:63]
	ds_read_b128 v[180:183], v192 offset:62464
	v_exp_f32_e32 v213, v29
	v_add_f32_e32 v207, 1.0, v207
	v_add_f32_e32 v208, 1.0, v208
	v_mfma_f32_32x32x16_f16 v[32:47], a[108:111], v[184:187], v[32:47]
	ds_read_b128 v[184:187], v192 offset:63488
	v_exp_f32_e32 v214, v30
	v_add_f32_e32 v209, 1.0, v209
	v_add_f32_e32 v210, 1.0, v210
	v_mfma_f32_32x32x16_f16 v[48:63], a[108:111], v[188:191], v[48:63]
	ds_read_b128 v[188:191], v192 offset:64512
	global_load_lds_dwordx4 v192, s[44:45] offset:2048 sc1
	v_exp_f32_e32 v215, v31
	v_add_f32_e32 v211, 1.0, v211
	v_add_f32_e32 v212, 1.0, v212
	s_waitcnt vmcnt(12)
	s_barrier
	s_waitcnt lgkmcnt(4)
	v_mfma_f32_32x32x16_f16 v[32:47], a[112:115], v[160:163], v[32:47]
	ds_read_b128 v[160:163], v193 offset:0
	v_add_f32_e32 v213, 1.0, v213
	v_add_f32_e32 v214, 1.0, v214
	v_rcp_f32_e32 v200, v200
	v_mfma_f32_32x32x16_f16 v[48:63], a[112:115], v[164:167], v[48:63]
	ds_read_b128 v[164:167], v193 offset:1024
	v_add_f32_e32 v215, 1.0, v215
	v_rcp_f32_e32 v201, v201
	v_mfma_f32_32x32x16_f16 v[32:47], a[116:119], v[168:171], v[32:47]
	ds_read_b128 v[168:171], v193 offset:2048
	v_rcp_f32_e32 v202, v202
	v_mfma_f32_32x32x16_f16 v[48:63], a[116:119], v[172:175], v[48:63]
	ds_read_b128 v[172:175], v193 offset:3072
	global_load_lds_dwordx4 v192, s[44:45] offset:3072 sc1
	v_rcp_f32_e32 v203, v203
	s_waitcnt lgkmcnt(4)
	v_mfma_f32_32x32x16_f16 v[32:47], a[120:123], v[176:179], v[32:47]
	ds_read_b128 v[176:179], v193 offset:4096
	v_rcp_f32_e32 v204, v204
	v_mfma_f32_32x32x16_f16 v[48:63], a[120:123], v[180:183], v[48:63]
	ds_read_b128 v[180:183], v193 offset:5120
	v_rcp_f32_e32 v205, v205
	v_mul_f32_e32 v204, v204, v132
	v_mfma_f32_32x32x16_f16 v[32:47], a[124:127], v[184:187], v[32:47]
	ds_read_b128 v[184:187], v193 offset:6144
	v_rcp_f32_e32 v206, v206
	v_mul_f32_e32 v205, v205, v133
	v_mfma_f32_32x32x16_f16 v[48:63], a[124:127], v[188:191], v[48:63]
	ds_read_b128 v[188:191], v193 offset:7168
	s_waitcnt vmcnt(3)
	v_cmp_gt_u32_e32 vcc, 3, v251
	s_cbranch_vccz .LD_tok26

.LD_tok26:
	s_and_b32 s64, s71, 1
	s_lshl_b32 s64, s64, 22
	s_add_u32 s64, s64, s49
	s_add_u32 s64, s64, 0x40000
	s_add_u32 s34, s6, s64
	s_addc_u32 s35, s7, 0
	s_add_u32 s44, s34, 0x0
	s_addc_u32 s45, s35, 0
	s_mov_b32 m0, s52
	s_nop 0
	global_load_lds_dwordx4 v192, s[44:45] sc1
	v_rcp_f32_e32 v207, v207
	v_mul_f32_e32 v206, v206, v134
	s_waitcnt lgkmcnt(4)
	v_mfma_f32_32x32x16_f16 v[32:47], a[128:131], v[160:163], v[32:47]
	ds_read_b128 v[160:163], v193 offset:8192
	v_rcp_f32_e32 v208, v208
	v_mul_f32_e32 v207, v207, v135
	v_mfma_f32_32x32x16_f16 v[48:63], a[128:131], v[164:167], v[48:63]
	ds_read_b128 v[164:167], v193 offset:9216
	v_rcp_f32_e32 v209, v209
	v_fmamk_f32 v208, v208, 0xc0b8aa3b, v198
	v_mfma_f32_32x32x16_f16 v[32:47], a[132:135], v[168:171], v[32:47]
	ds_read_b128 v[168:171], v193 offset:10240
	v_rcp_f32_e32 v210, v210
	v_fmamk_f32 v209, v209, 0xc0b8aa3b, v198
	v_fma_f32 v132, v200, v208, v204
	v_mfma_f32_32x32x16_f16 v[48:63], a[132:135], v[172:175], v[48:63]
	ds_read_b128 v[172:175], v193 offset:11264
	global_load_lds_dwordx4 v192, s[44:45] offset:1024 sc1
	v_rcp_f32_e32 v211, v211
	v_fmamk_f32 v210, v210, 0xc0b8aa3b, v198
	v_fma_f32 v133, v201, v209, v205
	s_waitcnt lgkmcnt(4)
	v_mfma_f32_32x32x16_f16 v[32:47], a[136:139], v[176:179], v[32:47]
	ds_read_b128 v[176:179], v193 offset:12288
	v_rcp_f32_e32 v212, v212
	v_fmamk_f32 v211, v211, 0xc0b8aa3b, v198
	v_fma_f32 v134, v202, v210, v206
	v_mfma_f32_32x32x16_f16 v[48:63], a[136:139], v[180:183], v[48:63]
	ds_read_b128 v[180:183], v193 offset:13312
	v_rcp_f32_e32 v213, v213
	v_fma_f32 v135, v203, v211, v207
	v_mfma_f32_32x32x16_f16 v[32:47], a[140:143], v[184:187], v[32:47]
	ds_read_b128 v[184:187], v193 offset:14336
	v_rcp_f32_e32 v214, v214
	v_mfma_f32_32x32x16_f16 v[48:63], a[140:143], v[188:191], v[48:63]
	ds_read_b128 v[188:191], v193 offset:15360
	global_load_lds_dwordx4 v192, s[44:45] offset:2048 sc1
	v_rcp_f32_e32 v215, v215
	s_waitcnt lgkmcnt(4)
	v_mfma_f32_32x32x16_f16 v[32:47], a[144:147], v[160:163], v[32:47]
	ds_read_b128 v[160:163], v193 offset:16384
	v_exp_f32_e32 v200, v132
	v_mfma_f32_32x32x16_f16 v[48:63], a[144:147], v[164:167], v[48:63]
	ds_read_b128 v[164:167], v193 offset:17408
	v_exp_f32_e32 v201, v133
	v_add_f32_e32 v200, 1.0, v200
	v_mfma_f32_32x32x16_f16 v[32:47], a[148:151], v[168:171], v[32:47]
	ds_read_b128 v[168:171], v193 offset:18432
	v_exp_f32_e32 v202, v134
	v_add_f32_e32 v201, 1.0, v201
	v_mfma_f32_32x32x16_f16 v[48:63], a[148:151], v[172:175], v[48:63]
	ds_read_b128 v[172:175], v193 offset:19456
	global_load_lds_dwordx4 v192, s[44:45] offset:3072 sc1
	v_exp_f32_e32 v203, v135
	v_add_f32_e32 v202, 1.0, v202
	s_waitcnt lgkmcnt(4)
	v_mfma_f32_32x32x16_f16 v[32:47], a[152:155], v[176:179], v[32:47]
	ds_read_b128 v[176:179], v193 offset:20480
	v_add_f32_e32 v203, 1.0, v203
	v_rcp_f32_e32 v200, v200
	v_mfma_f32_32x32x16_f16 v[48:63], a[152:155], v[180:183], v[48:63]
	ds_read_b128 v[180:183], v193 offset:21504
	v_rcp_f32_e32 v201, v201
	v_fma_f32 v200, v200, 2.0, -1.0
	v_mfma_f32_32x32x16_f16 v[32:47], a[156:159], v[184:187], v[32:47]
	ds_read_b128 v[184:187], v193 offset:22528
	v_rcp_f32_e32 v202, v202
	v_fma_f32 v201, v201, 2.0, -1.0
	v_mul_f32_e32 v216, v212, v200
	v_mfma_f32_32x32x16_f16 v[48:63], a[156:159], v[188:191], v[48:63]
	ds_read_b128 v[188:191], v193 offset:23552
	s_add_u32 s44, s34, 0x1000
	s_addc_u32 s45, s35, 0
	s_mov_b32 m0, s53
	s_nop 0
	global_load_lds_dwordx4 v192, s[44:45] sc1
	v_rcp_f32_e32 v203, v203
	v_fma_f32 v202, v202, 2.0, -1.0
	v_mul_f32_e32 v217, v213, v201
	s_waitcnt lgkmcnt(4)
	v_mfma_f32_32x32x16_f16 v[32:47], a[160:163], v[160:163], v[32:47]
	ds_read_b128 v[160:163], v193 offset:24576
	v_fma_f32 v203, v203, 2.0, -1.0
	v_mul_f32_e32 v218, v214, v202
	v_mfma_f32_32x32x16_f16 v[48:63], a[160:163], v[164:167], v[48:63]
	ds_read_b128 v[164:167], v193 offset:25600
	v_mul_f32_e32 v219, v215, v203
	v_mul_f32_e32 v236, v216, v228
	v_mfma_f32_32x32x16_f16 v[32:47], a[164:167], v[168:171], v[32:47]
	ds_read_b128 v[168:171], v193 offset:26624
	v_mul_f32_e32 v237, v216, v232
	v_fmac_f32_e32 v236, v217, v229
	v_mfma_f32_32x32x16_f16 v[48:63], a[164:167], v[172:175], v[48:63]
	ds_read_b128 v[172:175], v193 offset:27648
	global_load_lds_dwordx4 v192, s[44:45] offset:1024 sc1
	v_fmac_f32_e32 v237, v217, v233
	v_fmac_f32_e32 v236, v218, v230
	s_waitcnt lgkmcnt(4)
	v_mfma_f32_32x32x16_f16 v[32:47], a[168:171], v[176:179], v[32:47]
	ds_read_b128 v[176:179], v193 offset:28672
	v_fmac_f32_e32 v237, v218, v234
	v_fmac_f32_e32 v236, v219, v231
	v_mfma_f32_32x32x16_f16 v[48:63], a[168:171], v[180:183], v[48:63]
	ds_read_b128 v[180:183], v193 offset:29696
	v_fmac_f32_e32 v237, v219, v235
	v_mov_b32_e32 v238, v236
	v_mfma_f32_32x32x16_f16 v[32:47], a[172:175], v[184:187], v[32:47]
	ds_read_b128 v[184:187], v193 offset:30720
	v_mov_b32_e32 v239, v236
	v_mov_b32_e32 v240, v237
	v_mfma_f32_32x32x16_f16 v[48:63], a[172:175], v[188:191], v[48:63]
	ds_read_b128 v[188:191], v193 offset:31744
	global_load_lds_dwordx4 v192, s[44:45] offset:2048 sc1
	v_mov_b32_e32 v241, v237
	v_cvt_pk_f16_f32 v222, v216, v217
	s_waitcnt vmcnt(7)
	s_barrier
	s_waitcnt lgkmcnt(4)
	v_mfma_f32_32x32x16_f16 v[32:47], a[176:179], v[160:163], v[32:47]
	ds_read_b128 v[160:163], v193 offset:32768
	s_nop 1
	v_permlane32_swap_b32_e32 v238, v239
	v_permlane32_swap_b32_e32 v240, v241
	v_add_f32_e32 v238, v238, v239
	v_add_f32_e32 v239, v240, v241
	ds_write_b64 v248, v[238:239] offset:256
	v_mfma_f32_32x32x16_f16 v[48:63], a[176:179], v[164:167], v[48:63]
	ds_read_b128 v[164:167], v193 offset:33792
	v_cvt_pk_f16_f32 v223, v218, v219
	v_mfma_f32_32x32x16_f16 v[32:47], a[180:183], v[168:171], v[32:47]
	ds_read_b128 v[168:171], v193 offset:34816
	s_nop 1
	v_permlane32_swap_b32_e32 v220, v222
	v_permlane32_swap_b32_e32 v221, v223
	s_cmp_eq_u32 s31, 0
	s_cbranch_scc1 .LD_slow28
	global_store_dwordx4 v195, v[220:223], s[36:37] offset:0
	s_branch .LD_join29

.LD_join29:
	v_mfma_f32_32x32x16_f16 v[48:63], a[180:183], v[172:175], v[48:63]
	ds_read_b128 v[172:175], v193 offset:35840
	global_load_lds_dwordx4 v192, s[44:45] offset:3072 sc1
	s_waitcnt lgkmcnt(5)
	v_mfma_f32_32x32x16_f16 v[32:47], a[184:187], v[176:179], v[32:47]
	ds_read_b128 v[176:179], v193 offset:36864
	v_mfma_f32_32x32x16_f16 v[48:63], a[184:187], v[180:183], v[48:63]
	ds_read_b128 v[180:183], v193 offset:37888
	v_mfma_f32_32x32x16_f16 v[32:47], a[188:191], v[184:187], v[32:47]
	ds_read_b128 v[184:187], v193 offset:38912
	v_mfma_f32_32x32x16_f16 v[48:63], a[188:191], v[188:191], v[48:63]
	ds_read_b128 v[188:191], v193 offset:39936
	s_add_u32 s44, s34, 0x8000
	s_addc_u32 s45, s35, 0
	s_mov_b32 m0, s54
	s_nop 0
	global_load_lds_dwordx4 v192, s[44:45] sc1
	s_waitcnt lgkmcnt(4)
	v_mfma_f32_32x32x16_f16 v[32:47], a[192:195], v[160:163], v[32:47]
	ds_read_b128 v[160:163], v193 offset:40960
	v_mfma_f32_32x32x16_f16 v[48:63], a[192:195], v[164:167], v[48:63]
	ds_read_b128 v[164:167], v193 offset:41984
	v_mfma_f32_32x32x16_f16 v[32:47], a[196:199], v[168:171], v[32:47]
	ds_read_b128 v[168:171], v193 offset:43008
	v_mfma_f32_32x32x16_f16 v[48:63], a[196:199], v[172:175], v[48:63]
	ds_read_b128 v[172:175], v193 offset:44032
	global_load_lds_dwordx4 v192, s[44:45] offset:1024 sc1
	s_waitcnt lgkmcnt(4)
	v_mfma_f32_32x32x16_f16 v[32:47], a[200:203], v[176:179], v[32:47]
	ds_read_b128 v[176:179], v193 offset:45056
	v_mfma_f32_32x32x16_f16 v[48:63], a[200:203], v[180:183], v[48:63]
	ds_read_b128 v[180:183], v193 offset:46080
	v_mfma_f32_32x32x16_f16 v[32:47], a[204:207], v[184:187], v[32:47]
	ds_read_b128 v[184:187], v193 offset:47104
	v_mfma_f32_32x32x16_f16 v[48:63], a[204:207], v[188:191], v[48:63]
	ds_read_b128 v[188:191], v193 offset:48128
	global_load_lds_dwordx4 v192, s[44:45] offset:2048 sc1
	s_waitcnt vmcnt(4)
	s_barrier
	v_mov_b32_e32 v199, 1
	s_cmp_eq_u32 s31, 0
	s_cbranch_scc1 .LD_slow30
	global_store_dword v197, v199, s[40:41]
	s_branch .LD_join31

.LD_join31:
	ds_read_b64 v[200:201], v249 offset:0
	ds_read_b64 v[202:203], v249 offset:2048
	ds_read_b64 v[204:205], v249 offset:4096
	ds_read_b64 v[206:207], v249 offset:6144
	s_waitcnt lgkmcnt(8)
	v_mfma_f32_32x32x16_f16 v[32:47], a[208:211], v[160:163], v[32:47]
	ds_read_b128 v[160:163], v193 offset:49152
	v_mfma_f32_32x32x16_f16 v[48:63], a[208:211], v[164:167], v[48:63]
	ds_read_b128 v[164:167], v193 offset:50176
	v_mfma_f32_32x32x16_f16 v[32:47], a[212:215], v[168:171], v[32:47]
	ds_read_b128 v[168:171], v193 offset:51200
	v_mfma_f32_32x32x16_f16 v[48:63], a[212:215], v[172:175], v[48:63]
	ds_read_b128 v[172:175], v193 offset:52224
	global_load_lds_dwordx4 v192, s[44:45] offset:3072 sc1
	s_waitcnt lgkmcnt(8)
	v_mfma_f32_32x32x16_f16 v[32:47], a[216:219], v[176:179], v[32:47]
	ds_read_b128 v[176:179], v193 offset:53248
	v_mfma_f32_32x32x16_f16 v[48:63], a[216:219], v[180:183], v[48:63]
	ds_read_b128 v[180:183], v193 offset:54272
	v_mfma_f32_32x32x16_f16 v[32:47], a[220:223], v[184:187], v[32:47]
	ds_read_b128 v[184:187], v193 offset:55296
	v_mfma_f32_32x32x16_f16 v[48:63], a[220:223], v[188:191], v[48:63]
	ds_read_b128 v[188:191], v193 offset:56320
	s_add_u32 s44, s34, 0x9000
	s_addc_u32 s45, s35, 0
	s_mov_b32 m0, s55
	s_nop 0
	global_load_lds_dwordx4 v192, s[44:45] sc1
	s_waitcnt lgkmcnt(4)
	v_mfma_f32_32x32x16_f16 v[32:47], a[224:227], v[160:163], v[32:47]
	ds_read_b128 v[160:163], v193 offset:57344
	v_mfma_f32_32x32x16_f16 v[48:63], a[224:227], v[164:167], v[48:63]
	ds_read_b128 v[164:167], v193 offset:58368
	v_mfma_f32_32x32x16_f16 v[32:47], a[228:231], v[168:171], v[32:47]
	ds_read_b128 v[168:171], v193 offset:59392
	v_mfma_f32_32x32x16_f16 v[48:63], a[228:231], v[172:175], v[48:63]
	ds_read_b128 v[172:175], v193 offset:60416
	global_load_lds_dwordx4 v192, s[44:45] offset:1024 sc1
	v_add_f32_e32 v200, v200, v202
	v_add_f32_e32 v201, v201, v203
	v_add_f32_e32 v200, v200, v204
	v_add_f32_e32 v201, v201, v205
	v_add_f32_e32 v200, v200, v206
	v_add_f32_e32 v201, v201, v207
	global_store_dwordx2 v250, v[200:201], s[72:73]
	s_waitcnt lgkmcnt(4)
	v_mfma_f32_32x32x16_f16 v[32:47], a[232:235], v[176:179], v[32:47]
	ds_read_b128 v[176:179], v193 offset:61440
	v_mfma_f32_32x32x16_f16 v[48:63], a[232:235], v[180:183], v[48:63]
	ds_read_b128 v[180:183], v193 offset:62464
	v_mfma_f32_32x32x16_f16 v[32:47], a[236:239], v[184:187], v[32:47]
	ds_read_b128 v[184:187], v193 offset:63488
	v_mfma_f32_32x32x16_f16 v[48:63], a[236:239], v[188:191], v[48:63]
	ds_read_b128 v[188:191], v193 offset:64512
	global_load_lds_dwordx4 v192, s[44:45] offset:2048 sc1
	s_waitcnt vmcnt(9)
	s_barrier
	s_waitcnt lgkmcnt(4)
	v_mfma_f32_32x32x16_f16 v[32:47], a[240:243], v[160:163], v[32:47]
	ds_read_b128 v[160:163], v192 offset:0
	v_mfma_f32_32x32x16_f16 v[48:63], a[240:243], v[164:167], v[48:63]
	ds_read_b128 v[164:167], v192 offset:1024
	v_mfma_f32_32x32x16_f16 v[32:47], a[244:247], v[168:171], v[32:47]
	ds_read_b128 v[168:171], v192 offset:2048
	v_mfma_f32_32x32x16_f16 v[48:63], a[244:247], v[172:175], v[48:63]
	ds_read_b128 v[172:175], v192 offset:3072
	global_load_lds_dwordx4 v192, s[44:45] offset:3072 sc1
	s_waitcnt lgkmcnt(4)
	v_mfma_f32_32x32x16_f16 v[32:47], a[248:251], v[176:179], v[32:47]
	ds_read_b128 v[176:179], v192 offset:4096
	v_mfma_f32_32x32x16_f16 v[48:63], a[248:251], v[180:183], v[48:63]
	ds_read_b128 v[180:183], v192 offset:5120
	v_mfma_f32_32x32x16_f16 v[32:47], a[252:255], v[184:187], v[32:47]
	ds_read_b128 v[184:187], v192 offset:6144
	v_mfma_f32_32x32x16_f16 v[48:63], a[252:255], v[188:191], v[48:63]
	ds_read_b128 v[188:191], v192 offset:7168
	s_add_u32 s44, s34, 0x10000
	s_addc_u32 s45, s35, 0
	s_mov_b32 m0, s56
	s_nop 0
	global_load_lds_dwordx4 v192, s[44:45] sc1
	s_and_b32 s64, s33, 1
	s_lshl_b32 s64, s64, 22
	s_add_u32 s64, s64, s50
	s_add_u32 s64, s64, 0x20000
	s_add_u32 s36, s6, s64
	s_addc_u32 s37, s7, 0
	s_lshl_b32 s64, s33, 3
	s_add_u32 s64, s64, s29
	s_lshl_b32 s64, s64, 5
	s_add_u32 s64, s64, s30
	s_lshl_b32 s64, s64, 2
	s_add_u32 s40, s8, s64
	s_addc_u32 s41, s9, 0
	s_lshl_b32 s64, s33, 19
	s_add_u32 s64, s64, 0x200
	s_add_u32 s72, s62, s64
	s_addc_u32 s73, s63, 0
	s_nop 3
	s_waitcnt lgkmcnt(4)
	v_mfma_f32_32x32x16_f16 v[64:79], a[0:3], v[160:163], v[64:79]
	ds_read_b128 v[160:163], v192 offset:8192
	v_exp_f32_e32 v200, v32
	v_mfma_f32_32x32x16_f16 v[80:95], a[0:3], v[164:167], v[80:95]
	ds_read_b128 v[164:167], v192 offset:9216
	v_exp_f32_e32 v201, v33
	v_add_f32_e32 v200, 1.0, v200
	v_mfma_f32_32x32x16_f16 v[64:79], a[4:7], v[168:171], v[64:79]
	ds_read_b128 v[168:171], v192 offset:10240
	v_exp_f32_e32 v202, v34
	v_add_f32_e32 v201, 1.0, v201
	v_mfma_f32_32x32x16_f16 v[80:95], a[4:7], v[172:175], v[80:95]
	ds_read_b128 v[172:175], v192 offset:11264
	global_load_lds_dwordx4 v192, s[44:45] offset:1024 sc1
	v_exp_f32_e32 v203, v35
	v_add_f32_e32 v202, 1.0, v202
	s_waitcnt lgkmcnt(4)
	v_mfma_f32_32x32x16_f16 v[64:79], a[8:11], v[176:179], v[64:79]
	ds_read_b128 v[176:179], v192 offset:12288
	v_exp_f32_e32 v204, v36
	v_add_f32_e32 v203, 1.0, v203
	v_mfma_f32_32x32x16_f16 v[80:95], a[8:11], v[180:183], v[80:95]
	ds_read_b128 v[180:183], v192 offset:13312
	v_exp_f32_e32 v205, v37
	v_add_f32_e32 v204, 1.0, v204
	v_mfma_f32_32x32x16_f16 v[64:79], a[12:15], v[184:187], v[64:79]
	ds_read_b128 v[184:187], v192 offset:14336
	v_exp_f32_e32 v206, v38
	v_add_f32_e32 v205, 1.0, v205
	v_mfma_f32_32x32x16_f16 v[80:95], a[12:15], v[188:191], v[80:95]
	ds_read_b128 v[188:191], v192 offset:15360
	global_load_lds_dwordx4 v192, s[44:45] offset:2048 sc1
	v_exp_f32_e32 v207, v39
	v_add_f32_e32 v206, 1.0, v206
	s_waitcnt lgkmcnt(4)
	v_mfma_f32_32x32x16_f16 v[64:79], a[16:19], v[160:163], v[64:79]
	ds_read_b128 v[160:163], v192 offset:16384
	v_exp_f32_e32 v208, v40
	v_add_f32_e32 v207, 1.0, v207
	v_mfma_f32_32x32x16_f16 v[80:95], a[16:19], v[164:167], v[80:95]
	ds_read_b128 v[164:167], v192 offset:17408
	v_exp_f32_e32 v209, v41
	v_add_f32_e32 v208, 1.0, v208
	v_mfma_f32_32x32x16_f16 v[64:79], a[20:23], v[168:171], v[64:79]
	ds_read_b128 v[168:171], v192 offset:18432
	v_exp_f32_e32 v210, v42
	v_add_f32_e32 v209, 1.0, v209
	v_mfma_f32_32x32x16_f16 v[80:95], a[20:23], v[172:175], v[80:95]
	ds_read_b128 v[172:175], v192 offset:19456
	global_load_lds_dwordx4 v192, s[44:45] offset:3072 sc1
	v_exp_f32_e32 v211, v43
	v_add_f32_e32 v210, 1.0, v210
	s_waitcnt lgkmcnt(4)
	v_mfma_f32_32x32x16_f16 v[64:79], a[24:27], v[176:179], v[64:79]
	ds_read_b128 v[176:179], v192 offset:20480
	v_exp_f32_e32 v212, v44
	v_add_f32_e32 v211, 1.0, v211
	v_mfma_f32_32x32x16_f16 v[80:95], a[24:27], v[180:183], v[80:95]
	ds_read_b128 v[180:183], v192 offset:21504
	v_exp_f32_e32 v213, v45
	v_add_f32_e32 v212, 1.0, v212
	v_mfma_f32_32x32x16_f16 v[64:79], a[28:31], v[184:187], v[64:79]
	ds_read_b128 v[184:187], v192 offset:22528
	v_exp_f32_e32 v214, v46
	v_add_f32_e32 v213, 1.0, v213
	v_mfma_f32_32x32x16_f16 v[80:95], a[28:31], v[188:191], v[80:95]
	ds_read_b128 v[188:191], v192 offset:23552
	s_add_u32 s44, s34, 0x11000
	s_addc_u32 s45, s35, 0
	s_mov_b32 m0, s57
	s_nop 0
	global_load_lds_dwordx4 v192, s[44:45] sc1
	v_exp_f32_e32 v215, v47
	v_add_f32_e32 v214, 1.0, v214
	s_waitcnt lgkmcnt(4)
	v_mfma_f32_32x32x16_f16 v[64:79], a[32:35], v[160:163], v[64:79]
	ds_read_b128 v[160:163], v192 offset:24576
	v_add_f32_e32 v215, 1.0, v215
	v_rcp_f32_e32 v200, v200
	v_mfma_f32_32x32x16_f16 v[80:95], a[32:35], v[164:167], v[80:95]
	ds_read_b128 v[164:167], v192 offset:25600
	v_rcp_f32_e32 v201, v201
	v_mfma_f32_32x32x16_f16 v[64:79], a[36:39], v[168:171], v[64:79]
	ds_read_b128 v[168:171], v192 offset:26624
	v_rcp_f32_e32 v202, v202
	v_mfma_f32_32x32x16_f16 v[80:95], a[36:39], v[172:175], v[80:95]
	ds_read_b128 v[172:175], v192 offset:27648
	global_load_lds_dwordx4 v192, s[44:45] offset:1024 sc1
	v_rcp_f32_e32 v203, v203
	s_waitcnt lgkmcnt(4)
	v_mfma_f32_32x32x16_f16 v[64:79], a[40:43], v[176:179], v[64:79]
	ds_read_b128 v[176:179], v192 offset:28672
	v_rcp_f32_e32 v204, v204
	v_mfma_f32_32x32x16_f16 v[80:95], a[40:43], v[180:183], v[80:95]
	ds_read_b128 v[180:183], v192 offset:29696
	v_rcp_f32_e32 v205, v205
	v_mul_f32_e32 v204, v204, v136
	v_mfma_f32_32x32x16_f16 v[64:79], a[44:47], v[184:187], v[64:79]
	ds_read_b128 v[184:187], v192 offset:30720
	v_rcp_f32_e32 v206, v206
	v_mul_f32_e32 v205, v205, v137
	v_mfma_f32_32x32x16_f16 v[80:95], a[44:47], v[188:191], v[80:95]
	ds_read_b128 v[188:191], v192 offset:31744
	global_load_lds_dwordx4 v192, s[44:45] offset:2048 sc1
	v_rcp_f32_e32 v207, v207
	v_mul_f32_e32 v206, v206, v138
	s_waitcnt vmcnt(7)
	s_barrier
	s_waitcnt lgkmcnt(4)
	v_mfma_f32_32x32x16_f16 v[64:79], a[48:51], v[160:163], v[64:79]
	ds_read_b128 v[160:163], v192 offset:32768
	v_rcp_f32_e32 v208, v208
	v_mul_f32_e32 v207, v207, v139
	s_add_u32 s46, s42, 0x0
	s_addc_u32 s47, s43, 0
	global_load_dwordx4 v[0:3], v192, s[46:47] offset:0
	v_mfma_f32_32x32x16_f16 v[80:95], a[48:51], v[164:167], v[80:95]
	ds_read_b128 v[164:167], v192 offset:33792
	v_rcp_f32_e32 v209, v209
	v_fmamk_f32 v208, v208, 0xc0b8aa3b, v198
	global_load_dwordx4 v[4:7], v192, s[46:47] offset:1024
	global_load_dwordx4 v[8:11], v192, s[46:47] offset:2048
	v_mfma_f32_32x32x16_f16 v[64:79], a[52:55], v[168:171], v[64:79]
	ds_read_b128 v[168:171], v192 offset:34816
	v_rcp_f32_e32 v210, v210
	v_fmamk_f32 v209, v209, 0xc0b8aa3b, v198
	v_fma_f32 v136, v200, v208, v204
	global_load_dwordx4 v[12:15], v192, s[46:47] offset:3072
	s_add_u32 s46, s42, 0x1000
	s_addc_u32 s47, s43, 0
	v_mfma_f32_32x32x16_f16 v[80:95], a[52:55], v[172:175], v[80:95]
	ds_read_b128 v[172:175], v192 offset:35840
	global_load_lds_dwordx4 v192, s[44:45] offset:3072 sc1
	v_rcp_f32_e32 v211, v211
	v_fmamk_f32 v210, v210, 0xc0b8aa3b, v198
	v_fma_f32 v137, v201, v209, v205
	global_load_dwordx4 v[16:19], v192, s[46:47] offset:0
	global_load_dwordx4 v[20:23], v192, s[46:47] offset:1024
	s_waitcnt lgkmcnt(4)
	v_mfma_f32_32x32x16_f16 v[64:79], a[56:59], v[176:179], v[64:79]
	ds_read_b128 v[176:179], v192 offset:36864
	v_rcp_f32_e32 v212, v212
	v_fmamk_f32 v211, v211, 0xc0b8aa3b, v198
	v_fma_f32 v138, v202, v210, v206
	global_load_dwordx4 v[24:27], v192, s[46:47] offset:2048
	global_load_dwordx4 v[28:31], v192, s[46:47] offset:3072
	v_mfma_f32_32x32x16_f16 v[80:95], a[56:59], v[180:183], v[80:95]
	ds_read_b128 v[180:183], v192 offset:37888
	v_rcp_f32_e32 v213, v213
	v_fma_f32 v139, v203, v211, v207
	v_mfma_f32_32x32x16_f16 v[64:79], a[60:63], v[184:187], v[64:79]
	ds_read_b128 v[184:187], v192 offset:38912
	v_rcp_f32_e32 v214, v214
	v_mfma_f32_32x32x16_f16 v[80:95], a[60:63], v[188:191], v[80:95]
	ds_read_b128 v[188:191], v192 offset:39936
	s_add_u32 s44, s34, 0x18000
	s_addc_u32 s45, s35, 0
	s_mov_b32 m0, s58
	s_nop 0
	global_load_lds_dwordx4 v192, s[44:45] sc1
	v_rcp_f32_e32 v215, v215
	s_waitcnt lgkmcnt(4)
	v_mfma_f32_32x32x16_f16 v[64:79], a[64:67], v[160:163], v[64:79]
	ds_read_b128 v[160:163], v192 offset:40960
	v_exp_f32_e32 v200, v136
	v_mfma_f32_32x32x16_f16 v[80:95], a[64:67], v[164:167], v[80:95]
	ds_read_b128 v[164:167], v192 offset:41984
	v_exp_f32_e32 v201, v137
	v_add_f32_e32 v200, 1.0, v200
	v_mfma_f32_32x32x16_f16 v[64:79], a[68:71], v[168:171], v[64:79]
	ds_read_b128 v[168:171], v192 offset:43008
	v_exp_f32_e32 v202, v138
	v_add_f32_e32 v201, 1.0, v201
	v_mfma_f32_32x32x16_f16 v[80:95], a[68:71], v[172:175], v[80:95]
	ds_read_b128 v[172:175], v192 offset:44032
	global_load_lds_dwordx4 v192, s[44:45] offset:1024 sc1
	v_exp_f32_e32 v203, v139
	v_add_f32_e32 v202, 1.0, v202
	s_waitcnt lgkmcnt(4)
	v_mfma_f32_32x32x16_f16 v[64:79], a[72:75], v[176:179], v[64:79]
	ds_read_b128 v[176:179], v192 offset:45056
	v_add_f32_e32 v203, 1.0, v203
	v_rcp_f32_e32 v200, v200
	v_mfma_f32_32x32x16_f16 v[80:95], a[72:75], v[180:183], v[80:95]
	ds_read_b128 v[180:183], v192 offset:46080
	v_rcp_f32_e32 v201, v201
	v_fma_f32 v200, v200, 2.0, -1.0
	v_mfma_f32_32x32x16_f16 v[64:79], a[76:79], v[184:187], v[64:79]
	ds_read_b128 v[184:187], v192 offset:47104
	v_rcp_f32_e32 v202, v202
	v_fma_f32 v201, v201, 2.0, -1.0
	v_mul_f32_e32 v216, v212, v200
	v_mfma_f32_32x32x16_f16 v[80:95], a[76:79], v[188:191], v[80:95]
	ds_read_b128 v[188:191], v192 offset:48128
	global_load_lds_dwordx4 v192, s[44:45] offset:2048 sc1
	v_rcp_f32_e32 v203, v203
	v_fma_f32 v202, v202, 2.0, -1.0
	v_mul_f32_e32 v217, v213, v201
	s_waitcnt lgkmcnt(4)
	v_mfma_f32_32x32x16_f16 v[64:79], a[80:83], v[160:163], v[64:79]
	ds_read_b128 v[160:163], v192 offset:49152
	v_fma_f32 v203, v203, 2.0, -1.0
	v_mul_f32_e32 v218, v214, v202
	v_exp_f32_e32 v200, v48
	v_mfma_f32_32x32x16_f16 v[80:95], a[80:83], v[164:167], v[80:95]
	ds_read_b128 v[164:167], v192 offset:50176
	v_mul_f32_e32 v219, v215, v203
	v_mul_f32_e32 v236, v216, v228
	v_exp_f32_e32 v201, v49
	v_mfma_f32_32x32x16_f16 v[64:79], a[84:87], v[168:171], v[64:79]
	ds_read_b128 v[168:171], v192 offset:51200
	v_mul_f32_e32 v237, v216, v232
	v_fmac_f32_e32 v236, v217, v229
	v_exp_f32_e32 v202, v50
	v_mfma_f32_32x32x16_f16 v[80:95], a[84:87], v[172:175], v[80:95]
	ds_read_b128 v[172:175], v192 offset:52224
	global_load_lds_dwordx4 v192, s[44:45] offset:3072 sc1
	v_fmac_f32_e32 v237, v217, v233
	v_fmac_f32_e32 v236, v218, v230
	v_exp_f32_e32 v203, v51
	s_waitcnt lgkmcnt(4)
	v_mfma_f32_32x32x16_f16 v[64:79], a[88:91], v[176:179], v[64:79]
	ds_read_b128 v[176:179], v192 offset:53248
	v_fmac_f32_e32 v237, v218, v234
	v_fmac_f32_e32 v236, v219, v231
	v_exp_f32_e32 v204, v52
	v_mfma_f32_32x32x16_f16 v[80:95], a[88:91], v[180:183], v[80:95]
	ds_read_b128 v[180:183], v192 offset:54272
	v_fmac_f32_e32 v237, v219, v235
	v_mov_b32_e32 v238, v236
	v_exp_f32_e32 v205, v53
	v_mfma_f32_32x32x16_f16 v[64:79], a[92:95], v[184:187], v[64:79]
	ds_read_b128 v[184:187], v192 offset:55296
	v_mov_b32_e32 v239, v236
	v_mov_b32_e32 v240, v237
	v_exp_f32_e32 v206, v54
	v_mfma_f32_32x32x16_f16 v[80:95], a[92:95], v[188:191], v[80:95]
	ds_read_b128 v[188:191], v192 offset:56320
	s_add_u32 s44, s34, 0x19000
	s_addc_u32 s45, s35, 0
	s_mov_b32 m0, s59
	s_nop 0
	global_load_lds_dwordx4 v192, s[44:45] sc1
	s_lshl_b32 s64, s71, 3
	s_add_u32 s64, s64, s29
	s_lshl_b32 s64, s64, 7
	s_add_u32 s38, s8, s64
	s_addc_u32 s39, s9, 0
	global_load_dword v251, v196, s[38:39] sc1
	v_mov_b32_e32 v241, v237
	v_cvt_pk_f16_f32 v220, v216, v217
	v_exp_f32_e32 v207, v55
	s_waitcnt lgkmcnt(4)
	v_mfma_f32_32x32x16_f16 v[64:79], a[96:99], v[160:163], v[64:79]
	ds_read_b128 v[160:163], v192 offset:57344
	s_nop 1
	v_permlane32_swap_b32_e32 v238, v239
	v_permlane32_swap_b32_e32 v240, v241
	v_add_f32_e32 v238, v238, v239
	v_add_f32_e32 v239, v240, v241
	ds_write_b64 v248, v[238:239] offset:512
	v_exp_f32_e32 v208, v56
	v_mfma_f32_32x32x16_f16 v[80:95], a[96:99], v[164:167], v[80:95]
	ds_read_b128 v[164:167], v192 offset:58368
	v_cvt_pk_f16_f32 v221, v218, v219
	v_exp_f32_e32 v209, v57
	v_add_f32_e32 v200, 1.0, v200
	v_mfma_f32_32x32x16_f16 v[64:79], a[100:103], v[168:171], v[64:79]
	ds_read_b128 v[168:171], v192 offset:59392
	v_exp_f32_e32 v210, v58
	v_add_f32_e32 v201, 1.0, v201
	v_add_f32_e32 v202, 1.0, v202
	v_mfma_f32_32x32x16_f16 v[80:95], a[100:103], v[172:175], v[80:95]
	ds_read_b128 v[172:175], v192 offset:60416
	global_load_lds_dwordx4 v192, s[44:45] offset:1024 sc1
	v_exp_f32_e32 v211, v59
	v_add_f32_e32 v203, 1.0, v203
	v_add_f32_e32 v204, 1.0, v204
	s_waitcnt lgkmcnt(5)
	v_mfma_f32_32x32x16_f16 v[64:79], a[104:107], v[176:179], v[64:79]
	ds_read_b128 v[176:179], v192 offset:61440
	v_exp_f32_e32 v212, v60
	v_add_f32_e32 v205, 1.0, v205
	v_add_f32_e32 v206, 1.0, v206
	v_mfma_f32_32x32x16_f16 v[80:95], a[104:107], v[180:183], v[80:95]
	ds_read_b128 v[180:183], v192 offset:62464
	v_exp_f32_e32 v213, v61
	v_add_f32_e32 v207, 1.0, v207
	v_add_f32_e32 v208, 1.0, v208
	v_mfma_f32_32x32x16_f16 v[64:79], a[108:111], v[184:187], v[64:79]
	ds_read_b128 v[184:187], v192 offset:63488
	v_exp_f32_e32 v214, v62
	v_add_f32_e32 v209, 1.0, v209
	v_add_f32_e32 v210, 1.0, v210
	v_mfma_f32_32x32x16_f16 v[80:95], a[108:111], v[188:191], v[80:95]
	ds_read_b128 v[188:191], v192 offset:64512
	global_load_lds_dwordx4 v192, s[44:45] offset:2048 sc1
	v_exp_f32_e32 v215, v63
	v_add_f32_e32 v211, 1.0, v211
	v_add_f32_e32 v212, 1.0, v212
	s_waitcnt vmcnt(12)
	s_barrier
	s_waitcnt lgkmcnt(4)
	v_mfma_f32_32x32x16_f16 v[64:79], a[112:115], v[160:163], v[64:79]
	ds_read_b128 v[160:163], v193 offset:0
	v_add_f32_e32 v213, 1.0, v213
	v_add_f32_e32 v214, 1.0, v214
	v_rcp_f32_e32 v200, v200
	v_mfma_f32_32x32x16_f16 v[80:95], a[112:115], v[164:167], v[80:95]
	ds_read_b128 v[164:167], v193 offset:1024
	v_add_f32_e32 v215, 1.0, v215
	v_rcp_f32_e32 v201, v201
	v_mfma_f32_32x32x16_f16 v[64:79], a[116:119], v[168:171], v[64:79]
	ds_read_b128 v[168:171], v193 offset:2048
	v_rcp_f32_e32 v202, v202
	v_mfma_f32_32x32x16_f16 v[80:95], a[116:119], v[172:175], v[80:95]
	ds_read_b128 v[172:175], v193 offset:3072
	global_load_lds_dwordx4 v192, s[44:45] offset:3072 sc1
	v_rcp_f32_e32 v203, v203
	s_waitcnt lgkmcnt(4)
	v_mfma_f32_32x32x16_f16 v[64:79], a[120:123], v[176:179], v[64:79]
	ds_read_b128 v[176:179], v193 offset:4096
	v_rcp_f32_e32 v204, v204
	v_mfma_f32_32x32x16_f16 v[80:95], a[120:123], v[180:183], v[80:95]
	ds_read_b128 v[180:183], v193 offset:5120
	v_rcp_f32_e32 v205, v205
	v_mul_f32_e32 v204, v204, v140
	v_mfma_f32_32x32x16_f16 v[64:79], a[124:127], v[184:187], v[64:79]
	ds_read_b128 v[184:187], v193 offset:6144
	v_rcp_f32_e32 v206, v206
	v_mul_f32_e32 v205, v205, v141
	v_mfma_f32_32x32x16_f16 v[80:95], a[124:127], v[188:191], v[80:95]
	ds_read_b128 v[188:191], v193 offset:7168
	s_waitcnt vmcnt(3)
	v_cmp_gt_u32_e32 vcc, 4, v251
	s_cbranch_vccz .LD_tok32

.LD_tok32:
	s_and_b32 s64, s71, 1
	s_lshl_b32 s64, s64, 22
	s_add_u32 s64, s64, s49
	s_add_u32 s64, s64, 0x60000
	s_add_u32 s34, s6, s64
	s_addc_u32 s35, s7, 0
	s_add_u32 s44, s34, 0x0
	s_addc_u32 s45, s35, 0
	s_mov_b32 m0, s52
	s_nop 0
	global_load_lds_dwordx4 v192, s[44:45] sc1
	v_rcp_f32_e32 v207, v207
	v_mul_f32_e32 v206, v206, v142
	s_waitcnt lgkmcnt(4)
	v_mfma_f32_32x32x16_f16 v[64:79], a[128:131], v[160:163], v[64:79]
	ds_read_b128 v[160:163], v193 offset:8192
	v_rcp_f32_e32 v208, v208
	v_mul_f32_e32 v207, v207, v143
	v_mfma_f32_32x32x16_f16 v[80:95], a[128:131], v[164:167], v[80:95]
	ds_read_b128 v[164:167], v193 offset:9216
	v_rcp_f32_e32 v209, v209
	v_fmamk_f32 v208, v208, 0xc0b8aa3b, v198
	v_mfma_f32_32x32x16_f16 v[64:79], a[132:135], v[168:171], v[64:79]
	ds_read_b128 v[168:171], v193 offset:10240
	v_rcp_f32_e32 v210, v210
	v_fmamk_f32 v209, v209, 0xc0b8aa3b, v198
	v_fma_f32 v140, v200, v208, v204
	v_mfma_f32_32x32x16_f16 v[80:95], a[132:135], v[172:175], v[80:95]
	ds_read_b128 v[172:175], v193 offset:11264
	global_load_lds_dwordx4 v192, s[44:45] offset:1024 sc1
	v_rcp_f32_e32 v211, v211
	v_fmamk_f32 v210, v210, 0xc0b8aa3b, v198
	v_fma_f32 v141, v201, v209, v205
	s_waitcnt lgkmcnt(4)
	v_mfma_f32_32x32x16_f16 v[64:79], a[136:139], v[176:179], v[64:79]
	ds_read_b128 v[176:179], v193 offset:12288
	v_rcp_f32_e32 v212, v212
	v_fmamk_f32 v211, v211, 0xc0b8aa3b, v198
	v_fma_f32 v142, v202, v210, v206
	v_mfma_f32_32x32x16_f16 v[80:95], a[136:139], v[180:183], v[80:95]
	ds_read_b128 v[180:183], v193 offset:13312
	v_rcp_f32_e32 v213, v213
	v_fma_f32 v143, v203, v211, v207
	v_mfma_f32_32x32x16_f16 v[64:79], a[140:143], v[184:187], v[64:79]
	ds_read_b128 v[184:187], v193 offset:14336
	v_rcp_f32_e32 v214, v214
	v_mfma_f32_32x32x16_f16 v[80:95], a[140:143], v[188:191], v[80:95]
	ds_read_b128 v[188:191], v193 offset:15360
	global_load_lds_dwordx4 v192, s[44:45] offset:2048 sc1
	v_rcp_f32_e32 v215, v215
	s_waitcnt lgkmcnt(4)
	v_mfma_f32_32x32x16_f16 v[64:79], a[144:147], v[160:163], v[64:79]
	ds_read_b128 v[160:163], v193 offset:16384
	v_exp_f32_e32 v200, v140
	v_mfma_f32_32x32x16_f16 v[80:95], a[144:147], v[164:167], v[80:95]
	ds_read_b128 v[164:167], v193 offset:17408
	v_exp_f32_e32 v201, v141
	v_add_f32_e32 v200, 1.0, v200
	v_mfma_f32_32x32x16_f16 v[64:79], a[148:151], v[168:171], v[64:79]
	ds_read_b128 v[168:171], v193 offset:18432
	v_exp_f32_e32 v202, v142
	v_add_f32_e32 v201, 1.0, v201
	v_mfma_f32_32x32x16_f16 v[80:95], a[148:151], v[172:175], v[80:95]
	ds_read_b128 v[172:175], v193 offset:19456
	global_load_lds_dwordx4 v192, s[44:45] offset:3072 sc1
	v_exp_f32_e32 v203, v143
	v_add_f32_e32 v202, 1.0, v202
	s_waitcnt lgkmcnt(4)
	v_mfma_f32_32x32x16_f16 v[64:79], a[152:155], v[176:179], v[64:79]
	ds_read_b128 v[176:179], v193 offset:20480
	v_add_f32_e32 v203, 1.0, v203
	v_rcp_f32_e32 v200, v200
	v_mfma_f32_32x32x16_f16 v[80:95], a[152:155], v[180:183], v[80:95]
	ds_read_b128 v[180:183], v193 offset:21504
	v_rcp_f32_e32 v201, v201
	v_fma_f32 v200, v200, 2.0, -1.0
	v_mfma_f32_32x32x16_f16 v[64:79], a[156:159], v[184:187], v[64:79]
	ds_read_b128 v[184:187], v193 offset:22528
	v_rcp_f32_e32 v202, v202
	v_fma_f32 v201, v201, 2.0, -1.0
	v_mul_f32_e32 v216, v212, v200
	v_mfma_f32_32x32x16_f16 v[80:95], a[156:159], v[188:191], v[80:95]
	ds_read_b128 v[188:191], v193 offset:23552
	s_add_u32 s44, s34, 0x1000
	s_addc_u32 s45, s35, 0
	s_mov_b32 m0, s53
	s_nop 0
	global_load_lds_dwordx4 v192, s[44:45] sc1
	v_rcp_f32_e32 v203, v203
	v_fma_f32 v202, v202, 2.0, -1.0
	v_mul_f32_e32 v217, v213, v201
	s_waitcnt lgkmcnt(4)
	v_mfma_f32_32x32x16_f16 v[64:79], a[160:163], v[160:163], v[64:79]
	ds_read_b128 v[160:163], v193 offset:24576
	v_fma_f32 v203, v203, 2.0, -1.0
	v_mul_f32_e32 v218, v214, v202
	v_mfma_f32_32x32x16_f16 v[80:95], a[160:163], v[164:167], v[80:95]
	ds_read_b128 v[164:167], v193 offset:25600
	v_mul_f32_e32 v219, v215, v203
	v_mul_f32_e32 v236, v216, v228
	v_mfma_f32_32x32x16_f16 v[64:79], a[164:167], v[168:171], v[64:79]
	ds_read_b128 v[168:171], v193 offset:26624
	v_mul_f32_e32 v237, v216, v232
	v_fmac_f32_e32 v236, v217, v229
	v_mfma_f32_32x32x16_f16 v[80:95], a[164:167], v[172:175], v[80:95]
	ds_read_b128 v[172:175], v193 offset:27648
	global_load_lds_dwordx4 v192, s[44:45] offset:1024 sc1
	v_fmac_f32_e32 v237, v217, v233
	v_fmac_f32_e32 v236, v218, v230
	s_waitcnt lgkmcnt(4)
	v_mfma_f32_32x32x16_f16 v[64:79], a[168:171], v[176:179], v[64:79]
	ds_read_b128 v[176:179], v193 offset:28672
	v_fmac_f32_e32 v237, v218, v234
	v_fmac_f32_e32 v236, v219, v231
	v_mfma_f32_32x32x16_f16 v[80:95], a[168:171], v[180:183], v[80:95]
	ds_read_b128 v[180:183], v193 offset:29696
	v_fmac_f32_e32 v237, v219, v235
	v_mov_b32_e32 v238, v236
	v_mfma_f32_32x32x16_f16 v[64:79], a[172:175], v[184:187], v[64:79]
	ds_read_b128 v[184:187], v193 offset:30720
	v_mov_b32_e32 v239, v236
	v_mov_b32_e32 v240, v237
	v_mfma_f32_32x32x16_f16 v[80:95], a[172:175], v[188:191], v[80:95]
	ds_read_b128 v[188:191], v193 offset:31744
	global_load_lds_dwordx4 v192, s[44:45] offset:2048 sc1
	v_mov_b32_e32 v241, v237
	v_cvt_pk_f16_f32 v222, v216, v217
	s_waitcnt vmcnt(7)
	s_barrier
	s_waitcnt lgkmcnt(4)
	v_mfma_f32_32x32x16_f16 v[64:79], a[176:179], v[160:163], v[64:79]
	ds_read_b128 v[160:163], v193 offset:32768
	s_nop 1
	v_permlane32_swap_b32_e32 v238, v239
	v_permlane32_swap_b32_e32 v240, v241
	v_add_f32_e32 v238, v238, v239
	v_add_f32_e32 v239, v240, v241
	ds_write_b64 v248, v[238:239] offset:768
	v_mfma_f32_32x32x16_f16 v[80:95], a[176:179], v[164:167], v[80:95]
	ds_read_b128 v[164:167], v193 offset:33792
	v_cvt_pk_f16_f32 v223, v218, v219
	v_mfma_f32_32x32x16_f16 v[64:79], a[180:183], v[168:171], v[64:79]
	ds_read_b128 v[168:171], v193 offset:34816
	s_nop 1
	v_permlane32_swap_b32_e32 v220, v222
	v_permlane32_swap_b32_e32 v221, v223
	s_cmp_eq_u32 s31, 0
	s_cbranch_scc1 .LD_slow34
	global_store_dwordx4 v195, v[220:223], s[36:37] offset:0
	s_branch .LD_join35

.LD_join35:
	v_mfma_f32_32x32x16_f16 v[80:95], a[180:183], v[172:175], v[80:95]
	ds_read_b128 v[172:175], v193 offset:35840
	global_load_lds_dwordx4 v192, s[44:45] offset:3072 sc1
	s_waitcnt lgkmcnt(5)
	v_mfma_f32_32x32x16_f16 v[64:79], a[184:187], v[176:179], v[64:79]
	ds_read_b128 v[176:179], v193 offset:36864
	v_mfma_f32_32x32x16_f16 v[80:95], a[184:187], v[180:183], v[80:95]
	ds_read_b128 v[180:183], v193 offset:37888
	v_mfma_f32_32x32x16_f16 v[64:79], a[188:191], v[184:187], v[64:79]
	ds_read_b128 v[184:187], v193 offset:38912
	v_mfma_f32_32x32x16_f16 v[80:95], a[188:191], v[188:191], v[80:95]
	ds_read_b128 v[188:191], v193 offset:39936
	s_add_u32 s44, s34, 0x8000
	s_addc_u32 s45, s35, 0
	s_mov_b32 m0, s54
	s_nop 0
	global_load_lds_dwordx4 v192, s[44:45] sc1
	s_waitcnt lgkmcnt(4)
	v_mfma_f32_32x32x16_f16 v[64:79], a[192:195], v[160:163], v[64:79]
	ds_read_b128 v[160:163], v193 offset:40960
	v_mfma_f32_32x32x16_f16 v[80:95], a[192:195], v[164:167], v[80:95]
	ds_read_b128 v[164:167], v193 offset:41984
	v_mfma_f32_32x32x16_f16 v[64:79], a[196:199], v[168:171], v[64:79]
	ds_read_b128 v[168:171], v193 offset:43008
	v_mfma_f32_32x32x16_f16 v[80:95], a[196:199], v[172:175], v[80:95]
	ds_read_b128 v[172:175], v193 offset:44032
	global_load_lds_dwordx4 v192, s[44:45] offset:1024 sc1
	s_waitcnt lgkmcnt(4)
	v_mfma_f32_32x32x16_f16 v[64:79], a[200:203], v[176:179], v[64:79]
	ds_read_b128 v[176:179], v193 offset:45056
	v_mfma_f32_32x32x16_f16 v[80:95], a[200:203], v[180:183], v[80:95]
	ds_read_b128 v[180:183], v193 offset:46080
	v_mfma_f32_32x32x16_f16 v[64:79], a[204:207], v[184:187], v[64:79]
	ds_read_b128 v[184:187], v193 offset:47104
	v_mfma_f32_32x32x16_f16 v[80:95], a[204:207], v[188:191], v[80:95]
	ds_read_b128 v[188:191], v193 offset:48128
	global_load_lds_dwordx4 v192, s[44:45] offset:2048 sc1
	s_waitcnt vmcnt(4)
	s_barrier
	v_mov_b32_e32 v199, 2
	s_cmp_eq_u32 s31, 0
	s_cbranch_scc1 .LD_slow36
	global_store_dword v197, v199, s[40:41]
	s_branch .LD_join37

.LD_join37:
	ds_read_b64 v[200:201], v249 offset:512
	ds_read_b64 v[202:203], v249 offset:2560
	ds_read_b64 v[204:205], v249 offset:4608
	ds_read_b64 v[206:207], v249 offset:6656
	s_waitcnt lgkmcnt(8)
	v_mfma_f32_32x32x16_f16 v[64:79], a[208:211], v[160:163], v[64:79]
	ds_read_b128 v[160:163], v193 offset:49152
	v_mfma_f32_32x32x16_f16 v[80:95], a[208:211], v[164:167], v[80:95]
	ds_read_b128 v[164:167], v193 offset:50176
	v_mfma_f32_32x32x16_f16 v[64:79], a[212:215], v[168:171], v[64:79]
	ds_read_b128 v[168:171], v193 offset:51200
	v_mfma_f32_32x32x16_f16 v[80:95], a[212:215], v[172:175], v[80:95]
	ds_read_b128 v[172:175], v193 offset:52224
	global_load_lds_dwordx4 v192, s[44:45] offset:3072 sc1
	s_waitcnt lgkmcnt(8)
	v_mfma_f32_32x32x16_f16 v[64:79], a[216:219], v[176:179], v[64:79]
	ds_read_b128 v[176:179], v193 offset:53248
	v_mfma_f32_32x32x16_f16 v[80:95], a[216:219], v[180:183], v[80:95]
	ds_read_b128 v[180:183], v193 offset:54272
	v_mfma_f32_32x32x16_f16 v[64:79], a[220:223], v[184:187], v[64:79]
	ds_read_b128 v[184:187], v193 offset:55296
	v_mfma_f32_32x32x16_f16 v[80:95], a[220:223], v[188:191], v[80:95]
	ds_read_b128 v[188:191], v193 offset:56320
	s_add_u32 s44, s34, 0x9000
	s_addc_u32 s45, s35, 0
	s_mov_b32 m0, s55
	s_nop 0
	global_load_lds_dwordx4 v192, s[44:45] sc1
	s_waitcnt lgkmcnt(4)
	v_mfma_f32_32x32x16_f16 v[64:79], a[224:227], v[160:163], v[64:79]
	ds_read_b128 v[160:163], v193 offset:57344
	v_mfma_f32_32x32x16_f16 v[80:95], a[224:227], v[164:167], v[80:95]
	ds_read_b128 v[164:167], v193 offset:58368
	v_mfma_f32_32x32x16_f16 v[64:79], a[228:231], v[168:171], v[64:79]
	ds_read_b128 v[168:171], v193 offset:59392
	v_mfma_f32_32x32x16_f16 v[80:95], a[228:231], v[172:175], v[80:95]
	ds_read_b128 v[172:175], v193 offset:60416
	global_load_lds_dwordx4 v192, s[44:45] offset:1024 sc1
	v_add_f32_e32 v200, v200, v202
	v_add_f32_e32 v201, v201, v203
	v_add_f32_e32 v200, v200, v204
	v_add_f32_e32 v201, v201, v205
	v_add_f32_e32 v200, v200, v206
	v_add_f32_e32 v201, v201, v207
	global_store_dwordx2 v250, v[200:201], s[72:73]
	s_waitcnt lgkmcnt(4)
	v_mfma_f32_32x32x16_f16 v[64:79], a[232:235], v[176:179], v[64:79]
	ds_read_b128 v[176:179], v193 offset:61440
	v_mfma_f32_32x32x16_f16 v[80:95], a[232:235], v[180:183], v[80:95]
	ds_read_b128 v[180:183], v193 offset:62464
	v_mfma_f32_32x32x16_f16 v[64:79], a[236:239], v[184:187], v[64:79]
	ds_read_b128 v[184:187], v193 offset:63488
	v_mfma_f32_32x32x16_f16 v[80:95], a[236:239], v[188:191], v[80:95]
	ds_read_b128 v[188:191], v193 offset:64512
	global_load_lds_dwordx4 v192, s[44:45] offset:2048 sc1
	s_waitcnt vmcnt(9)
	s_barrier
	s_waitcnt lgkmcnt(4)
	v_mfma_f32_32x32x16_f16 v[64:79], a[240:243], v[160:163], v[64:79]
	ds_read_b128 v[160:163], v192 offset:0
	v_mfma_f32_32x32x16_f16 v[80:95], a[240:243], v[164:167], v[80:95]
	ds_read_b128 v[164:167], v192 offset:1024
	v_mfma_f32_32x32x16_f16 v[64:79], a[244:247], v[168:171], v[64:79]
	ds_read_b128 v[168:171], v192 offset:2048
	v_mfma_f32_32x32x16_f16 v[80:95], a[244:247], v[172:175], v[80:95]
	ds_read_b128 v[172:175], v192 offset:3072
	global_load_lds_dwordx4 v192, s[44:45] offset:3072 sc1
	s_waitcnt lgkmcnt(4)
	v_mfma_f32_32x32x16_f16 v[64:79], a[248:251], v[176:179], v[64:79]
	ds_read_b128 v[176:179], v192 offset:4096
	v_mfma_f32_32x32x16_f16 v[80:95], a[248:251], v[180:183], v[80:95]
	ds_read_b128 v[180:183], v192 offset:5120
	v_mfma_f32_32x32x16_f16 v[64:79], a[252:255], v[184:187], v[64:79]
	ds_read_b128 v[184:187], v192 offset:6144
	v_mfma_f32_32x32x16_f16 v[80:95], a[252:255], v[188:191], v[80:95]
	ds_read_b128 v[188:191], v192 offset:7168
	s_add_u32 s44, s34, 0x10000
	s_addc_u32 s45, s35, 0
	s_mov_b32 m0, s56
	s_nop 0
	global_load_lds_dwordx4 v192, s[44:45] sc1
	s_and_b32 s64, s33, 1
	s_lshl_b32 s64, s64, 22
	s_add_u32 s64, s64, s50
	s_add_u32 s64, s64, 0x40000
	s_add_u32 s36, s6, s64
	s_addc_u32 s37, s7, 0
	s_lshl_b32 s64, s33, 3
	s_add_u32 s64, s64, s29
	s_lshl_b32 s64, s64, 5
	s_add_u32 s64, s64, s30
	s_lshl_b32 s64, s64, 2
	s_add_u32 s40, s8, s64
	s_addc_u32 s41, s9, 0
	s_lshl_b32 s64, s33, 19
	s_add_u32 s64, s64, 0x400
	s_add_u32 s72, s62, s64
	s_addc_u32 s73, s63, 0
	s_nop 3
	s_waitcnt lgkmcnt(4)
	v_mfma_f32_32x32x16_f16 v[96:111], a[0:3], v[160:163], v[96:111]
	ds_read_b128 v[160:163], v192 offset:8192
	v_exp_f32_e32 v200, v64
	v_mfma_f32_32x32x16_f16 v[112:127], a[0:3], v[164:167], v[112:127]
	ds_read_b128 v[164:167], v192 offset:9216
	v_exp_f32_e32 v201, v65
	v_add_f32_e32 v200, 1.0, v200
	v_mfma_f32_32x32x16_f16 v[96:111], a[4:7], v[168:171], v[96:111]
	ds_read_b128 v[168:171], v192 offset:10240
	v_exp_f32_e32 v202, v66
	v_add_f32_e32 v201, 1.0, v201
	v_mfma_f32_32x32x16_f16 v[112:127], a[4:7], v[172:175], v[112:127]
	ds_read_b128 v[172:175], v192 offset:11264
	global_load_lds_dwordx4 v192, s[44:45] offset:1024 sc1
	v_exp_f32_e32 v203, v67
	v_add_f32_e32 v202, 1.0, v202
	s_waitcnt lgkmcnt(4)
	v_mfma_f32_32x32x16_f16 v[96:111], a[8:11], v[176:179], v[96:111]
	ds_read_b128 v[176:179], v192 offset:12288
	v_exp_f32_e32 v204, v68
	v_add_f32_e32 v203, 1.0, v203
	v_mfma_f32_32x32x16_f16 v[112:127], a[8:11], v[180:183], v[112:127]
	ds_read_b128 v[180:183], v192 offset:13312
	v_exp_f32_e32 v205, v69
	v_add_f32_e32 v204, 1.0, v204
	v_mfma_f32_32x32x16_f16 v[96:111], a[12:15], v[184:187], v[96:111]
	ds_read_b128 v[184:187], v192 offset:14336
	v_exp_f32_e32 v206, v70
	v_add_f32_e32 v205, 1.0, v205
	v_mfma_f32_32x32x16_f16 v[112:127], a[12:15], v[188:191], v[112:127]
	ds_read_b128 v[188:191], v192 offset:15360
	global_load_lds_dwordx4 v192, s[44:45] offset:2048 sc1
	v_exp_f32_e32 v207, v71
	v_add_f32_e32 v206, 1.0, v206
	s_waitcnt lgkmcnt(4)
	v_mfma_f32_32x32x16_f16 v[96:111], a[16:19], v[160:163], v[96:111]
	ds_read_b128 v[160:163], v192 offset:16384
	v_exp_f32_e32 v208, v72
	v_add_f32_e32 v207, 1.0, v207
	v_mfma_f32_32x32x16_f16 v[112:127], a[16:19], v[164:167], v[112:127]
	ds_read_b128 v[164:167], v192 offset:17408
	v_exp_f32_e32 v209, v73
	v_add_f32_e32 v208, 1.0, v208
	v_mfma_f32_32x32x16_f16 v[96:111], a[20:23], v[168:171], v[96:111]
	ds_read_b128 v[168:171], v192 offset:18432
	v_exp_f32_e32 v210, v74
	v_add_f32_e32 v209, 1.0, v209
	v_mfma_f32_32x32x16_f16 v[112:127], a[20:23], v[172:175], v[112:127]
	ds_read_b128 v[172:175], v192 offset:19456
	global_load_lds_dwordx4 v192, s[44:45] offset:3072 sc1
	v_exp_f32_e32 v211, v75
	v_add_f32_e32 v210, 1.0, v210
	s_waitcnt lgkmcnt(4)
	v_mfma_f32_32x32x16_f16 v[96:111], a[24:27], v[176:179], v[96:111]
	ds_read_b128 v[176:179], v192 offset:20480
	v_exp_f32_e32 v212, v76
	v_add_f32_e32 v211, 1.0, v211
	v_mfma_f32_32x32x16_f16 v[112:127], a[24:27], v[180:183], v[112:127]
	ds_read_b128 v[180:183], v192 offset:21504
	v_exp_f32_e32 v213, v77
	v_add_f32_e32 v212, 1.0, v212
	v_mfma_f32_32x32x16_f16 v[96:111], a[28:31], v[184:187], v[96:111]
	ds_read_b128 v[184:187], v192 offset:22528
	v_exp_f32_e32 v214, v78
	v_add_f32_e32 v213, 1.0, v213
	v_mfma_f32_32x32x16_f16 v[112:127], a[28:31], v[188:191], v[112:127]
	ds_read_b128 v[188:191], v192 offset:23552
	s_add_u32 s44, s34, 0x11000
	s_addc_u32 s45, s35, 0
	s_mov_b32 m0, s57
	s_nop 0
	global_load_lds_dwordx4 v192, s[44:45] sc1
	v_exp_f32_e32 v215, v79
	v_add_f32_e32 v214, 1.0, v214
	s_waitcnt lgkmcnt(4)
	v_mfma_f32_32x32x16_f16 v[96:111], a[32:35], v[160:163], v[96:111]
	ds_read_b128 v[160:163], v192 offset:24576
	v_add_f32_e32 v215, 1.0, v215
	v_rcp_f32_e32 v200, v200
	v_mfma_f32_32x32x16_f16 v[112:127], a[32:35], v[164:167], v[112:127]
	ds_read_b128 v[164:167], v192 offset:25600
	v_rcp_f32_e32 v201, v201
	v_mfma_f32_32x32x16_f16 v[96:111], a[36:39], v[168:171], v[96:111]
	ds_read_b128 v[168:171], v192 offset:26624
	v_rcp_f32_e32 v202, v202
	v_mfma_f32_32x32x16_f16 v[112:127], a[36:39], v[172:175], v[112:127]
	ds_read_b128 v[172:175], v192 offset:27648
	global_load_lds_dwordx4 v192, s[44:45] offset:1024 sc1
	v_rcp_f32_e32 v203, v203
	s_waitcnt lgkmcnt(4)
	v_mfma_f32_32x32x16_f16 v[96:111], a[40:43], v[176:179], v[96:111]
	ds_read_b128 v[176:179], v192 offset:28672
	v_rcp_f32_e32 v204, v204
	v_mfma_f32_32x32x16_f16 v[112:127], a[40:43], v[180:183], v[112:127]
	ds_read_b128 v[180:183], v192 offset:29696
	v_rcp_f32_e32 v205, v205
	v_mul_f32_e32 v204, v204, v144
	v_mfma_f32_32x32x16_f16 v[96:111], a[44:47], v[184:187], v[96:111]
	ds_read_b128 v[184:187], v192 offset:30720
	v_rcp_f32_e32 v206, v206
	v_mul_f32_e32 v205, v205, v145
	v_mfma_f32_32x32x16_f16 v[112:127], a[44:47], v[188:191], v[112:127]
	ds_read_b128 v[188:191], v192 offset:31744
	global_load_lds_dwordx4 v192, s[44:45] offset:2048 sc1
	v_rcp_f32_e32 v207, v207
	v_mul_f32_e32 v206, v206, v146
	s_waitcnt vmcnt(7)
	s_barrier
	s_waitcnt lgkmcnt(4)
	v_mfma_f32_32x32x16_f16 v[96:111], a[48:51], v[160:163], v[96:111]
	ds_read_b128 v[160:163], v192 offset:32768
	v_rcp_f32_e32 v208, v208
	v_mul_f32_e32 v207, v207, v147
	s_add_u32 s46, s42, 0x2000
	s_addc_u32 s47, s43, 0
	global_load_dwordx4 v[32:35], v192, s[46:47] offset:0
	v_mfma_f32_32x32x16_f16 v[112:127], a[48:51], v[164:167], v[112:127]
	ds_read_b128 v[164:167], v192 offset:33792
	v_rcp_f32_e32 v209, v209
	v_fmamk_f32 v208, v208, 0xc0b8aa3b, v198
	global_load_dwordx4 v[36:39], v192, s[46:47] offset:1024
	global_load_dwordx4 v[40:43], v192, s[46:47] offset:2048
	v_mfma_f32_32x32x16_f16 v[96:111], a[52:55], v[168:171], v[96:111]
	ds_read_b128 v[168:171], v192 offset:34816
	v_rcp_f32_e32 v210, v210
	v_fmamk_f32 v209, v209, 0xc0b8aa3b, v198
	v_fma_f32 v144, v200, v208, v204
	global_load_dwordx4 v[44:47], v192, s[46:47] offset:3072
	s_add_u32 s46, s42, 0x3000
	s_addc_u32 s47, s43, 0
	v_mfma_f32_32x32x16_f16 v[112:127], a[52:55], v[172:175], v[112:127]
	ds_read_b128 v[172:175], v192 offset:35840
	global_load_lds_dwordx4 v192, s[44:45] offset:3072 sc1
	v_rcp_f32_e32 v211, v211
	v_fmamk_f32 v210, v210, 0xc0b8aa3b, v198
	v_fma_f32 v145, v201, v209, v205
	global_load_dwordx4 v[48:51], v192, s[46:47] offset:0
	global_load_dwordx4 v[52:55], v192, s[46:47] offset:1024
	s_waitcnt lgkmcnt(4)
	v_mfma_f32_32x32x16_f16 v[96:111], a[56:59], v[176:179], v[96:111]
	ds_read_b128 v[176:179], v192 offset:36864
	v_rcp_f32_e32 v212, v212
	v_fmamk_f32 v211, v211, 0xc0b8aa3b, v198
	v_fma_f32 v146, v202, v210, v206
	global_load_dwordx4 v[56:59], v192, s[46:47] offset:2048
	global_load_dwordx4 v[60:63], v192, s[46:47] offset:3072
	v_mfma_f32_32x32x16_f16 v[112:127], a[56:59], v[180:183], v[112:127]
	ds_read_b128 v[180:183], v192 offset:37888
	v_rcp_f32_e32 v213, v213
	v_fma_f32 v147, v203, v211, v207
	v_mfma_f32_32x32x16_f16 v[96:111], a[60:63], v[184:187], v[96:111]
	ds_read_b128 v[184:187], v192 offset:38912
	v_rcp_f32_e32 v214, v214
	v_mfma_f32_32x32x16_f16 v[112:127], a[60:63], v[188:191], v[112:127]
	ds_read_b128 v[188:191], v192 offset:39936
	s_add_u32 s44, s34, 0x18000
	s_addc_u32 s45, s35, 0
	s_mov_b32 m0, s58
	s_nop 0
	global_load_lds_dwordx4 v192, s[44:45] sc1
	v_rcp_f32_e32 v215, v215
	s_waitcnt lgkmcnt(4)
	v_mfma_f32_32x32x16_f16 v[96:111], a[64:67], v[160:163], v[96:111]
	ds_read_b128 v[160:163], v192 offset:40960
	v_exp_f32_e32 v200, v144
	v_mfma_f32_32x32x16_f16 v[112:127], a[64:67], v[164:167], v[112:127]
	ds_read_b128 v[164:167], v192 offset:41984
	v_exp_f32_e32 v201, v145
	v_add_f32_e32 v200, 1.0, v200
	v_mfma_f32_32x32x16_f16 v[96:111], a[68:71], v[168:171], v[96:111]
	ds_read_b128 v[168:171], v192 offset:43008
	v_exp_f32_e32 v202, v146
	v_add_f32_e32 v201, 1.0, v201
	v_mfma_f32_32x32x16_f16 v[112:127], a[68:71], v[172:175], v[112:127]
	ds_read_b128 v[172:175], v192 offset:44032
	global_load_lds_dwordx4 v192, s[44:45] offset:1024 sc1
	v_exp_f32_e32 v203, v147
	v_add_f32_e32 v202, 1.0, v202
	s_waitcnt lgkmcnt(4)
	v_mfma_f32_32x32x16_f16 v[96:111], a[72:75], v[176:179], v[96:111]
	ds_read_b128 v[176:179], v192 offset:45056
	v_add_f32_e32 v203, 1.0, v203
	v_rcp_f32_e32 v200, v200
	v_mfma_f32_32x32x16_f16 v[112:127], a[72:75], v[180:183], v[112:127]
	ds_read_b128 v[180:183], v192 offset:46080
	v_rcp_f32_e32 v201, v201
	v_fma_f32 v200, v200, 2.0, -1.0
	v_mfma_f32_32x32x16_f16 v[96:111], a[76:79], v[184:187], v[96:111]
	ds_read_b128 v[184:187], v192 offset:47104
	v_rcp_f32_e32 v202, v202
	v_fma_f32 v201, v201, 2.0, -1.0
	v_mul_f32_e32 v216, v212, v200
	v_mfma_f32_32x32x16_f16 v[112:127], a[76:79], v[188:191], v[112:127]
	ds_read_b128 v[188:191], v192 offset:48128
	global_load_lds_dwordx4 v192, s[44:45] offset:2048 sc1
	v_rcp_f32_e32 v203, v203
	v_fma_f32 v202, v202, 2.0, -1.0
	v_mul_f32_e32 v217, v213, v201
	s_waitcnt lgkmcnt(4)
	v_mfma_f32_32x32x16_f16 v[96:111], a[80:83], v[160:163], v[96:111]
	ds_read_b128 v[160:163], v192 offset:49152
	v_fma_f32 v203, v203, 2.0, -1.0
	v_mul_f32_e32 v218, v214, v202
	v_exp_f32_e32 v200, v80
	v_mfma_f32_32x32x16_f16 v[112:127], a[80:83], v[164:167], v[112:127]
	ds_read_b128 v[164:167], v192 offset:50176
	v_mul_f32_e32 v219, v215, v203
	v_mul_f32_e32 v236, v216, v228
	v_exp_f32_e32 v201, v81
	v_mfma_f32_32x32x16_f16 v[96:111], a[84:87], v[168:171], v[96:111]
	ds_read_b128 v[168:171], v192 offset:51200
	v_mul_f32_e32 v237, v216, v232
	v_fmac_f32_e32 v236, v217, v229
	v_exp_f32_e32 v202, v82
	v_mfma_f32_32x32x16_f16 v[112:127], a[84:87], v[172:175], v[112:127]
	ds_read_b128 v[172:175], v192 offset:52224
	global_load_lds_dwordx4 v192, s[44:45] offset:3072 sc1
	v_fmac_f32_e32 v237, v217, v233
	v_fmac_f32_e32 v236, v218, v230
	v_exp_f32_e32 v203, v83
	s_waitcnt lgkmcnt(4)
	v_mfma_f32_32x32x16_f16 v[96:111], a[88:91], v[176:179], v[96:111]
	ds_read_b128 v[176:179], v192 offset:53248
	v_fmac_f32_e32 v237, v218, v234
	v_fmac_f32_e32 v236, v219, v231
	v_exp_f32_e32 v204, v84
	v_mfma_f32_32x32x16_f16 v[112:127], a[88:91], v[180:183], v[112:127]
	ds_read_b128 v[180:183], v192 offset:54272
	v_fmac_f32_e32 v237, v219, v235
	v_mov_b32_e32 v238, v236
	v_exp_f32_e32 v205, v85
	v_mfma_f32_32x32x16_f16 v[96:111], a[92:95], v[184:187], v[96:111]
	ds_read_b128 v[184:187], v192 offset:55296
	v_mov_b32_e32 v239, v236
	v_mov_b32_e32 v240, v237
	v_exp_f32_e32 v206, v86
	v_mfma_f32_32x32x16_f16 v[112:127], a[92:95], v[188:191], v[112:127]
	ds_read_b128 v[188:191], v192 offset:56320
	s_add_u32 s44, s34, 0x19000
	s_addc_u32 s45, s35, 0
	s_mov_b32 m0, s59
	s_nop 0
	global_load_lds_dwordx4 v192, s[44:45] sc1
	s_lshl_b32 s64, s33, 3
	s_add_u32 s64, s64, s29
	s_lshl_b32 s64, s64, 7
	s_add_u32 s38, s8, s64
	s_addc_u32 s39, s9, 0
	global_load_dword v251, v196, s[38:39] sc1
	v_mov_b32_e32 v241, v237
	v_cvt_pk_f16_f32 v220, v216, v217
	v_exp_f32_e32 v207, v87
	s_waitcnt lgkmcnt(4)
	v_mfma_f32_32x32x16_f16 v[96:111], a[96:99], v[160:163], v[96:111]
	ds_read_b128 v[160:163], v192 offset:57344
	s_nop 1
	v_permlane32_swap_b32_e32 v238, v239
	v_permlane32_swap_b32_e32 v240, v241
	v_add_f32_e32 v238, v238, v239
	v_add_f32_e32 v239, v240, v241
	ds_write_b64 v248, v[238:239] offset:1024
	v_exp_f32_e32 v208, v88
	v_mfma_f32_32x32x16_f16 v[112:127], a[96:99], v[164:167], v[112:127]
	ds_read_b128 v[164:167], v192 offset:58368
	v_cvt_pk_f16_f32 v221, v218, v219
	v_exp_f32_e32 v209, v89
	v_add_f32_e32 v200, 1.0, v200
	v_mfma_f32_32x32x16_f16 v[96:111], a[100:103], v[168:171], v[96:111]
	ds_read_b128 v[168:171], v192 offset:59392
	v_exp_f32_e32 v210, v90
	v_add_f32_e32 v201, 1.0, v201
	v_add_f32_e32 v202, 1.0, v202
	v_mfma_f32_32x32x16_f16 v[112:127], a[100:103], v[172:175], v[112:127]
	ds_read_b128 v[172:175], v192 offset:60416
	global_load_lds_dwordx4 v192, s[44:45] offset:1024 sc1
	v_exp_f32_e32 v211, v91
	v_add_f32_e32 v203, 1.0, v203
	v_add_f32_e32 v204, 1.0, v204
	s_waitcnt lgkmcnt(5)
	v_mfma_f32_32x32x16_f16 v[96:111], a[104:107], v[176:179], v[96:111]
	ds_read_b128 v[176:179], v192 offset:61440
	v_exp_f32_e32 v212, v92
	v_add_f32_e32 v205, 1.0, v205
	v_add_f32_e32 v206, 1.0, v206
	v_mfma_f32_32x32x16_f16 v[112:127], a[104:107], v[180:183], v[112:127]
	ds_read_b128 v[180:183], v192 offset:62464
	v_exp_f32_e32 v213, v93
	v_add_f32_e32 v207, 1.0, v207
	v_add_f32_e32 v208, 1.0, v208
	v_mfma_f32_32x32x16_f16 v[96:111], a[108:111], v[184:187], v[96:111]
	ds_read_b128 v[184:187], v192 offset:63488
	v_exp_f32_e32 v214, v94
	v_add_f32_e32 v209, 1.0, v209
	v_add_f32_e32 v210, 1.0, v210
	v_mfma_f32_32x32x16_f16 v[112:127], a[108:111], v[188:191], v[112:127]
	ds_read_b128 v[188:191], v192 offset:64512
	global_load_lds_dwordx4 v192, s[44:45] offset:2048 sc1
	v_exp_f32_e32 v215, v95
	v_add_f32_e32 v211, 1.0, v211
	v_add_f32_e32 v212, 1.0, v212
	s_waitcnt vmcnt(12)
	s_barrier
	s_waitcnt lgkmcnt(4)
	v_mfma_f32_32x32x16_f16 v[96:111], a[112:115], v[160:163], v[96:111]
	ds_read_b128 v[160:163], v193 offset:0
	v_add_f32_e32 v213, 1.0, v213
	v_add_f32_e32 v214, 1.0, v214
	v_rcp_f32_e32 v200, v200
	v_mfma_f32_32x32x16_f16 v[112:127], a[112:115], v[164:167], v[112:127]
	ds_read_b128 v[164:167], v193 offset:1024
	v_add_f32_e32 v215, 1.0, v215
	v_rcp_f32_e32 v201, v201
	v_mfma_f32_32x32x16_f16 v[96:111], a[116:119], v[168:171], v[96:111]
	ds_read_b128 v[168:171], v193 offset:2048
	v_rcp_f32_e32 v202, v202
	v_mfma_f32_32x32x16_f16 v[112:127], a[116:119], v[172:175], v[112:127]
	ds_read_b128 v[172:175], v193 offset:3072
	global_load_lds_dwordx4 v192, s[44:45] offset:3072 sc1
	v_rcp_f32_e32 v203, v203
	s_waitcnt lgkmcnt(4)
	v_mfma_f32_32x32x16_f16 v[96:111], a[120:123], v[176:179], v[96:111]
	ds_read_b128 v[176:179], v193 offset:4096
	v_rcp_f32_e32 v204, v204
	v_mfma_f32_32x32x16_f16 v[112:127], a[120:123], v[180:183], v[112:127]
	ds_read_b128 v[180:183], v193 offset:5120
	v_rcp_f32_e32 v205, v205
	v_mul_f32_e32 v204, v204, v148
	v_mfma_f32_32x32x16_f16 v[96:111], a[124:127], v[184:187], v[96:111]
	ds_read_b128 v[184:187], v193 offset:6144
	v_rcp_f32_e32 v206, v206
	v_mul_f32_e32 v205, v205, v149
	v_mfma_f32_32x32x16_f16 v[112:127], a[124:127], v[188:191], v[112:127]
	ds_read_b128 v[188:191], v193 offset:7168
	s_waitcnt vmcnt(3)
	v_cmp_gt_u32_e32 vcc, 1, v251
	s_cbranch_vccz .LD_tok38

.LD_tok38:
	s_and_b32 s64, s33, 1
	s_lshl_b32 s64, s64, 22
	s_add_u32 s64, s64, s49
	s_add_u32 s34, s6, s64
	s_addc_u32 s35, s7, 0
	s_add_u32 s44, s34, 0x0
	s_addc_u32 s45, s35, 0
	s_mov_b32 m0, s52
	s_nop 0
	global_load_lds_dwordx4 v192, s[44:45] sc1
	v_rcp_f32_e32 v207, v207
	v_mul_f32_e32 v206, v206, v150
	s_waitcnt lgkmcnt(4)
	v_mfma_f32_32x32x16_f16 v[96:111], a[128:131], v[160:163], v[96:111]
	ds_read_b128 v[160:163], v193 offset:8192
	v_rcp_f32_e32 v208, v208
	v_mul_f32_e32 v207, v207, v151
	v_mfma_f32_32x32x16_f16 v[112:127], a[128:131], v[164:167], v[112:127]
	ds_read_b128 v[164:167], v193 offset:9216
	v_rcp_f32_e32 v209, v209
	v_fmamk_f32 v208, v208, 0xc0b8aa3b, v198
	v_mfma_f32_32x32x16_f16 v[96:111], a[132:135], v[168:171], v[96:111]
	ds_read_b128 v[168:171], v193 offset:10240
	v_rcp_f32_e32 v210, v210
	v_fmamk_f32 v209, v209, 0xc0b8aa3b, v198
	v_fma_f32 v148, v200, v208, v204
	v_mfma_f32_32x32x16_f16 v[112:127], a[132:135], v[172:175], v[112:127]
	ds_read_b128 v[172:175], v193 offset:11264
	global_load_lds_dwordx4 v192, s[44:45] offset:1024 sc1
	v_rcp_f32_e32 v211, v211
	v_fmamk_f32 v210, v210, 0xc0b8aa3b, v198
	v_fma_f32 v149, v201, v209, v205
	s_waitcnt lgkmcnt(4)
	v_mfma_f32_32x32x16_f16 v[96:111], a[136:139], v[176:179], v[96:111]
	ds_read_b128 v[176:179], v193 offset:12288
	v_rcp_f32_e32 v212, v212
	v_fmamk_f32 v211, v211, 0xc0b8aa3b, v198
	v_fma_f32 v150, v202, v210, v206
	v_mfma_f32_32x32x16_f16 v[112:127], a[136:139], v[180:183], v[112:127]
	ds_read_b128 v[180:183], v193 offset:13312
	v_rcp_f32_e32 v213, v213
	v_fma_f32 v151, v203, v211, v207
	v_mfma_f32_32x32x16_f16 v[96:111], a[140:143], v[184:187], v[96:111]
	ds_read_b128 v[184:187], v193 offset:14336
	v_rcp_f32_e32 v214, v214
	v_mfma_f32_32x32x16_f16 v[112:127], a[140:143], v[188:191], v[112:127]
	ds_read_b128 v[188:191], v193 offset:15360
	global_load_lds_dwordx4 v192, s[44:45] offset:2048 sc1
	v_rcp_f32_e32 v215, v215
	s_waitcnt lgkmcnt(4)
	v_mfma_f32_32x32x16_f16 v[96:111], a[144:147], v[160:163], v[96:111]
	ds_read_b128 v[160:163], v193 offset:16384
	v_exp_f32_e32 v200, v148
	v_mfma_f32_32x32x16_f16 v[112:127], a[144:147], v[164:167], v[112:127]
	ds_read_b128 v[164:167], v193 offset:17408
	v_exp_f32_e32 v201, v149
	v_add_f32_e32 v200, 1.0, v200
	v_mfma_f32_32x32x16_f16 v[96:111], a[148:151], v[168:171], v[96:111]
	ds_read_b128 v[168:171], v193 offset:18432
	v_exp_f32_e32 v202, v150
	v_add_f32_e32 v201, 1.0, v201
	v_mfma_f32_32x32x16_f16 v[112:127], a[148:151], v[172:175], v[112:127]
	ds_read_b128 v[172:175], v193 offset:19456
	global_load_lds_dwordx4 v192, s[44:45] offset:3072 sc1
	v_exp_f32_e32 v203, v151
	v_add_f32_e32 v202, 1.0, v202
	s_waitcnt lgkmcnt(4)
	v_mfma_f32_32x32x16_f16 v[96:111], a[152:155], v[176:179], v[96:111]
	ds_read_b128 v[176:179], v193 offset:20480
	v_add_f32_e32 v203, 1.0, v203
	v_rcp_f32_e32 v200, v200
	v_mfma_f32_32x32x16_f16 v[112:127], a[152:155], v[180:183], v[112:127]
	ds_read_b128 v[180:183], v193 offset:21504
	v_rcp_f32_e32 v201, v201
	v_fma_f32 v200, v200, 2.0, -1.0
	v_mfma_f32_32x32x16_f16 v[96:111], a[156:159], v[184:187], v[96:111]
	ds_read_b128 v[184:187], v193 offset:22528
	v_rcp_f32_e32 v202, v202
	v_fma_f32 v201, v201, 2.0, -1.0
	v_mul_f32_e32 v216, v212, v200
	v_mfma_f32_32x32x16_f16 v[112:127], a[156:159], v[188:191], v[112:127]
	ds_read_b128 v[188:191], v193 offset:23552
	s_add_u32 s44, s34, 0x1000
	s_addc_u32 s45, s35, 0
	s_mov_b32 m0, s53
	s_nop 0
	global_load_lds_dwordx4 v192, s[44:45] sc1
	v_rcp_f32_e32 v203, v203
	v_fma_f32 v202, v202, 2.0, -1.0
	v_mul_f32_e32 v217, v213, v201
	s_waitcnt lgkmcnt(4)
	v_mfma_f32_32x32x16_f16 v[96:111], a[160:163], v[160:163], v[96:111]
	ds_read_b128 v[160:163], v193 offset:24576
	v_fma_f32 v203, v203, 2.0, -1.0
	v_mul_f32_e32 v218, v214, v202
	v_mfma_f32_32x32x16_f16 v[112:127], a[160:163], v[164:167], v[112:127]
	ds_read_b128 v[164:167], v193 offset:25600
	v_mul_f32_e32 v219, v215, v203
	v_mul_f32_e32 v236, v216, v228
	v_mfma_f32_32x32x16_f16 v[96:111], a[164:167], v[168:171], v[96:111]
	ds_read_b128 v[168:171], v193 offset:26624
	v_mul_f32_e32 v237, v216, v232
	v_fmac_f32_e32 v236, v217, v229
	v_mfma_f32_32x32x16_f16 v[112:127], a[164:167], v[172:175], v[112:127]
	ds_read_b128 v[172:175], v193 offset:27648
	global_load_lds_dwordx4 v192, s[44:45] offset:1024 sc1
	v_fmac_f32_e32 v237, v217, v233
	v_fmac_f32_e32 v236, v218, v230
	s_waitcnt lgkmcnt(4)
	v_mfma_f32_32x32x16_f16 v[96:111], a[168:171], v[176:179], v[96:111]
	ds_read_b128 v[176:179], v193 offset:28672
	v_fmac_f32_e32 v237, v218, v234
	v_fmac_f32_e32 v236, v219, v231
	v_mfma_f32_32x32x16_f16 v[112:127], a[168:171], v[180:183], v[112:127]
	ds_read_b128 v[180:183], v193 offset:29696
	v_fmac_f32_e32 v237, v219, v235
	v_mov_b32_e32 v238, v236
	v_mfma_f32_32x32x16_f16 v[96:111], a[172:175], v[184:187], v[96:111]
	ds_read_b128 v[184:187], v193 offset:30720
	v_mov_b32_e32 v239, v236
	v_mov_b32_e32 v240, v237
	v_mfma_f32_32x32x16_f16 v[112:127], a[172:175], v[188:191], v[112:127]
	ds_read_b128 v[188:191], v193 offset:31744
	global_load_lds_dwordx4 v192, s[44:45] offset:2048 sc1
	v_mov_b32_e32 v241, v237
	v_cvt_pk_f16_f32 v222, v216, v217
	s_waitcnt vmcnt(7)
	s_barrier
	s_waitcnt lgkmcnt(4)
	v_mfma_f32_32x32x16_f16 v[96:111], a[176:179], v[160:163], v[96:111]
	ds_read_b128 v[160:163], v193 offset:32768
	s_nop 1
	v_permlane32_swap_b32_e32 v238, v239
	v_permlane32_swap_b32_e32 v240, v241
	v_add_f32_e32 v238, v238, v239
	v_add_f32_e32 v239, v240, v241
	ds_write_b64 v248, v[238:239] offset:1280
	v_mfma_f32_32x32x16_f16 v[112:127], a[176:179], v[164:167], v[112:127]
	ds_read_b128 v[164:167], v193 offset:33792
	v_cvt_pk_f16_f32 v223, v218, v219
	v_mfma_f32_32x32x16_f16 v[96:111], a[180:183], v[168:171], v[96:111]
	ds_read_b128 v[168:171], v193 offset:34816
	s_nop 1
	v_permlane32_swap_b32_e32 v220, v222
	v_permlane32_swap_b32_e32 v221, v223
	s_cmp_eq_u32 s31, 0
	s_cbranch_scc1 .LD_slow40
	global_store_dwordx4 v195, v[220:223], s[36:37] offset:0
	s_branch .LD_join41

.LD_join41:
	v_mfma_f32_32x32x16_f16 v[112:127], a[180:183], v[172:175], v[112:127]
	ds_read_b128 v[172:175], v193 offset:35840
	global_load_lds_dwordx4 v192, s[44:45] offset:3072 sc1
	s_waitcnt lgkmcnt(5)
	v_mfma_f32_32x32x16_f16 v[96:111], a[184:187], v[176:179], v[96:111]
	ds_read_b128 v[176:179], v193 offset:36864
	v_mfma_f32_32x32x16_f16 v[112:127], a[184:187], v[180:183], v[112:127]
	ds_read_b128 v[180:183], v193 offset:37888
	v_mfma_f32_32x32x16_f16 v[96:111], a[188:191], v[184:187], v[96:111]
	ds_read_b128 v[184:187], v193 offset:38912
	v_mfma_f32_32x32x16_f16 v[112:127], a[188:191], v[188:191], v[112:127]
	ds_read_b128 v[188:191], v193 offset:39936
	s_add_u32 s44, s34, 0x8000
	s_addc_u32 s45, s35, 0
	s_mov_b32 m0, s54
	s_nop 0
	global_load_lds_dwordx4 v192, s[44:45] sc1
	s_waitcnt lgkmcnt(4)
	v_mfma_f32_32x32x16_f16 v[96:111], a[192:195], v[160:163], v[96:111]
	ds_read_b128 v[160:163], v193 offset:40960
	v_mfma_f32_32x32x16_f16 v[112:127], a[192:195], v[164:167], v[112:127]
	ds_read_b128 v[164:167], v193 offset:41984
	v_mfma_f32_32x32x16_f16 v[96:111], a[196:199], v[168:171], v[96:111]
	ds_read_b128 v[168:171], v193 offset:43008
	v_mfma_f32_32x32x16_f16 v[112:127], a[196:199], v[172:175], v[112:127]
	ds_read_b128 v[172:175], v193 offset:44032
	global_load_lds_dwordx4 v192, s[44:45] offset:1024 sc1
	s_waitcnt lgkmcnt(4)
	v_mfma_f32_32x32x16_f16 v[96:111], a[200:203], v[176:179], v[96:111]
	ds_read_b128 v[176:179], v193 offset:45056
	v_mfma_f32_32x32x16_f16 v[112:127], a[200:203], v[180:183], v[112:127]
	ds_read_b128 v[180:183], v193 offset:46080
	v_mfma_f32_32x32x16_f16 v[96:111], a[204:207], v[184:187], v[96:111]
	ds_read_b128 v[184:187], v193 offset:47104
	v_mfma_f32_32x32x16_f16 v[112:127], a[204:207], v[188:191], v[112:127]
	ds_read_b128 v[188:191], v193 offset:48128
	global_load_lds_dwordx4 v192, s[44:45] offset:2048 sc1
	s_waitcnt vmcnt(4)
	s_barrier
	v_mov_b32_e32 v199, 3
	s_cmp_eq_u32 s31, 0
	s_cbranch_scc1 .LD_slow42
	global_store_dword v197, v199, s[40:41]
	s_branch .LD_join43

.LD_join43:
	ds_read_b64 v[200:201], v249 offset:1024
	ds_read_b64 v[202:203], v249 offset:3072
	ds_read_b64 v[204:205], v249 offset:5120
	ds_read_b64 v[206:207], v249 offset:7168
	s_waitcnt lgkmcnt(8)
	v_mfma_f32_32x32x16_f16 v[96:111], a[208:211], v[160:163], v[96:111]
	ds_read_b128 v[160:163], v193 offset:49152
	v_mfma_f32_32x32x16_f16 v[112:127], a[208:211], v[164:167], v[112:127]
	ds_read_b128 v[164:167], v193 offset:50176
	v_mfma_f32_32x32x16_f16 v[96:111], a[212:215], v[168:171], v[96:111]
	ds_read_b128 v[168:171], v193 offset:51200
	v_mfma_f32_32x32x16_f16 v[112:127], a[212:215], v[172:175], v[112:127]
	ds_read_b128 v[172:175], v193 offset:52224
	global_load_lds_dwordx4 v192, s[44:45] offset:3072 sc1
	s_waitcnt lgkmcnt(8)
	v_mfma_f32_32x32x16_f16 v[96:111], a[216:219], v[176:179], v[96:111]
	ds_read_b128 v[176:179], v193 offset:53248
	v_mfma_f32_32x32x16_f16 v[112:127], a[216:219], v[180:183], v[112:127]
	ds_read_b128 v[180:183], v193 offset:54272
	v_mfma_f32_32x32x16_f16 v[96:111], a[220:223], v[184:187], v[96:111]
	ds_read_b128 v[184:187], v193 offset:55296
	v_mfma_f32_32x32x16_f16 v[112:127], a[220:223], v[188:191], v[112:127]
	ds_read_b128 v[188:191], v193 offset:56320
	s_add_u32 s44, s34, 0x9000
	s_addc_u32 s45, s35, 0
	s_mov_b32 m0, s55
	s_nop 0
	global_load_lds_dwordx4 v192, s[44:45] sc1
	s_waitcnt lgkmcnt(4)
	v_mfma_f32_32x32x16_f16 v[96:111], a[224:227], v[160:163], v[96:111]
	ds_read_b128 v[160:163], v193 offset:57344
	v_mfma_f32_32x32x16_f16 v[112:127], a[224:227], v[164:167], v[112:127]
	ds_read_b128 v[164:167], v193 offset:58368
	v_mfma_f32_32x32x16_f16 v[96:111], a[228:231], v[168:171], v[96:111]
	ds_read_b128 v[168:171], v193 offset:59392
	v_mfma_f32_32x32x16_f16 v[112:127], a[228:231], v[172:175], v[112:127]
	ds_read_b128 v[172:175], v193 offset:60416
	global_load_lds_dwordx4 v192, s[44:45] offset:1024 sc1
	v_add_f32_e32 v200, v200, v202
	v_add_f32_e32 v201, v201, v203
	v_add_f32_e32 v200, v200, v204
	v_add_f32_e32 v201, v201, v205
	v_add_f32_e32 v200, v200, v206
	v_add_f32_e32 v201, v201, v207
	global_store_dwordx2 v250, v[200:201], s[72:73]
	s_waitcnt lgkmcnt(4)
	v_mfma_f32_32x32x16_f16 v[96:111], a[232:235], v[176:179], v[96:111]
	ds_read_b128 v[176:179], v193 offset:61440
	v_mfma_f32_32x32x16_f16 v[112:127], a[232:235], v[180:183], v[112:127]
	ds_read_b128 v[180:183], v193 offset:62464
	v_mfma_f32_32x32x16_f16 v[96:111], a[236:239], v[184:187], v[96:111]
	ds_read_b128 v[184:187], v193 offset:63488
	v_mfma_f32_32x32x16_f16 v[112:127], a[236:239], v[188:191], v[112:127]
	ds_read_b128 v[188:191], v193 offset:64512
	global_load_lds_dwordx4 v192, s[44:45] offset:2048 sc1
	s_waitcnt vmcnt(9)
	s_barrier
	s_waitcnt lgkmcnt(4)
	v_mfma_f32_32x32x16_f16 v[96:111], a[240:243], v[160:163], v[96:111]
	ds_read_b128 v[160:163], v192 offset:0
	v_mfma_f32_32x32x16_f16 v[112:127], a[240:243], v[164:167], v[112:127]
	ds_read_b128 v[164:167], v192 offset:1024
	v_mfma_f32_32x32x16_f16 v[96:111], a[244:247], v[168:171], v[96:111]
	ds_read_b128 v[168:171], v192 offset:2048
	v_mfma_f32_32x32x16_f16 v[112:127], a[244:247], v[172:175], v[112:127]
	ds_read_b128 v[172:175], v192 offset:3072
	global_load_lds_dwordx4 v192, s[44:45] offset:3072 sc1
	s_waitcnt lgkmcnt(4)
	v_mfma_f32_32x32x16_f16 v[96:111], a[248:251], v[176:179], v[96:111]
	ds_read_b128 v[176:179], v192 offset:4096
	v_mfma_f32_32x32x16_f16 v[112:127], a[248:251], v[180:183], v[112:127]
	ds_read_b128 v[180:183], v192 offset:5120
	v_mfma_f32_32x32x16_f16 v[96:111], a[252:255], v[184:187], v[96:111]
	ds_read_b128 v[184:187], v192 offset:6144
	v_mfma_f32_32x32x16_f16 v[112:127], a[252:255], v[188:191], v[112:127]
	ds_read_b128 v[188:191], v192 offset:7168
	s_add_u32 s44, s34, 0x10000
	s_addc_u32 s45, s35, 0
	s_mov_b32 m0, s56
	s_nop 0
	global_load_lds_dwordx4 v192, s[44:45] sc1
	s_add_u32 s33, s33, 1
	s_cmp_lt_u32 s33, s28
	s_cbranch_scc1 .LD_loop16
